# speedup vs baseline: 1.0096x; 1.0065x over previous
.LE_loop16:
	s_sub_u32 s71, s33, 1
	s_add_u32 s61, s33, 1
	s_min_u32 s61, s61, s60
	s_and_b32 s64, s71, 1
	s_lshl_b32 s64, s64, 22
	s_add_u32 s64, s64, s50
	s_add_u32 s64, s64, 0x60000
	s_add_u32 s36, s6, s64
	s_addc_u32 s37, s7, 0
	s_lshl_b32 s64, s71, 3
	s_add_u32 s64, s64, s29
	s_lshl_b32 s64, s64, 5
	s_add_u32 s64, s64, s30
	s_lshl_b32 s64, s64, 2
	s_add_u32 s40, s8, s64
	s_addc_u32 s41, s9, 0
	s_lshl_b32 s64, s33, 11
	s_lshl_b32 s65, s29, 8
	s_add_u32 s64, s64, s65
	s_add_u32 s64, s64, 128
	s_lshl_b32 s64, s64, 3
	s_add_u32 s42, s12, s64
	s_addc_u32 s43, s13, 0
	s_nop 3
	global_load_dwordx2 v[228:229], v249, s[42:43] offset:0
	global_load_dwordx2 v[230:231], v249, s[42:43] offset:256
	s_waitcnt lgkmcnt(4)
	v_mfma_f32_32x32x16_f16 v[0:15], a[0:3], v[160:163], v[0:15]
	ds_read_b128 v[160:163], v192 offset:8192
	v_exp_f32_e32 v200, v96
	v_mfma_f32_32x32x16_f16 v[16:31], a[0:3], v[164:167], v[16:31]
	ds_read_b128 v[164:167], v192 offset:9216
	v_exp_f32_e32 v201, v97
	v_add_f32_e32 v200, 1.0, v200
	v_mfma_f32_32x32x16_f16 v[0:15], a[4:7], v[168:171], v[0:15]
	ds_read_b128 v[168:171], v192 offset:10240
	v_exp_f32_e32 v202, v98
	v_add_f32_e32 v201, 1.0, v201
	v_mfma_f32_32x32x16_f16 v[16:31], a[4:7], v[172:175], v[16:31]
	ds_read_b128 v[172:175], v192 offset:11264
	global_load_lds_dwordx4 v192, s[44:45] offset:1024 sc1
	v_exp_f32_e32 v203, v99
	v_add_f32_e32 v202, 1.0, v202
	s_waitcnt lgkmcnt(4)
	v_mfma_f32_32x32x16_f16 v[0:15], a[8:11], v[176:179], v[0:15]
	ds_read_b128 v[176:179], v192 offset:12288
	v_exp_f32_e32 v204, v100
	v_add_f32_e32 v203, 1.0, v203
	v_mfma_f32_32x32x16_f16 v[16:31], a[8:11], v[180:183], v[16:31]
	ds_read_b128 v[180:183], v192 offset:13312
	v_exp_f32_e32 v205, v101
	v_add_f32_e32 v204, 1.0, v204
	v_mfma_f32_32x32x16_f16 v[0:15], a[12:15], v[184:187], v[0:15]
	ds_read_b128 v[184:187], v192 offset:14336
	v_exp_f32_e32 v206, v102
	v_add_f32_e32 v205, 1.0, v205
	v_mfma_f32_32x32x16_f16 v[16:31], a[12:15], v[188:191], v[16:31]
	ds_read_b128 v[188:191], v192 offset:15360
	global_load_lds_dwordx4 v192, s[44:45] offset:2048 sc1
	v_exp_f32_e32 v207, v103
	v_add_f32_e32 v206, 1.0, v206
	s_waitcnt lgkmcnt(4)
	v_mfma_f32_32x32x16_f16 v[0:15], a[16:19], v[160:163], v[0:15]
	ds_read_b128 v[160:163], v192 offset:16384
	v_exp_f32_e32 v208, v104
	v_add_f32_e32 v207, 1.0, v207
	v_mfma_f32_32x32x16_f16 v[16:31], a[16:19], v[164:167], v[16:31]
	ds_read_b128 v[164:167], v192 offset:17408
	v_exp_f32_e32 v209, v105
	v_add_f32_e32 v208, 1.0, v208
	v_mfma_f32_32x32x16_f16 v[0:15], a[20:23], v[168:171], v[0:15]
	ds_read_b128 v[168:171], v192 offset:18432
	v_exp_f32_e32 v210, v106
	v_add_f32_e32 v209, 1.0, v209
	v_mfma_f32_32x32x16_f16 v[16:31], a[20:23], v[172:175], v[16:31]
	ds_read_b128 v[172:175], v192 offset:19456
	global_load_lds_dwordx4 v192, s[44:45] offset:3072 sc1
	v_exp_f32_e32 v211, v107
	v_add_f32_e32 v210, 1.0, v210
	s_waitcnt lgkmcnt(4)
	v_mfma_f32_32x32x16_f16 v[0:15], a[24:27], v[176:179], v[0:15]
	ds_read_b128 v[176:179], v192 offset:20480
	v_exp_f32_e32 v212, v108
	v_add_f32_e32 v211, 1.0, v211
	v_mfma_f32_32x32x16_f16 v[16:31], a[24:27], v[180:183], v[16:31]
	ds_read_b128 v[180:183], v192 offset:21504
	v_exp_f32_e32 v213, v109
	v_add_f32_e32 v212, 1.0, v212
	v_mfma_f32_32x32x16_f16 v[0:15], a[28:31], v[184:187], v[0:15]
	ds_read_b128 v[184:187], v192 offset:22528
	v_exp_f32_e32 v214, v110
	v_add_f32_e32 v213, 1.0, v213
	v_mfma_f32_32x32x16_f16 v[16:31], a[28:31], v[188:191], v[16:31]
	ds_read_b128 v[188:191], v192 offset:23552
	s_add_u32 s44, s34, 0x11000
	s_addc_u32 s45, s35, 0
	s_mov_b32 m0, s57
	s_nop 0
	global_load_lds_dwordx4 v192, s[44:45] sc1
	v_exp_f32_e32 v215, v111
	v_add_f32_e32 v214, 1.0, v214
	s_waitcnt lgkmcnt(4)
	v_mfma_f32_32x32x16_f16 v[0:15], a[32:35], v[160:163], v[0:15]
	ds_read_b128 v[160:163], v192 offset:24576
	v_add_f32_e32 v215, 1.0, v215
	v_rcp_f32_e32 v200, v200
	v_mfma_f32_32x32x16_f16 v[16:31], a[32:35], v[164:167], v[16:31]
	ds_read_b128 v[164:167], v192 offset:25600
	v_rcp_f32_e32 v201, v201
	v_mfma_f32_32x32x16_f16 v[0:15], a[36:39], v[168:171], v[0:15]
	ds_read_b128 v[168:171], v192 offset:26624
	v_rcp_f32_e32 v202, v202
	v_mfma_f32_32x32x16_f16 v[16:31], a[36:39], v[172:175], v[16:31]
	ds_read_b128 v[172:175], v192 offset:27648
	global_load_lds_dwordx4 v192, s[44:45] offset:1024 sc1
	v_rcp_f32_e32 v203, v203
	s_waitcnt lgkmcnt(4)
	v_mfma_f32_32x32x16_f16 v[0:15], a[40:43], v[176:179], v[0:15]
	ds_read_b128 v[176:179], v192 offset:28672
	v_rcp_f32_e32 v204, v204
	v_mfma_f32_32x32x16_f16 v[16:31], a[40:43], v[180:183], v[16:31]
	ds_read_b128 v[180:183], v192 offset:29696
	v_rcp_f32_e32 v205, v205
	v_mul_f32_e32 v204, v204, v152
	v_mfma_f32_32x32x16_f16 v[0:15], a[44:47], v[184:187], v[0:15]
	ds_read_b128 v[184:187], v192 offset:30720
	v_rcp_f32_e32 v206, v206
	v_mul_f32_e32 v205, v205, v153
	v_mfma_f32_32x32x16_f16 v[16:31], a[44:47], v[188:191], v[16:31]
	ds_read_b128 v[188:191], v192 offset:31744
	global_load_lds_dwordx4 v192, s[44:45] offset:2048 sc1
	v_rcp_f32_e32 v207, v207
	v_mul_f32_e32 v206, v206, v154
	s_waitcnt vmcnt(9)
	s_barrier
	s_waitcnt lgkmcnt(4)
	v_mfma_f32_32x32x16_f16 v[0:15], a[48:51], v[160:163], v[0:15]
	ds_read_b128 v[160:163], v192 offset:32768
	v_rcp_f32_e32 v208, v208
	v_mul_f32_e32 v207, v207, v155
	v_mfma_f32_32x32x16_f16 v[16:31], a[48:51], v[164:167], v[16:31]
	ds_read_b128 v[164:167], v192 offset:33792
	v_rcp_f32_e32 v209, v209
	v_fmamk_f32 v208, v208, 0xc0b8aa3b, v198
	v_mfma_f32_32x32x16_f16 v[0:15], a[52:55], v[168:171], v[0:15]
	ds_read_b128 v[168:171], v192 offset:34816
	v_rcp_f32_e32 v210, v210
	v_fmamk_f32 v209, v209, 0xc0b8aa3b, v198
	v_fma_f32 v152, v200, v208, v204
	v_mfma_f32_32x32x16_f16 v[16:31], a[52:55], v[172:175], v[16:31]
	ds_read_b128 v[172:175], v192 offset:35840
	global_load_lds_dwordx4 v192, s[44:45] offset:3072 sc1
	v_rcp_f32_e32 v211, v211
	v_fmamk_f32 v210, v210, 0xc0b8aa3b, v198
	v_fma_f32 v153, v201, v209, v205
	s_waitcnt lgkmcnt(4)
	v_mfma_f32_32x32x16_f16 v[0:15], a[56:59], v[176:179], v[0:15]
	ds_read_b128 v[176:179], v192 offset:36864
	v_rcp_f32_e32 v212, v212
	v_fmamk_f32 v211, v211, 0xc0b8aa3b, v198
	v_fma_f32 v154, v202, v210, v206
	v_mfma_f32_32x32x16_f16 v[16:31], a[56:59], v[180:183], v[16:31]
	ds_read_b128 v[180:183], v192 offset:37888
	v_rcp_f32_e32 v213, v213
	v_fma_f32 v155, v203, v211, v207
	v_mfma_f32_32x32x16_f16 v[0:15], a[60:63], v[184:187], v[0:15]
	ds_read_b128 v[184:187], v192 offset:38912
	v_rcp_f32_e32 v214, v214
	v_mfma_f32_32x32x16_f16 v[16:31], a[60:63], v[188:191], v[16:31]
	ds_read_b128 v[188:191], v192 offset:39936
	s_add_u32 s44, s34, 0x18000
	s_addc_u32 s45, s35, 0
	s_mov_b32 m0, s58
	s_nop 0
	global_load_lds_dwordx4 v192, s[44:45] sc1
	v_rcp_f32_e32 v215, v215
	s_waitcnt lgkmcnt(4)
	v_mfma_f32_32x32x16_f16 v[0:15], a[64:67], v[160:163], v[0:15]
	ds_read_b128 v[160:163], v192 offset:40960
	v_exp_f32_e32 v200, v152
	v_mfma_f32_32x32x16_f16 v[16:31], a[64:67], v[164:167], v[16:31]
	ds_read_b128 v[164:167], v192 offset:41984
	v_exp_f32_e32 v201, v153
	v_add_f32_e32 v200, 1.0, v200
	v_mfma_f32_32x32x16_f16 v[0:15], a[68:71], v[168:171], v[0:15]
	ds_read_b128 v[168:171], v192 offset:43008
	v_exp_f32_e32 v202, v154
	v_add_f32_e32 v201, 1.0, v201
	v_mfma_f32_32x32x16_f16 v[16:31], a[68:71], v[172:175], v[16:31]
	ds_read_b128 v[172:175], v192 offset:44032
	global_load_lds_dwordx4 v192, s[44:45] offset:1024 sc1
	v_exp_f32_e32 v203, v155
	v_add_f32_e32 v202, 1.0, v202
	s_waitcnt lgkmcnt(4)
	v_mfma_f32_32x32x16_f16 v[0:15], a[72:75], v[176:179], v[0:15]
	ds_read_b128 v[176:179], v192 offset:45056
	v_add_f32_e32 v203, 1.0, v203
	v_rcp_f32_e32 v200, v200
	v_mfma_f32_32x32x16_f16 v[16:31], a[72:75], v[180:183], v[16:31]
	ds_read_b128 v[180:183], v192 offset:46080
	v_rcp_f32_e32 v201, v201
	v_fma_f32 v200, v200, 2.0, -1.0
	v_mfma_f32_32x32x16_f16 v[0:15], a[76:79], v[184:187], v[0:15]
	ds_read_b128 v[184:187], v192 offset:47104
	v_rcp_f32_e32 v202, v202
	v_fma_f32 v201, v201, 2.0, -1.0
	v_mul_f32_e32 v216, v212, v200
	v_mfma_f32_32x32x16_f16 v[16:31], a[76:79], v[188:191], v[16:31]
	ds_read_b128 v[188:191], v192 offset:48128
	global_load_lds_dwordx4 v192, s[44:45] offset:2048 sc1
	v_rcp_f32_e32 v203, v203
	v_fma_f32 v202, v202, 2.0, -1.0
	v_mul_f32_e32 v217, v213, v201
	s_waitcnt lgkmcnt(4)
	v_mfma_f32_32x32x16_f16 v[0:15], a[80:83], v[160:163], v[0:15]
	ds_read_b128 v[160:163], v192 offset:49152
	v_fma_f32 v203, v203, 2.0, -1.0
	v_mul_f32_e32 v218, v214, v202
	v_exp_f32_e32 v200, v112
	v_mfma_f32_32x32x16_f16 v[16:31], a[80:83], v[164:167], v[16:31]
	ds_read_b128 v[164:167], v192 offset:50176
	v_mul_f32_e32 v219, v215, v203
	v_cvt_pk_f16_f32 v220, v216, v217
	v_exp_f32_e32 v201, v113
	v_mfma_f32_32x32x16_f16 v[0:15], a[84:87], v[168:171], v[0:15]
	ds_read_b128 v[168:171], v192 offset:51200
	v_cvt_pk_f16_f32 v221, v218, v219
	v_exp_f32_e32 v202, v114
	v_add_f32_e32 v200, 1.0, v200
	v_mfma_f32_32x32x16_f16 v[16:31], a[84:87], v[172:175], v[16:31]
	ds_read_b128 v[172:175], v192 offset:52224
	global_load_lds_dwordx4 v192, s[44:45] offset:3072 sc1
	v_exp_f32_e32 v203, v115
	v_add_f32_e32 v201, 1.0, v201
	v_add_f32_e32 v202, 1.0, v202
	s_waitcnt lgkmcnt(4)
	v_mfma_f32_32x32x16_f16 v[0:15], a[88:91], v[176:179], v[0:15]
	ds_read_b128 v[176:179], v192 offset:53248
	v_exp_f32_e32 v204, v116
	v_add_f32_e32 v203, 1.0, v203
	v_mfma_f32_32x32x16_f16 v[16:31], a[88:91], v[180:183], v[16:31]
	ds_read_b128 v[180:183], v192 offset:54272
	v_exp_f32_e32 v205, v117
	v_add_f32_e32 v204, 1.0, v204
	v_mfma_f32_32x32x16_f16 v[0:15], a[92:95], v[184:187], v[0:15]
	ds_read_b128 v[184:187], v192 offset:55296
	v_exp_f32_e32 v206, v118
	v_add_f32_e32 v205, 1.0, v205
	v_mfma_f32_32x32x16_f16 v[16:31], a[92:95], v[188:191], v[16:31]
	ds_read_b128 v[188:191], v192 offset:56320
	s_add_u32 s44, s34, 0x19000
	s_addc_u32 s45, s35, 0
	s_mov_b32 m0, s59
	s_nop 0
	global_load_lds_dwordx4 v192, s[44:45] sc1
	s_lshl_b32 s64, s71, 3
	s_add_u32 s64, s64, s29
	s_lshl_b32 s64, s64, 7
	s_add_u32 s38, s8, s64
	s_addc_u32 s39, s9, 0
	global_load_dword v251, v196, s[38:39] sc1
	v_exp_f32_e32 v207, v119
	v_add_f32_e32 v206, 1.0, v206
	s_waitcnt lgkmcnt(4)
	v_mfma_f32_32x32x16_f16 v[0:15], a[96:99], v[160:163], v[0:15]
	ds_read_b128 v[160:163], v192 offset:57344
	v_exp_f32_e32 v208, v120
	v_add_f32_e32 v207, 1.0, v207
	v_mfma_f32_32x32x16_f16 v[16:31], a[96:99], v[164:167], v[16:31]
	ds_read_b128 v[164:167], v192 offset:58368
	v_exp_f32_e32 v209, v121
	v_add_f32_e32 v208, 1.0, v208
	v_mfma_f32_32x32x16_f16 v[0:15], a[100:103], v[168:171], v[0:15]
	ds_read_b128 v[168:171], v192 offset:59392
	v_exp_f32_e32 v210, v122
	v_add_f32_e32 v209, 1.0, v209
	v_mfma_f32_32x32x16_f16 v[16:31], a[100:103], v[172:175], v[16:31]
	ds_read_b128 v[172:175], v192 offset:60416
	global_load_lds_dwordx4 v192, s[44:45] offset:1024 sc1
	v_exp_f32_e32 v211, v123
	v_add_f32_e32 v210, 1.0, v210
	s_waitcnt lgkmcnt(4)
	v_mfma_f32_32x32x16_f16 v[0:15], a[104:107], v[176:179], v[0:15]
	ds_read_b128 v[176:179], v192 offset:61440
	v_exp_f32_e32 v212, v124
	v_add_f32_e32 v211, 1.0, v211
	v_mfma_f32_32x32x16_f16 v[16:31], a[104:107], v[180:183], v[16:31]
	ds_read_b128 v[180:183], v192 offset:62464
	v_exp_f32_e32 v213, v125
	v_add_f32_e32 v212, 1.0, v212
	v_mfma_f32_32x32x16_f16 v[0:15], a[108:111], v[184:187], v[0:15]
	ds_read_b128 v[184:187], v192 offset:63488
	v_exp_f32_e32 v214, v126
	v_add_f32_e32 v213, 1.0, v213
	v_mfma_f32_32x32x16_f16 v[16:31], a[108:111], v[188:191], v[16:31]
	ds_read_b128 v[188:191], v192 offset:64512
	global_load_lds_dwordx4 v192, s[44:45] offset:2048 sc1
	v_exp_f32_e32 v215, v127
	v_add_f32_e32 v214, 1.0, v214
	s_waitcnt vmcnt(8)
	s_barrier
	s_waitcnt lgkmcnt(4)
	v_mfma_f32_32x32x16_f16 v[0:15], a[112:115], v[160:163], v[0:15]
	ds_read_b128 v[160:163], v193 offset:0
	v_add_f32_e32 v215, 1.0, v215
	v_rcp_f32_e32 v200, v200
	v_mfma_f32_32x32x16_f16 v[16:31], a[112:115], v[164:167], v[16:31]
	ds_read_b128 v[164:167], v193 offset:1024
	v_rcp_f32_e32 v201, v201
	v_mfma_f32_32x32x16_f16 v[0:15], a[116:119], v[168:171], v[0:15]
	ds_read_b128 v[168:171], v193 offset:2048
	v_rcp_f32_e32 v202, v202
	v_mfma_f32_32x32x16_f16 v[16:31], a[116:119], v[172:175], v[16:31]
	ds_read_b128 v[172:175], v193 offset:3072
	global_load_lds_dwordx4 v192, s[44:45] offset:3072 sc1
	v_rcp_f32_e32 v203, v203
	s_waitcnt lgkmcnt(4)
	v_mfma_f32_32x32x16_f16 v[0:15], a[120:123], v[176:179], v[0:15]
	ds_read_b128 v[176:179], v193 offset:4096
	v_rcp_f32_e32 v204, v204
	ds_read_b128 v[236:239], v248 offset:0
	ds_read_b64 v[240:241], v248 offset:32
	ds_read_b128 v[242:245], v248 offset:16
	ds_read_b64 v[246:247], v248 offset:40
	v_mfma_f32_32x32x16_f16 v[16:31], a[120:123], v[180:183], v[16:31]
	ds_read_b128 v[180:183], v193 offset:5120
	v_rcp_f32_e32 v205, v205
	v_mul_f32_e32 v204, v204, v156
	s_waitcnt lgkmcnt(3)
	v_fma_f32 v64, v229, v237, v240
	v_mfma_f32_32x32x16_f16 v[0:15], a[124:127], v[184:187], v[0:15]
	ds_read_b128 v[184:187], v193 offset:6144
	v_rcp_f32_e32 v206, v206
	v_mul_f32_e32 v205, v205, v157
	v_fma_f32 v65, v229, v239, v241
	v_fmac_f32_e32 v64, v228, v236
	v_mfma_f32_32x32x16_f16 v[16:31], a[124:127], v[188:191], v[16:31]
	ds_read_b128 v[188:191], v193 offset:7168
	s_waitcnt vmcnt(3)
	v_cmp_gt_u32_e32 vcc, 2, v251
	s_cbranch_vccz .LE_tok20

.LE_tok20:
	s_and_b32 s64, s71, 1
	s_lshl_b32 s64, s64, 22
	s_add_u32 s64, s64, s49
	s_add_u32 s64, s64, 0x20000
	s_add_u32 s34, s6, s64
	s_addc_u32 s35, s7, 0
	s_add_u32 s44, s34, 0x0
	s_addc_u32 s45, s35, 0
	s_mov_b32 m0, s52
	s_nop 0
	global_load_lds_dwordx4 v192, s[44:45] sc1
	v_rcp_f32_e32 v207, v207
	v_mul_f32_e32 v206, v206, v158
	v_fmac_f32_e32 v65, v228, v238
	v_fma_f32 v80, v231, v237, v240
	v_mfma_f32_32x32x16_f16 v[0:15], a[128:131], v[160:163], v[0:15]
	ds_read_b128 v[160:163], v193 offset:8192
	v_rcp_f32_e32 v208, v208
	v_mul_f32_e32 v207, v207, v159
	v_fma_f32 v81, v231, v239, v241
	v_fmac_f32_e32 v80, v230, v236
	v_mfma_f32_32x32x16_f16 v[16:31], a[128:131], v[164:167], v[16:31]
	ds_read_b128 v[164:167], v193 offset:9216
	v_rcp_f32_e32 v209, v209
	v_fmamk_f32 v208, v208, 0xc0b8aa3b, v198
	v_fmac_f32_e32 v81, v230, v238
	ds_read_b128 v[236:239], v248 offset:48
	ds_read_b64 v[240:241], v248 offset:80
	v_mfma_f32_32x32x16_f16 v[0:15], a[132:135], v[168:171], v[0:15]
	ds_read_b128 v[168:171], v193 offset:10240
	v_rcp_f32_e32 v210, v210
	v_fmamk_f32 v209, v209, 0xc0b8aa3b, v198
	v_fma_f32 v156, v200, v208, v204
	s_waitcnt lgkmcnt(8)
	v_fma_f32 v66, v229, v243, v246
	v_mfma_f32_32x32x16_f16 v[16:31], a[132:135], v[172:175], v[16:31]
	ds_read_b128 v[172:175], v193 offset:11264
	global_load_lds_dwordx4 v192, s[44:45] offset:1024 sc1
	v_rcp_f32_e32 v211, v211
	v_fmamk_f32 v210, v210, 0xc0b8aa3b, v198
	v_fma_f32 v157, v201, v209, v205
	v_fma_f32 v67, v229, v245, v247
	v_fmac_f32_e32 v66, v228, v242
	s_waitcnt lgkmcnt(6)
	v_mfma_f32_32x32x16_f16 v[0:15], a[136:139], v[176:179], v[0:15]
	ds_read_b128 v[176:179], v193 offset:12288
	v_rcp_f32_e32 v212, v212
	v_fmamk_f32 v211, v211, 0xc0b8aa3b, v198
	v_fma_f32 v158, v202, v210, v206
	v_fmac_f32_e32 v67, v228, v244
	v_fma_f32 v82, v231, v243, v246
	v_mfma_f32_32x32x16_f16 v[16:31], a[136:139], v[180:183], v[16:31]
	ds_read_b128 v[180:183], v193 offset:13312
	v_rcp_f32_e32 v213, v213
	v_fma_f32 v159, v203, v211, v207
	v_fma_f32 v83, v231, v245, v247
	v_fmac_f32_e32 v82, v230, v242
	v_mfma_f32_32x32x16_f16 v[0:15], a[140:143], v[184:187], v[0:15]
	ds_read_b128 v[184:187], v193 offset:14336
	v_rcp_f32_e32 v214, v214
	v_fmac_f32_e32 v83, v230, v244
	ds_read_b128 v[242:245], v248 offset:64
	ds_read_b64 v[246:247], v248 offset:88
	v_mfma_f32_32x32x16_f16 v[16:31], a[140:143], v[188:191], v[16:31]
	ds_read_b128 v[188:191], v193 offset:15360
	global_load_lds_dwordx4 v192, s[44:45] offset:2048 sc1
	v_rcp_f32_e32 v215, v215
	s_waitcnt lgkmcnt(8)
	v_fma_f32 v68, v229, v237, v240
	s_waitcnt lgkmcnt(6)
	v_mfma_f32_32x32x16_f16 v[0:15], a[144:147], v[160:163], v[0:15]
	ds_read_b128 v[160:163], v193 offset:16384
	v_exp_f32_e32 v200, v156
	v_fma_f32 v69, v229, v239, v241
	v_fmac_f32_e32 v68, v228, v236
	v_mfma_f32_32x32x16_f16 v[16:31], a[144:147], v[164:167], v[16:31]
	ds_read_b128 v[164:167], v193 offset:17408
	v_exp_f32_e32 v201, v157
	v_add_f32_e32 v200, 1.0, v200
	v_fmac_f32_e32 v69, v228, v238
	v_fma_f32 v84, v231, v237, v240
	v_mfma_f32_32x32x16_f16 v[0:15], a[148:151], v[168:171], v[0:15]
	ds_read_b128 v[168:171], v193 offset:18432
	v_exp_f32_e32 v202, v158
	v_add_f32_e32 v201, 1.0, v201
	v_fma_f32 v85, v231, v239, v241
	v_fmac_f32_e32 v84, v230, v236
	v_mfma_f32_32x32x16_f16 v[16:31], a[148:151], v[172:175], v[16:31]
	ds_read_b128 v[172:175], v193 offset:19456
	global_load_lds_dwordx4 v192, s[44:45] offset:3072 sc1
	v_exp_f32_e32 v203, v159
	v_add_f32_e32 v202, 1.0, v202
	v_fmac_f32_e32 v85, v230, v238
	ds_read_b128 v[236:239], v248 offset:96
	ds_read_b64 v[240:241], v248 offset:128
	s_waitcnt lgkmcnt(6)
	v_mfma_f32_32x32x16_f16 v[0:15], a[152:155], v[176:179], v[0:15]
	ds_read_b128 v[176:179], v193 offset:20480
	v_add_f32_e32 v203, 1.0, v203
	v_rcp_f32_e32 v200, v200
	v_fma_f32 v70, v229, v243, v246
	v_mfma_f32_32x32x16_f16 v[16:31], a[152:155], v[180:183], v[16:31]
	ds_read_b128 v[180:183], v193 offset:21504
	v_rcp_f32_e32 v201, v201
	v_fma_f32 v200, v200, 2.0, -1.0
	v_fma_f32 v71, v229, v245, v247
	v_fmac_f32_e32 v70, v228, v242
	v_mfma_f32_32x32x16_f16 v[0:15], a[156:159], v[184:187], v[0:15]
	ds_read_b128 v[184:187], v193 offset:22528
	v_rcp_f32_e32 v202, v202
	v_fma_f32 v201, v201, 2.0, -1.0
	v_mul_f32_e32 v216, v212, v200
	v_fmac_f32_e32 v71, v228, v244
	v_fma_f32 v86, v231, v243, v246
	v_mfma_f32_32x32x16_f16 v[16:31], a[156:159], v[188:191], v[16:31]
	ds_read_b128 v[188:191], v193 offset:23552
	s_add_u32 s44, s34, 0x1000
	s_addc_u32 s45, s35, 0
	s_mov_b32 m0, s53
	s_nop 0
	global_load_lds_dwordx4 v192, s[44:45] sc1
	v_rcp_f32_e32 v203, v203
	v_fma_f32 v202, v202, 2.0, -1.0
	v_mul_f32_e32 v217, v213, v201
	v_fma_f32 v87, v231, v245, v247
	v_fmac_f32_e32 v86, v230, v242
	s_waitcnt lgkmcnt(6)
	v_mfma_f32_32x32x16_f16 v[0:15], a[160:163], v[160:163], v[0:15]
	ds_read_b128 v[160:163], v193 offset:24576
	v_fma_f32 v203, v203, 2.0, -1.0
	v_mul_f32_e32 v218, v214, v202
	v_fmac_f32_e32 v87, v230, v244
	ds_read_b128 v[242:245], v248 offset:112
	ds_read_b64 v[246:247], v248 offset:136
	v_mfma_f32_32x32x16_f16 v[16:31], a[160:163], v[164:167], v[16:31]
	ds_read_b128 v[164:167], v193 offset:25600
	v_mul_f32_e32 v219, v215, v203
	v_cvt_pk_f16_f32 v222, v216, v217
	s_waitcnt lgkmcnt(8)
	v_fma_f32 v72, v229, v237, v240
	v_mfma_f32_32x32x16_f16 v[0:15], a[164:167], v[168:171], v[0:15]
	ds_read_b128 v[168:171], v193 offset:26624
	v_cvt_pk_f16_f32 v223, v218, v219
	v_fma_f32 v73, v229, v239, v241
	v_fmac_f32_e32 v72, v228, v236
	v_mfma_f32_32x32x16_f16 v[16:31], a[164:167], v[172:175], v[16:31]
	ds_read_b128 v[172:175], v193 offset:27648
	global_load_lds_dwordx4 v192, s[44:45] offset:1024 sc1
	s_nop 1
	v_permlane32_swap_b32_e32 v220, v222
	v_permlane32_swap_b32_e32 v221, v223
	s_cmp_eq_u32 s31, 0
	s_cbranch_scc1 .LE_slow22
	global_store_dwordx4 v195, v[220:223], s[36:37] offset:0
	s_branch .LE_join23

.LE_join23:
	v_fmac_f32_e32 v73, v228, v238
	v_fma_f32 v88, v231, v237, v240
	s_waitcnt lgkmcnt(6)
	v_mfma_f32_32x32x16_f16 v[0:15], a[168:171], v[176:179], v[0:15]
	ds_read_b128 v[176:179], v193 offset:28672
	v_fma_f32 v89, v231, v239, v241
	v_fmac_f32_e32 v88, v230, v236
	v_mfma_f32_32x32x16_f16 v[16:31], a[168:171], v[180:183], v[16:31]
	ds_read_b128 v[180:183], v193 offset:29696
	v_fmac_f32_e32 v89, v230, v238
	ds_read_b128 v[236:239], v248 offset:144
	ds_read_b64 v[240:241], v248 offset:176
	v_mfma_f32_32x32x16_f16 v[0:15], a[172:175], v[184:187], v[0:15]
	ds_read_b128 v[184:187], v193 offset:30720
	s_waitcnt lgkmcnt(8)
	v_fma_f32 v74, v229, v243, v246
	v_mfma_f32_32x32x16_f16 v[16:31], a[172:175], v[188:191], v[16:31]
	ds_read_b128 v[188:191], v193 offset:31744
	global_load_lds_dwordx4 v192, s[44:45] offset:2048 sc1
	v_fma_f32 v75, v229, v245, v247
	v_fmac_f32_e32 v74, v228, v242
	s_waitcnt vmcnt(8)
	s_barrier
	s_waitcnt lgkmcnt(6)
	v_mfma_f32_32x32x16_f16 v[0:15], a[176:179], v[160:163], v[0:15]
	ds_read_b128 v[160:163], v193 offset:32768
	v_fmac_f32_e32 v75, v228, v244
	v_fma_f32 v90, v231, v243, v246
	v_mfma_f32_32x32x16_f16 v[16:31], a[176:179], v[164:167], v[16:31]
	ds_read_b128 v[164:167], v193 offset:33792
	v_fma_f32 v91, v231, v245, v247
	v_fmac_f32_e32 v90, v230, v242
	v_mfma_f32_32x32x16_f16 v[0:15], a[180:183], v[168:171], v[0:15]
	ds_read_b128 v[168:171], v193 offset:34816
	v_fmac_f32_e32 v91, v230, v244
	ds_read_b128 v[242:245], v248 offset:160
	ds_read_b64 v[246:247], v248 offset:184
	v_mfma_f32_32x32x16_f16 v[16:31], a[180:183], v[172:175], v[16:31]
	ds_read_b128 v[172:175], v193 offset:35840
	global_load_lds_dwordx4 v192, s[44:45] offset:3072 sc1
	s_waitcnt lgkmcnt(8)
	v_fma_f32 v76, v229, v237, v240
	s_waitcnt lgkmcnt(6)
	v_mfma_f32_32x32x16_f16 v[0:15], a[184:187], v[176:179], v[0:15]
	ds_read_b128 v[176:179], v193 offset:36864
	v_fma_f32 v77, v229, v239, v241
	v_fmac_f32_e32 v76, v228, v236
	v_mfma_f32_32x32x16_f16 v[16:31], a[184:187], v[180:183], v[16:31]
	ds_read_b128 v[180:183], v193 offset:37888
	v_fmac_f32_e32 v77, v228, v238
	v_fma_f32 v92, v231, v237, v240
	v_mfma_f32_32x32x16_f16 v[0:15], a[188:191], v[184:187], v[0:15]
	ds_read_b128 v[184:187], v193 offset:38912
	v_fma_f32 v93, v231, v239, v241
	v_fmac_f32_e32 v92, v230, v236
	v_mfma_f32_32x32x16_f16 v[16:31], a[188:191], v[188:191], v[16:31]
	ds_read_b128 v[188:191], v193 offset:39936
	s_add_u32 s44, s34, 0x8000
	s_addc_u32 s45, s35, 0
	s_mov_b32 m0, s54
	s_nop 0
	global_load_lds_dwordx4 v192, s[44:45] sc1
	v_fmac_f32_e32 v93, v230, v238
	s_waitcnt lgkmcnt(5)
	s_waitcnt lgkmcnt(4)
	v_mfma_f32_32x32x16_f16 v[0:15], a[192:195], v[160:163], v[0:15]
	ds_read_b128 v[160:163], v193 offset:40960
	v_fma_f32 v78, v229, v243, v246
	v_fma_f32 v79, v229, v245, v247
	s_waitcnt vmcnt(3)
	s_barrier
	v_mov_b32_e32 v199, 4
	s_cmp_eq_u32 s31, 0
	s_cbranch_scc1 .LE_slow24
	global_store_dword v197, v199, s[40:41]
	s_branch .LE_join25

.LE_join25:
	v_mfma_f32_32x32x16_f16 v[16:31], a[192:195], v[164:167], v[16:31]
	ds_read_b128 v[164:167], v193 offset:41984
	v_fmac_f32_e32 v78, v228, v242
	v_fmac_f32_e32 v79, v228, v244
	v_mfma_f32_32x32x16_f16 v[0:15], a[196:199], v[168:171], v[0:15]
	ds_read_b128 v[168:171], v193 offset:43008
	v_fma_f32 v94, v231, v243, v246
	v_fma_f32 v95, v231, v245, v247
	v_mfma_f32_32x32x16_f16 v[16:31], a[196:199], v[172:175], v[16:31]
	ds_read_b128 v[172:175], v193 offset:44032
	global_load_lds_dwordx4 v192, s[44:45] offset:1024 sc1
	v_fmac_f32_e32 v94, v230, v242
	v_fmac_f32_e32 v95, v230, v244
	s_waitcnt lgkmcnt(4)
	v_mfma_f32_32x32x16_f16 v[0:15], a[200:203], v[176:179], v[0:15]
	ds_read_b128 v[176:179], v193 offset:45056
	v_mfma_f32_32x32x16_f16 v[16:31], a[200:203], v[180:183], v[16:31]
	ds_read_b128 v[180:183], v193 offset:46080
	v_mfma_f32_32x32x16_f16 v[0:15], a[204:207], v[184:187], v[0:15]
	ds_read_b128 v[184:187], v193 offset:47104
	v_mfma_f32_32x32x16_f16 v[16:31], a[204:207], v[188:191], v[16:31]
	ds_read_b128 v[188:191], v193 offset:48128
	global_load_lds_dwordx4 v192, s[44:45] offset:2048 sc1
	s_waitcnt lgkmcnt(4)
	v_mfma_f32_32x32x16_f16 v[0:15], a[208:211], v[160:163], v[0:15]
	ds_read_b128 v[160:163], v193 offset:49152
	v_mfma_f32_32x32x16_f16 v[16:31], a[208:211], v[164:167], v[16:31]
	ds_read_b128 v[164:167], v193 offset:50176
	v_mfma_f32_32x32x16_f16 v[0:15], a[212:215], v[168:171], v[0:15]
	ds_read_b128 v[168:171], v193 offset:51200
	v_mfma_f32_32x32x16_f16 v[16:31], a[212:215], v[172:175], v[16:31]
	ds_read_b128 v[172:175], v193 offset:52224
	global_load_lds_dwordx4 v192, s[44:45] offset:3072 sc1
	s_waitcnt lgkmcnt(4)
	v_mfma_f32_32x32x16_f16 v[0:15], a[216:219], v[176:179], v[0:15]
	ds_read_b128 v[176:179], v193 offset:53248
	v_mfma_f32_32x32x16_f16 v[16:31], a[216:219], v[180:183], v[16:31]
	ds_read_b128 v[180:183], v193 offset:54272
	v_mfma_f32_32x32x16_f16 v[0:15], a[220:223], v[184:187], v[0:15]
	ds_read_b128 v[184:187], v193 offset:55296
	v_mfma_f32_32x32x16_f16 v[16:31], a[220:223], v[188:191], v[16:31]
	ds_read_b128 v[188:191], v193 offset:56320
	s_add_u32 s44, s34, 0x9000
	s_addc_u32 s45, s35, 0
	s_mov_b32 m0, s55
	s_nop 0
	global_load_lds_dwordx4 v192, s[44:45] sc1
	s_waitcnt lgkmcnt(4)
	v_mfma_f32_32x32x16_f16 v[0:15], a[224:227], v[160:163], v[0:15]
	ds_read_b128 v[160:163], v193 offset:57344
	v_mfma_f32_32x32x16_f16 v[16:31], a[224:227], v[164:167], v[16:31]
	ds_read_b128 v[164:167], v193 offset:58368
	v_mfma_f32_32x32x16_f16 v[0:15], a[228:231], v[168:171], v[0:15]
	ds_read_b128 v[168:171], v193 offset:59392
	v_mfma_f32_32x32x16_f16 v[16:31], a[228:231], v[172:175], v[16:31]
	ds_read_b128 v[172:175], v193 offset:60416
	global_load_lds_dwordx4 v192, s[44:45] offset:1024 sc1
	s_waitcnt lgkmcnt(4)
	v_mfma_f32_32x32x16_f16 v[0:15], a[232:235], v[176:179], v[0:15]
	ds_read_b128 v[176:179], v193 offset:61440
	v_mfma_f32_32x32x16_f16 v[16:31], a[232:235], v[180:183], v[16:31]
	ds_read_b128 v[180:183], v193 offset:62464
	v_mfma_f32_32x32x16_f16 v[0:15], a[236:239], v[184:187], v[0:15]
	ds_read_b128 v[184:187], v193 offset:63488
	v_mfma_f32_32x32x16_f16 v[16:31], a[236:239], v[188:191], v[16:31]
	ds_read_b128 v[188:191], v193 offset:64512
	global_load_lds_dwordx4 v192, s[44:45] offset:2048 sc1
	s_waitcnt vmcnt(8)
	s_barrier
	s_waitcnt lgkmcnt(4)
	v_mfma_f32_32x32x16_f16 v[0:15], a[240:243], v[160:163], v[0:15]
	ds_read_b128 v[160:163], v192 offset:0
	v_mfma_f32_32x32x16_f16 v[16:31], a[240:243], v[164:167], v[16:31]
	ds_read_b128 v[164:167], v192 offset:1024
	v_mfma_f32_32x32x16_f16 v[0:15], a[244:247], v[168:171], v[0:15]
	ds_read_b128 v[168:171], v192 offset:2048
	v_mfma_f32_32x32x16_f16 v[16:31], a[244:247], v[172:175], v[16:31]
	ds_read_b128 v[172:175], v192 offset:3072
	global_load_lds_dwordx4 v192, s[44:45] offset:3072 sc1
	s_waitcnt lgkmcnt(4)
	v_mfma_f32_32x32x16_f16 v[0:15], a[248:251], v[176:179], v[0:15]
	ds_read_b128 v[176:179], v192 offset:4096
	v_mfma_f32_32x32x16_f16 v[16:31], a[248:251], v[180:183], v[16:31]
	ds_read_b128 v[180:183], v192 offset:5120
	v_mfma_f32_32x32x16_f16 v[0:15], a[252:255], v[184:187], v[0:15]
	ds_read_b128 v[184:187], v192 offset:6144
	v_mfma_f32_32x32x16_f16 v[16:31], a[252:255], v[188:191], v[16:31]
	ds_read_b128 v[188:191], v192 offset:7168
	s_add_u32 s44, s34, 0x10000
	s_addc_u32 s45, s35, 0
	s_mov_b32 m0, s56
	s_nop 0
	global_load_lds_dwordx4 v192, s[44:45] sc1
	s_and_b32 s64, s33, 1
	s_lshl_b32 s64, s64, 22
	s_add_u32 s64, s64, s50
	s_add_u32 s36, s6, s64
	s_addc_u32 s37, s7, 0
	s_lshl_b32 s64, s33, 3
	s_add_u32 s64, s64, s29
	s_lshl_b32 s64, s64, 5
	s_add_u32 s64, s64, s30
	s_lshl_b32 s64, s64, 2
	s_add_u32 s40, s8, s64
	s_addc_u32 s41, s9, 0
	s_lshl_b32 s64, s33, 11
	s_lshl_b32 s65, s29, 8
	s_add_u32 s64, s64, s65
	s_add_u32 s64, s64, 192
	s_lshl_b32 s64, s64, 3
	s_add_u32 s42, s12, s64
	s_addc_u32 s43, s13, 0
	s_nop 3
	global_load_dwordx2 v[228:229], v249, s[42:43] offset:0
	global_load_dwordx2 v[230:231], v249, s[42:43] offset:256
	s_waitcnt lgkmcnt(4)
	v_mfma_f32_32x32x16_f16 v[32:47], a[0:3], v[160:163], v[32:47]
	ds_read_b128 v[160:163], v192 offset:8192
	v_exp_f32_e32 v200, v0
	v_mfma_f32_32x32x16_f16 v[48:63], a[0:3], v[164:167], v[48:63]
	ds_read_b128 v[164:167], v192 offset:9216
	v_exp_f32_e32 v201, v1
	v_add_f32_e32 v200, 1.0, v200
	v_mfma_f32_32x32x16_f16 v[32:47], a[4:7], v[168:171], v[32:47]
	ds_read_b128 v[168:171], v192 offset:10240
	v_exp_f32_e32 v202, v2
	v_add_f32_e32 v201, 1.0, v201
	v_mfma_f32_32x32x16_f16 v[48:63], a[4:7], v[172:175], v[48:63]
	ds_read_b128 v[172:175], v192 offset:11264
	global_load_lds_dwordx4 v192, s[44:45] offset:1024 sc1
	v_exp_f32_e32 v203, v3
	v_add_f32_e32 v202, 1.0, v202
	s_waitcnt lgkmcnt(4)
	v_mfma_f32_32x32x16_f16 v[32:47], a[8:11], v[176:179], v[32:47]
	ds_read_b128 v[176:179], v192 offset:12288
	v_exp_f32_e32 v204, v4
	v_add_f32_e32 v203, 1.0, v203
	v_mfma_f32_32x32x16_f16 v[48:63], a[8:11], v[180:183], v[48:63]
	ds_read_b128 v[180:183], v192 offset:13312
	v_exp_f32_e32 v205, v5
	v_add_f32_e32 v204, 1.0, v204
	v_mfma_f32_32x32x16_f16 v[32:47], a[12:15], v[184:187], v[32:47]
	ds_read_b128 v[184:187], v192 offset:14336
	v_exp_f32_e32 v206, v6
	v_add_f32_e32 v205, 1.0, v205
	v_mfma_f32_32x32x16_f16 v[48:63], a[12:15], v[188:191], v[48:63]
	ds_read_b128 v[188:191], v192 offset:15360
	global_load_lds_dwordx4 v192, s[44:45] offset:2048 sc1
	v_exp_f32_e32 v207, v7
	v_add_f32_e32 v206, 1.0, v206
	s_waitcnt lgkmcnt(4)
	v_mfma_f32_32x32x16_f16 v[32:47], a[16:19], v[160:163], v[32:47]
	ds_read_b128 v[160:163], v192 offset:16384
	v_exp_f32_e32 v208, v8
	v_add_f32_e32 v207, 1.0, v207
	v_mfma_f32_32x32x16_f16 v[48:63], a[16:19], v[164:167], v[48:63]
	ds_read_b128 v[164:167], v192 offset:17408
	v_exp_f32_e32 v209, v9
	v_add_f32_e32 v208, 1.0, v208
	v_mfma_f32_32x32x16_f16 v[32:47], a[20:23], v[168:171], v[32:47]
	ds_read_b128 v[168:171], v192 offset:18432
	v_exp_f32_e32 v210, v10
	v_add_f32_e32 v209, 1.0, v209
	v_mfma_f32_32x32x16_f16 v[48:63], a[20:23], v[172:175], v[48:63]
	ds_read_b128 v[172:175], v192 offset:19456
	global_load_lds_dwordx4 v192, s[44:45] offset:3072 sc1
	v_exp_f32_e32 v211, v11
	v_add_f32_e32 v210, 1.0, v210
	s_waitcnt lgkmcnt(4)
	v_mfma_f32_32x32x16_f16 v[32:47], a[24:27], v[176:179], v[32:47]
	ds_read_b128 v[176:179], v192 offset:20480
	v_exp_f32_e32 v212, v12
	v_add_f32_e32 v211, 1.0, v211
	v_mfma_f32_32x32x16_f16 v[48:63], a[24:27], v[180:183], v[48:63]
	ds_read_b128 v[180:183], v192 offset:21504
	v_exp_f32_e32 v213, v13
	v_add_f32_e32 v212, 1.0, v212
	v_mfma_f32_32x32x16_f16 v[32:47], a[28:31], v[184:187], v[32:47]
	ds_read_b128 v[184:187], v192 offset:22528
	v_exp_f32_e32 v214, v14
	v_add_f32_e32 v213, 1.0, v213
	v_mfma_f32_32x32x16_f16 v[48:63], a[28:31], v[188:191], v[48:63]
	ds_read_b128 v[188:191], v192 offset:23552
	s_add_u32 s44, s34, 0x11000
	s_addc_u32 s45, s35, 0
	s_mov_b32 m0, s57
	s_nop 0
	global_load_lds_dwordx4 v192, s[44:45] sc1
	v_exp_f32_e32 v215, v15
	v_add_f32_e32 v214, 1.0, v214
	s_waitcnt lgkmcnt(4)
	v_mfma_f32_32x32x16_f16 v[32:47], a[32:35], v[160:163], v[32:47]
	ds_read_b128 v[160:163], v192 offset:24576
	v_add_f32_e32 v215, 1.0, v215
	v_rcp_f32_e32 v200, v200
	v_mfma_f32_32x32x16_f16 v[48:63], a[32:35], v[164:167], v[48:63]
	ds_read_b128 v[164:167], v192 offset:25600
	v_rcp_f32_e32 v201, v201
	v_mfma_f32_32x32x16_f16 v[32:47], a[36:39], v[168:171], v[32:47]
	ds_read_b128 v[168:171], v192 offset:26624
	v_rcp_f32_e32 v202, v202
	v_mfma_f32_32x32x16_f16 v[48:63], a[36:39], v[172:175], v[48:63]
	ds_read_b128 v[172:175], v192 offset:27648
	global_load_lds_dwordx4 v192, s[44:45] offset:1024 sc1
	v_rcp_f32_e32 v203, v203
	s_waitcnt lgkmcnt(4)
	v_mfma_f32_32x32x16_f16 v[32:47], a[40:43], v[176:179], v[32:47]
	ds_read_b128 v[176:179], v192 offset:28672
	v_rcp_f32_e32 v204, v204
	v_mfma_f32_32x32x16_f16 v[48:63], a[40:43], v[180:183], v[48:63]
	ds_read_b128 v[180:183], v192 offset:29696
	v_rcp_f32_e32 v205, v205
	v_mul_f32_e32 v204, v204, v128
	v_mfma_f32_32x32x16_f16 v[32:47], a[44:47], v[184:187], v[32:47]
	ds_read_b128 v[184:187], v192 offset:30720
	v_rcp_f32_e32 v206, v206
	v_mul_f32_e32 v205, v205, v129
	v_mfma_f32_32x32x16_f16 v[48:63], a[44:47], v[188:191], v[48:63]
	ds_read_b128 v[188:191], v192 offset:31744
	global_load_lds_dwordx4 v192, s[44:45] offset:2048 sc1
	v_rcp_f32_e32 v207, v207
	v_mul_f32_e32 v206, v206, v130
	s_waitcnt vmcnt(9)
	s_barrier
	s_waitcnt lgkmcnt(4)
	v_mfma_f32_32x32x16_f16 v[32:47], a[48:51], v[160:163], v[32:47]
	ds_read_b128 v[160:163], v192 offset:32768
	v_rcp_f32_e32 v208, v208
	v_mul_f32_e32 v207, v207, v131
	v_mfma_f32_32x32x16_f16 v[48:63], a[48:51], v[164:167], v[48:63]
	ds_read_b128 v[164:167], v192 offset:33792
	v_rcp_f32_e32 v209, v209
	v_fmamk_f32 v208, v208, 0xc0b8aa3b, v198
	v_mfma_f32_32x32x16_f16 v[32:47], a[52:55], v[168:171], v[32:47]
	ds_read_b128 v[168:171], v192 offset:34816
	v_rcp_f32_e32 v210, v210
	v_fmamk_f32 v209, v209, 0xc0b8aa3b, v198
	v_fma_f32 v128, v200, v208, v204
	v_mfma_f32_32x32x16_f16 v[48:63], a[52:55], v[172:175], v[48:63]
	ds_read_b128 v[172:175], v192 offset:35840
	global_load_lds_dwordx4 v192, s[44:45] offset:3072 sc1
	v_rcp_f32_e32 v211, v211
	v_fmamk_f32 v210, v210, 0xc0b8aa3b, v198
	v_fma_f32 v129, v201, v209, v205
	s_waitcnt lgkmcnt(4)
	v_mfma_f32_32x32x16_f16 v[32:47], a[56:59], v[176:179], v[32:47]
	ds_read_b128 v[176:179], v192 offset:36864
	v_rcp_f32_e32 v212, v212
	v_fmamk_f32 v211, v211, 0xc0b8aa3b, v198
	v_fma_f32 v130, v202, v210, v206
	v_mfma_f32_32x32x16_f16 v[48:63], a[56:59], v[180:183], v[48:63]
	ds_read_b128 v[180:183], v192 offset:37888
	v_rcp_f32_e32 v213, v213
	v_fma_f32 v131, v203, v211, v207
	v_mfma_f32_32x32x16_f16 v[32:47], a[60:63], v[184:187], v[32:47]
	ds_read_b128 v[184:187], v192 offset:38912
	v_rcp_f32_e32 v214, v214
	v_mfma_f32_32x32x16_f16 v[48:63], a[60:63], v[188:191], v[48:63]
	ds_read_b128 v[188:191], v192 offset:39936
	s_add_u32 s44, s34, 0x18000
	s_addc_u32 s45, s35, 0
	s_mov_b32 m0, s58
	s_nop 0
	global_load_lds_dwordx4 v192, s[44:45] sc1
	v_rcp_f32_e32 v215, v215
	s_waitcnt lgkmcnt(4)
	v_mfma_f32_32x32x16_f16 v[32:47], a[64:67], v[160:163], v[32:47]
	ds_read_b128 v[160:163], v192 offset:40960
	v_exp_f32_e32 v200, v128
	v_mfma_f32_32x32x16_f16 v[48:63], a[64:67], v[164:167], v[48:63]
	ds_read_b128 v[164:167], v192 offset:41984
	v_exp_f32_e32 v201, v129
	v_add_f32_e32 v200, 1.0, v200
	v_mfma_f32_32x32x16_f16 v[32:47], a[68:71], v[168:171], v[32:47]
	ds_read_b128 v[168:171], v192 offset:43008
	v_exp_f32_e32 v202, v130
	v_add_f32_e32 v201, 1.0, v201
	v_mfma_f32_32x32x16_f16 v[48:63], a[68:71], v[172:175], v[48:63]
	ds_read_b128 v[172:175], v192 offset:44032
	global_load_lds_dwordx4 v192, s[44:45] offset:1024 sc1
	v_exp_f32_e32 v203, v131
	v_add_f32_e32 v202, 1.0, v202
	s_waitcnt lgkmcnt(4)
	v_mfma_f32_32x32x16_f16 v[32:47], a[72:75], v[176:179], v[32:47]
	ds_read_b128 v[176:179], v192 offset:45056
	v_add_f32_e32 v203, 1.0, v203
	v_rcp_f32_e32 v200, v200
	v_mfma_f32_32x32x16_f16 v[48:63], a[72:75], v[180:183], v[48:63]
	ds_read_b128 v[180:183], v192 offset:46080
	v_rcp_f32_e32 v201, v201
	v_fma_f32 v200, v200, 2.0, -1.0
	v_mfma_f32_32x32x16_f16 v[32:47], a[76:79], v[184:187], v[32:47]
	ds_read_b128 v[184:187], v192 offset:47104
	v_rcp_f32_e32 v202, v202
	v_fma_f32 v201, v201, 2.0, -1.0
	v_mul_f32_e32 v216, v212, v200
	v_mfma_f32_32x32x16_f16 v[48:63], a[76:79], v[188:191], v[48:63]
	ds_read_b128 v[188:191], v192 offset:48128
	global_load_lds_dwordx4 v192, s[44:45] offset:2048 sc1
	v_rcp_f32_e32 v203, v203
	v_fma_f32 v202, v202, 2.0, -1.0
	v_mul_f32_e32 v217, v213, v201
	s_waitcnt lgkmcnt(4)
	v_mfma_f32_32x32x16_f16 v[32:47], a[80:83], v[160:163], v[32:47]
	ds_read_b128 v[160:163], v192 offset:49152
	v_fma_f32 v203, v203, 2.0, -1.0
	v_mul_f32_e32 v218, v214, v202
	v_exp_f32_e32 v200, v16
	v_mfma_f32_32x32x16_f16 v[48:63], a[80:83], v[164:167], v[48:63]
	ds_read_b128 v[164:167], v192 offset:50176
	v_mul_f32_e32 v219, v215, v203
	v_cvt_pk_f16_f32 v220, v216, v217
	v_exp_f32_e32 v201, v17
	v_mfma_f32_32x32x16_f16 v[32:47], a[84:87], v[168:171], v[32:47]
	ds_read_b128 v[168:171], v192 offset:51200
	v_cvt_pk_f16_f32 v221, v218, v219
	v_exp_f32_e32 v202, v18
	v_add_f32_e32 v200, 1.0, v200
	v_mfma_f32_32x32x16_f16 v[48:63], a[84:87], v[172:175], v[48:63]
	ds_read_b128 v[172:175], v192 offset:52224
	global_load_lds_dwordx4 v192, s[44:45] offset:3072 sc1
	s_cmp_lg_u32 s33, s60
	s_cbranch_scc1 .LE_nht26
	s_add_u32 s46, s62, 0x0
	s_addc_u32 s47, s63, 0
	global_store_dwordx4 v250, v[216:219], s[46:47]
	s_waitcnt vmcnt(0)
.LE_nht26:
	v_exp_f32_e32 v203, v19
	s_waitcnt lgkmcnt(4)
	v_mfma_f32_32x32x16_f16 v[32:47], a[88:91], v[176:179], v[32:47]
	ds_read_b128 v[176:179], v192 offset:53248
	v_exp_f32_e32 v204, v20
	v_add_f32_e32 v201, 1.0, v201
	v_add_f32_e32 v202, 1.0, v202
	v_mfma_f32_32x32x16_f16 v[48:63], a[88:91], v[180:183], v[48:63]
	ds_read_b128 v[180:183], v192 offset:54272
	v_exp_f32_e32 v205, v21
	v_add_f32_e32 v203, 1.0, v203
	v_add_f32_e32 v204, 1.0, v204
	v_mfma_f32_32x32x16_f16 v[32:47], a[92:95], v[184:187], v[32:47]
	ds_read_b128 v[184:187], v192 offset:55296
	v_exp_f32_e32 v206, v22
	v_add_f32_e32 v205, 1.0, v205
	v_mfma_f32_32x32x16_f16 v[48:63], a[92:95], v[188:191], v[48:63]
	ds_read_b128 v[188:191], v192 offset:56320
	s_add_u32 s44, s34, 0x19000
	s_addc_u32 s45, s35, 0
	s_mov_b32 m0, s59
	s_nop 0
	global_load_lds_dwordx4 v192, s[44:45] sc1
	s_lshl_b32 s64, s71, 3
	s_add_u32 s64, s64, s29
	s_lshl_b32 s64, s64, 7
	s_add_u32 s38, s8, s64
	s_addc_u32 s39, s9, 0
	global_load_dword v251, v196, s[38:39] sc1
	v_exp_f32_e32 v207, v23
	v_add_f32_e32 v206, 1.0, v206
	s_waitcnt lgkmcnt(4)
	v_mfma_f32_32x32x16_f16 v[32:47], a[96:99], v[160:163], v[32:47]
	ds_read_b128 v[160:163], v192 offset:57344
	v_exp_f32_e32 v208, v24
	v_add_f32_e32 v207, 1.0, v207
	v_mfma_f32_32x32x16_f16 v[48:63], a[96:99], v[164:167], v[48:63]
	ds_read_b128 v[164:167], v192 offset:58368
	v_exp_f32_e32 v209, v25
	v_add_f32_e32 v208, 1.0, v208
	v_mfma_f32_32x32x16_f16 v[32:47], a[100:103], v[168:171], v[32:47]
	ds_read_b128 v[168:171], v192 offset:59392
	v_exp_f32_e32 v210, v26
	v_add_f32_e32 v209, 1.0, v209
	v_mfma_f32_32x32x16_f16 v[48:63], a[100:103], v[172:175], v[48:63]
	ds_read_b128 v[172:175], v192 offset:60416
	global_load_lds_dwordx4 v192, s[44:45] offset:1024 sc1
	v_exp_f32_e32 v211, v27
	v_add_f32_e32 v210, 1.0, v210
	s_waitcnt lgkmcnt(4)
	v_mfma_f32_32x32x16_f16 v[32:47], a[104:107], v[176:179], v[32:47]
	ds_read_b128 v[176:179], v192 offset:61440
	v_exp_f32_e32 v212, v28
	v_add_f32_e32 v211, 1.0, v211
	v_mfma_f32_32x32x16_f16 v[48:63], a[104:107], v[180:183], v[48:63]
	ds_read_b128 v[180:183], v192 offset:62464
	v_exp_f32_e32 v213, v29
	v_add_f32_e32 v212, 1.0, v212
	v_mfma_f32_32x32x16_f16 v[32:47], a[108:111], v[184:187], v[32:47]
	ds_read_b128 v[184:187], v192 offset:63488
	v_exp_f32_e32 v214, v30
	v_add_f32_e32 v213, 1.0, v213
	v_mfma_f32_32x32x16_f16 v[48:63], a[108:111], v[188:191], v[48:63]
	ds_read_b128 v[188:191], v192 offset:64512
	global_load_lds_dwordx4 v192, s[44:45] offset:2048 sc1
	v_exp_f32_e32 v215, v31
	v_add_f32_e32 v214, 1.0, v214
	s_waitcnt vmcnt(8)
	s_barrier
	s_waitcnt lgkmcnt(4)
	v_mfma_f32_32x32x16_f16 v[32:47], a[112:115], v[160:163], v[32:47]
	ds_read_b128 v[160:163], v193 offset:0
	v_add_f32_e32 v215, 1.0, v215
	v_rcp_f32_e32 v200, v200
	v_mfma_f32_32x32x16_f16 v[48:63], a[112:115], v[164:167], v[48:63]
	ds_read_b128 v[164:167], v193 offset:1024
	v_rcp_f32_e32 v201, v201
	v_mfma_f32_32x32x16_f16 v[32:47], a[116:119], v[168:171], v[32:47]
	ds_read_b128 v[168:171], v193 offset:2048
	v_rcp_f32_e32 v202, v202
	v_mfma_f32_32x32x16_f16 v[48:63], a[116:119], v[172:175], v[48:63]
	ds_read_b128 v[172:175], v193 offset:3072
	global_load_lds_dwordx4 v192, s[44:45] offset:3072 sc1
	v_rcp_f32_e32 v203, v203
	s_waitcnt lgkmcnt(4)
	v_mfma_f32_32x32x16_f16 v[32:47], a[120:123], v[176:179], v[32:47]
	ds_read_b128 v[176:179], v193 offset:4096
	v_rcp_f32_e32 v204, v204
	ds_read_b128 v[236:239], v248 offset:0
	ds_read_b64 v[240:241], v248 offset:32
	ds_read_b128 v[242:245], v248 offset:16
	ds_read_b64 v[246:247], v248 offset:40
	v_mfma_f32_32x32x16_f16 v[48:63], a[120:123], v[180:183], v[48:63]
	ds_read_b128 v[180:183], v193 offset:5120
	v_rcp_f32_e32 v205, v205
	v_mul_f32_e32 v204, v204, v132
	s_waitcnt lgkmcnt(3)
	v_fma_f32 v96, v229, v237, v240
	v_mfma_f32_32x32x16_f16 v[32:47], a[124:127], v[184:187], v[32:47]
	ds_read_b128 v[184:187], v193 offset:6144
	v_rcp_f32_e32 v206, v206
	v_mul_f32_e32 v205, v205, v133
	v_fma_f32 v97, v229, v239, v241
	v_fmac_f32_e32 v96, v228, v236
	v_mfma_f32_32x32x16_f16 v[48:63], a[124:127], v[188:191], v[48:63]
	ds_read_b128 v[188:191], v193 offset:7168
	s_waitcnt vmcnt(3)
	v_cmp_gt_u32_e32 vcc, 3, v251
	s_cbranch_vccz .LE_tok27

.LE_tok27:
	s_and_b32 s64, s71, 1
	s_lshl_b32 s64, s64, 22
	s_add_u32 s64, s64, s49
	s_add_u32 s64, s64, 0x40000
	s_add_u32 s34, s6, s64
	s_addc_u32 s35, s7, 0
	s_add_u32 s44, s34, 0x0
	s_addc_u32 s45, s35, 0
	s_mov_b32 m0, s52
	s_nop 0
	global_load_lds_dwordx4 v192, s[44:45] sc1
	v_rcp_f32_e32 v207, v207
	v_mul_f32_e32 v206, v206, v134
	v_fmac_f32_e32 v97, v228, v238
	v_fma_f32 v112, v231, v237, v240
	v_mfma_f32_32x32x16_f16 v[32:47], a[128:131], v[160:163], v[32:47]
	ds_read_b128 v[160:163], v193 offset:8192
	v_rcp_f32_e32 v208, v208
	v_mul_f32_e32 v207, v207, v135
	v_fma_f32 v113, v231, v239, v241
	v_fmac_f32_e32 v112, v230, v236
	v_mfma_f32_32x32x16_f16 v[48:63], a[128:131], v[164:167], v[48:63]
	ds_read_b128 v[164:167], v193 offset:9216
	v_rcp_f32_e32 v209, v209
	v_fmamk_f32 v208, v208, 0xc0b8aa3b, v198
	v_fmac_f32_e32 v113, v230, v238
	ds_read_b128 v[236:239], v248 offset:48
	ds_read_b64 v[240:241], v248 offset:80
	v_mfma_f32_32x32x16_f16 v[32:47], a[132:135], v[168:171], v[32:47]
	ds_read_b128 v[168:171], v193 offset:10240
	v_rcp_f32_e32 v210, v210
	v_fmamk_f32 v209, v209, 0xc0b8aa3b, v198
	v_fma_f32 v132, v200, v208, v204
	s_waitcnt lgkmcnt(8)
	v_fma_f32 v98, v229, v243, v246
	v_mfma_f32_32x32x16_f16 v[48:63], a[132:135], v[172:175], v[48:63]
	ds_read_b128 v[172:175], v193 offset:11264
	global_load_lds_dwordx4 v192, s[44:45] offset:1024 sc1
	v_rcp_f32_e32 v211, v211
	v_fmamk_f32 v210, v210, 0xc0b8aa3b, v198
	v_fma_f32 v133, v201, v209, v205
	v_fma_f32 v99, v229, v245, v247
	v_fmac_f32_e32 v98, v228, v242
	s_waitcnt lgkmcnt(6)
	v_mfma_f32_32x32x16_f16 v[32:47], a[136:139], v[176:179], v[32:47]
	ds_read_b128 v[176:179], v193 offset:12288
	v_rcp_f32_e32 v212, v212
	v_fmamk_f32 v211, v211, 0xc0b8aa3b, v198
	v_fma_f32 v134, v202, v210, v206
	v_fmac_f32_e32 v99, v228, v244
	v_fma_f32 v114, v231, v243, v246
	v_mfma_f32_32x32x16_f16 v[48:63], a[136:139], v[180:183], v[48:63]
	ds_read_b128 v[180:183], v193 offset:13312
	v_rcp_f32_e32 v213, v213
	v_fma_f32 v135, v203, v211, v207
	v_fma_f32 v115, v231, v245, v247
	v_fmac_f32_e32 v114, v230, v242
	v_mfma_f32_32x32x16_f16 v[32:47], a[140:143], v[184:187], v[32:47]
	ds_read_b128 v[184:187], v193 offset:14336
	v_rcp_f32_e32 v214, v214
	v_fmac_f32_e32 v115, v230, v244
	ds_read_b128 v[242:245], v248 offset:64
	ds_read_b64 v[246:247], v248 offset:88
	v_mfma_f32_32x32x16_f16 v[48:63], a[140:143], v[188:191], v[48:63]
	ds_read_b128 v[188:191], v193 offset:15360
	global_load_lds_dwordx4 v192, s[44:45] offset:2048 sc1
	v_rcp_f32_e32 v215, v215
	s_waitcnt lgkmcnt(8)
	v_fma_f32 v100, v229, v237, v240
	s_waitcnt lgkmcnt(6)
	v_mfma_f32_32x32x16_f16 v[32:47], a[144:147], v[160:163], v[32:47]
	ds_read_b128 v[160:163], v193 offset:16384
	v_exp_f32_e32 v200, v132
	v_fma_f32 v101, v229, v239, v241
	v_fmac_f32_e32 v100, v228, v236
	v_mfma_f32_32x32x16_f16 v[48:63], a[144:147], v[164:167], v[48:63]
	ds_read_b128 v[164:167], v193 offset:17408
	v_exp_f32_e32 v201, v133
	v_add_f32_e32 v200, 1.0, v200
	v_fmac_f32_e32 v101, v228, v238
	v_fma_f32 v116, v231, v237, v240
	v_mfma_f32_32x32x16_f16 v[32:47], a[148:151], v[168:171], v[32:47]
	ds_read_b128 v[168:171], v193 offset:18432
	v_exp_f32_e32 v202, v134
	v_add_f32_e32 v201, 1.0, v201
	v_fma_f32 v117, v231, v239, v241
	v_fmac_f32_e32 v116, v230, v236
	v_mfma_f32_32x32x16_f16 v[48:63], a[148:151], v[172:175], v[48:63]
	ds_read_b128 v[172:175], v193 offset:19456
	global_load_lds_dwordx4 v192, s[44:45] offset:3072 sc1
	v_exp_f32_e32 v203, v135
	v_add_f32_e32 v202, 1.0, v202
	v_fmac_f32_e32 v117, v230, v238
	ds_read_b128 v[236:239], v248 offset:96
	ds_read_b64 v[240:241], v248 offset:128
	s_waitcnt lgkmcnt(6)
	v_mfma_f32_32x32x16_f16 v[32:47], a[152:155], v[176:179], v[32:47]
	ds_read_b128 v[176:179], v193 offset:20480
	v_add_f32_e32 v203, 1.0, v203
	v_rcp_f32_e32 v200, v200
	v_fma_f32 v102, v229, v243, v246
	v_mfma_f32_32x32x16_f16 v[48:63], a[152:155], v[180:183], v[48:63]
	ds_read_b128 v[180:183], v193 offset:21504
	v_rcp_f32_e32 v201, v201
	v_fma_f32 v200, v200, 2.0, -1.0
	v_fma_f32 v103, v229, v245, v247
	v_fmac_f32_e32 v102, v228, v242
	v_mfma_f32_32x32x16_f16 v[32:47], a[156:159], v[184:187], v[32:47]
	ds_read_b128 v[184:187], v193 offset:22528
	v_rcp_f32_e32 v202, v202
	v_fma_f32 v201, v201, 2.0, -1.0
	v_mul_f32_e32 v216, v212, v200
	v_fmac_f32_e32 v103, v228, v244
	v_fma_f32 v118, v231, v243, v246
	v_mfma_f32_32x32x16_f16 v[48:63], a[156:159], v[188:191], v[48:63]
	ds_read_b128 v[188:191], v193 offset:23552
	s_add_u32 s44, s34, 0x1000
	s_addc_u32 s45, s35, 0
	s_mov_b32 m0, s53
	s_nop 0
	global_load_lds_dwordx4 v192, s[44:45] sc1
	v_rcp_f32_e32 v203, v203
	v_fma_f32 v202, v202, 2.0, -1.0
	v_mul_f32_e32 v217, v213, v201
	v_fma_f32 v119, v231, v245, v247
	v_fmac_f32_e32 v118, v230, v242
	s_waitcnt lgkmcnt(6)
	v_mfma_f32_32x32x16_f16 v[32:47], a[160:163], v[160:163], v[32:47]
	ds_read_b128 v[160:163], v193 offset:24576
	v_fma_f32 v203, v203, 2.0, -1.0
	v_mul_f32_e32 v218, v214, v202
	v_fmac_f32_e32 v119, v230, v244
	ds_read_b128 v[242:245], v248 offset:112
	ds_read_b64 v[246:247], v248 offset:136
	v_mfma_f32_32x32x16_f16 v[48:63], a[160:163], v[164:167], v[48:63]
	ds_read_b128 v[164:167], v193 offset:25600
	v_mul_f32_e32 v219, v215, v203
	v_cvt_pk_f16_f32 v222, v216, v217
	s_waitcnt lgkmcnt(8)
	v_fma_f32 v104, v229, v237, v240
	v_mfma_f32_32x32x16_f16 v[32:47], a[164:167], v[168:171], v[32:47]
	ds_read_b128 v[168:171], v193 offset:26624
	v_cvt_pk_f16_f32 v223, v218, v219
	v_fma_f32 v105, v229, v239, v241
	v_fmac_f32_e32 v104, v228, v236
	v_mfma_f32_32x32x16_f16 v[48:63], a[164:167], v[172:175], v[48:63]
	ds_read_b128 v[172:175], v193 offset:27648
	global_load_lds_dwordx4 v192, s[44:45] offset:1024 sc1
	s_cmp_lg_u32 s33, s60
	s_cbranch_scc1 .LE_nht29
	s_add_u32 s46, s62, 0x20000
	s_addc_u32 s47, s63, 0
	global_store_dwordx4 v250, v[216:219], s[46:47]
	s_waitcnt vmcnt(0)
.LE_nht29:
	v_fmac_f32_e32 v105, v228, v238
	v_fma_f32 v120, v231, v237, v240
	s_waitcnt lgkmcnt(6)
	v_mfma_f32_32x32x16_f16 v[32:47], a[168:171], v[176:179], v[32:47]
	ds_read_b128 v[176:179], v193 offset:28672
	s_nop 1
	v_permlane32_swap_b32_e32 v220, v222
	v_permlane32_swap_b32_e32 v221, v223
	s_cmp_eq_u32 s31, 0
	s_cbranch_scc1 .LE_slow30
	global_store_dwordx4 v195, v[220:223], s[36:37] offset:0
	s_branch .LE_join31

.LE_join31:
	v_fma_f32 v121, v231, v239, v241
	v_fmac_f32_e32 v120, v230, v236
	v_mfma_f32_32x32x16_f16 v[48:63], a[168:171], v[180:183], v[48:63]
	ds_read_b128 v[180:183], v193 offset:29696
	v_fmac_f32_e32 v121, v230, v238
	ds_read_b128 v[236:239], v248 offset:144
	ds_read_b64 v[240:241], v248 offset:176
	v_mfma_f32_32x32x16_f16 v[32:47], a[172:175], v[184:187], v[32:47]
	ds_read_b128 v[184:187], v193 offset:30720
	s_waitcnt lgkmcnt(8)
	v_fma_f32 v106, v229, v243, v246
	v_mfma_f32_32x32x16_f16 v[48:63], a[172:175], v[188:191], v[48:63]
	ds_read_b128 v[188:191], v193 offset:31744
	global_load_lds_dwordx4 v192, s[44:45] offset:2048 sc1
	v_fma_f32 v107, v229, v245, v247
	v_fmac_f32_e32 v106, v228, v242
	s_waitcnt vmcnt(8)
	s_barrier
	s_waitcnt lgkmcnt(6)
	v_mfma_f32_32x32x16_f16 v[32:47], a[176:179], v[160:163], v[32:47]
	ds_read_b128 v[160:163], v193 offset:32768
	v_fmac_f32_e32 v107, v228, v244
	v_fma_f32 v122, v231, v243, v246
	v_mfma_f32_32x32x16_f16 v[48:63], a[176:179], v[164:167], v[48:63]
	ds_read_b128 v[164:167], v193 offset:33792
	v_fma_f32 v123, v231, v245, v247
	v_fmac_f32_e32 v122, v230, v242
	v_mfma_f32_32x32x16_f16 v[32:47], a[180:183], v[168:171], v[32:47]
	ds_read_b128 v[168:171], v193 offset:34816
	v_fmac_f32_e32 v123, v230, v244
	ds_read_b128 v[242:245], v248 offset:160
	ds_read_b64 v[246:247], v248 offset:184
	v_mfma_f32_32x32x16_f16 v[48:63], a[180:183], v[172:175], v[48:63]
	ds_read_b128 v[172:175], v193 offset:35840
	global_load_lds_dwordx4 v192, s[44:45] offset:3072 sc1
	s_waitcnt lgkmcnt(8)
	v_fma_f32 v108, v229, v237, v240
	s_waitcnt lgkmcnt(6)
	v_mfma_f32_32x32x16_f16 v[32:47], a[184:187], v[176:179], v[32:47]
	ds_read_b128 v[176:179], v193 offset:36864
	v_fma_f32 v109, v229, v239, v241
	v_fmac_f32_e32 v108, v228, v236
	v_mfma_f32_32x32x16_f16 v[48:63], a[184:187], v[180:183], v[48:63]
	ds_read_b128 v[180:183], v193 offset:37888
	v_fmac_f32_e32 v109, v228, v238
	v_fma_f32 v124, v231, v237, v240
	v_mfma_f32_32x32x16_f16 v[32:47], a[188:191], v[184:187], v[32:47]
	ds_read_b128 v[184:187], v193 offset:38912
	v_fma_f32 v125, v231, v239, v241
	v_fmac_f32_e32 v124, v230, v236
	v_mfma_f32_32x32x16_f16 v[48:63], a[188:191], v[188:191], v[48:63]
	ds_read_b128 v[188:191], v193 offset:39936
	s_add_u32 s44, s34, 0x8000
	s_addc_u32 s45, s35, 0
	s_mov_b32 m0, s54
	s_nop 0
	global_load_lds_dwordx4 v192, s[44:45] sc1
	v_fmac_f32_e32 v125, v230, v238
	s_waitcnt lgkmcnt(5)
	s_waitcnt lgkmcnt(4)
	v_mfma_f32_32x32x16_f16 v[32:47], a[192:195], v[160:163], v[32:47]
	ds_read_b128 v[160:163], v193 offset:40960
	v_fma_f32 v110, v229, v243, v246
	v_fma_f32 v111, v229, v245, v247
	v_mfma_f32_32x32x16_f16 v[48:63], a[192:195], v[164:167], v[48:63]
	ds_read_b128 v[164:167], v193 offset:41984
	v_fmac_f32_e32 v110, v228, v242
	v_fmac_f32_e32 v111, v228, v244
	s_waitcnt vmcnt(3)
	s_barrier
	v_mov_b32_e32 v199, 1
	s_cmp_eq_u32 s31, 0
	s_cbranch_scc1 .LE_slow32
	global_store_dword v197, v199, s[40:41]
	s_branch .LE_join33

.LE_join33:
	v_mfma_f32_32x32x16_f16 v[32:47], a[196:199], v[168:171], v[32:47]
	ds_read_b128 v[168:171], v193 offset:43008
	v_fma_f32 v126, v231, v243, v246
	v_fma_f32 v127, v231, v245, v247
	v_mfma_f32_32x32x16_f16 v[48:63], a[196:199], v[172:175], v[48:63]
	ds_read_b128 v[172:175], v193 offset:44032
	global_load_lds_dwordx4 v192, s[44:45] offset:1024 sc1
	v_fmac_f32_e32 v126, v230, v242
	v_fmac_f32_e32 v127, v230, v244
	s_waitcnt lgkmcnt(4)
	v_mfma_f32_32x32x16_f16 v[32:47], a[200:203], v[176:179], v[32:47]
	ds_read_b128 v[176:179], v193 offset:45056
	v_mfma_f32_32x32x16_f16 v[48:63], a[200:203], v[180:183], v[48:63]
	ds_read_b128 v[180:183], v193 offset:46080
	v_mfma_f32_32x32x16_f16 v[32:47], a[204:207], v[184:187], v[32:47]
	ds_read_b128 v[184:187], v193 offset:47104
	v_mfma_f32_32x32x16_f16 v[48:63], a[204:207], v[188:191], v[48:63]
	ds_read_b128 v[188:191], v193 offset:48128
	global_load_lds_dwordx4 v192, s[44:45] offset:2048 sc1
	s_waitcnt lgkmcnt(4)
	v_mfma_f32_32x32x16_f16 v[32:47], a[208:211], v[160:163], v[32:47]
	ds_read_b128 v[160:163], v193 offset:49152
	v_mfma_f32_32x32x16_f16 v[48:63], a[208:211], v[164:167], v[48:63]
	ds_read_b128 v[164:167], v193 offset:50176
	v_mfma_f32_32x32x16_f16 v[32:47], a[212:215], v[168:171], v[32:47]
	ds_read_b128 v[168:171], v193 offset:51200
	v_mfma_f32_32x32x16_f16 v[48:63], a[212:215], v[172:175], v[48:63]
	ds_read_b128 v[172:175], v193 offset:52224
	global_load_lds_dwordx4 v192, s[44:45] offset:3072 sc1
	s_waitcnt lgkmcnt(4)
	v_mfma_f32_32x32x16_f16 v[32:47], a[216:219], v[176:179], v[32:47]
	ds_read_b128 v[176:179], v193 offset:53248
	v_mfma_f32_32x32x16_f16 v[48:63], a[216:219], v[180:183], v[48:63]
	ds_read_b128 v[180:183], v193 offset:54272
	v_mfma_f32_32x32x16_f16 v[32:47], a[220:223], v[184:187], v[32:47]
	ds_read_b128 v[184:187], v193 offset:55296
	v_mfma_f32_32x32x16_f16 v[48:63], a[220:223], v[188:191], v[48:63]
	ds_read_b128 v[188:191], v193 offset:56320
	s_add_u32 s44, s34, 0x9000
	s_addc_u32 s45, s35, 0
	s_mov_b32 m0, s55
	s_nop 0
	global_load_lds_dwordx4 v192, s[44:45] sc1
	s_waitcnt lgkmcnt(4)
	v_mfma_f32_32x32x16_f16 v[32:47], a[224:227], v[160:163], v[32:47]
	ds_read_b128 v[160:163], v193 offset:57344
	v_mfma_f32_32x32x16_f16 v[48:63], a[224:227], v[164:167], v[48:63]
	ds_read_b128 v[164:167], v193 offset:58368
	v_mfma_f32_32x32x16_f16 v[32:47], a[228:231], v[168:171], v[32:47]
	ds_read_b128 v[168:171], v193 offset:59392
	v_mfma_f32_32x32x16_f16 v[48:63], a[228:231], v[172:175], v[48:63]
	ds_read_b128 v[172:175], v193 offset:60416
	global_load_lds_dwordx4 v192, s[44:45] offset:1024 sc1
	s_waitcnt lgkmcnt(4)
	v_mfma_f32_32x32x16_f16 v[32:47], a[232:235], v[176:179], v[32:47]
	ds_read_b128 v[176:179], v193 offset:61440
	v_mfma_f32_32x32x16_f16 v[48:63], a[232:235], v[180:183], v[48:63]
	ds_read_b128 v[180:183], v193 offset:62464
	v_mfma_f32_32x32x16_f16 v[32:47], a[236:239], v[184:187], v[32:47]
	ds_read_b128 v[184:187], v193 offset:63488
	v_mfma_f32_32x32x16_f16 v[48:63], a[236:239], v[188:191], v[48:63]
	ds_read_b128 v[188:191], v193 offset:64512
	global_load_lds_dwordx4 v192, s[44:45] offset:2048 sc1
	s_waitcnt vmcnt(8)
	s_barrier
	s_waitcnt lgkmcnt(4)
	v_mfma_f32_32x32x16_f16 v[32:47], a[240:243], v[160:163], v[32:47]
	ds_read_b128 v[160:163], v192 offset:0
	v_mfma_f32_32x32x16_f16 v[48:63], a[240:243], v[164:167], v[48:63]
	ds_read_b128 v[164:167], v192 offset:1024
	v_mfma_f32_32x32x16_f16 v[32:47], a[244:247], v[168:171], v[32:47]
	ds_read_b128 v[168:171], v192 offset:2048
	v_mfma_f32_32x32x16_f16 v[48:63], a[244:247], v[172:175], v[48:63]
	ds_read_b128 v[172:175], v192 offset:3072
	global_load_lds_dwordx4 v192, s[44:45] offset:3072 sc1
	s_waitcnt lgkmcnt(4)
	v_mfma_f32_32x32x16_f16 v[32:47], a[248:251], v[176:179], v[32:47]
	ds_read_b128 v[176:179], v192 offset:4096
	v_mfma_f32_32x32x16_f16 v[48:63], a[248:251], v[180:183], v[48:63]
	ds_read_b128 v[180:183], v192 offset:5120
	v_mfma_f32_32x32x16_f16 v[32:47], a[252:255], v[184:187], v[32:47]
	ds_read_b128 v[184:187], v192 offset:6144
	v_mfma_f32_32x32x16_f16 v[48:63], a[252:255], v[188:191], v[48:63]
	ds_read_b128 v[188:191], v192 offset:7168
	s_add_u32 s44, s34, 0x10000
	s_addc_u32 s45, s35, 0
	s_mov_b32 m0, s56
	s_nop 0
	global_load_lds_dwordx4 v192, s[44:45] sc1
	s_and_b32 s64, s33, 1
	s_lshl_b32 s64, s64, 22
	s_add_u32 s64, s64, s50
	s_add_u32 s64, s64, 0x20000
	s_add_u32 s36, s6, s64
	s_addc_u32 s37, s7, 0
	s_lshl_b32 s64, s33, 3
	s_add_u32 s64, s64, s29
	s_lshl_b32 s64, s64, 5
	s_add_u32 s64, s64, s30
	s_lshl_b32 s64, s64, 2
	s_add_u32 s40, s8, s64
	s_addc_u32 s41, s9, 0
	s_lshl_b32 s64, s61, 11
	s_lshl_b32 s65, s29, 8
	s_add_u32 s64, s64, s65
	s_lshl_b32 s64, s64, 3
	s_add_u32 s42, s12, s64
	s_addc_u32 s43, s13, 0
	s_nop 3
	global_load_dwordx2 v[228:229], v249, s[42:43] offset:0
	global_load_dwordx2 v[230:231], v249, s[42:43] offset:256
	s_waitcnt lgkmcnt(4)
	v_mfma_f32_32x32x16_f16 v[64:79], a[0:3], v[160:163], v[64:79]
	ds_read_b128 v[160:163], v192 offset:8192
	v_exp_f32_e32 v200, v32
	v_mfma_f32_32x32x16_f16 v[80:95], a[0:3], v[164:167], v[80:95]
	ds_read_b128 v[164:167], v192 offset:9216
	v_exp_f32_e32 v201, v33
	v_add_f32_e32 v200, 1.0, v200
	v_mfma_f32_32x32x16_f16 v[64:79], a[4:7], v[168:171], v[64:79]
	ds_read_b128 v[168:171], v192 offset:10240
	v_exp_f32_e32 v202, v34
	v_add_f32_e32 v201, 1.0, v201
	v_mfma_f32_32x32x16_f16 v[80:95], a[4:7], v[172:175], v[80:95]
	ds_read_b128 v[172:175], v192 offset:11264
	global_load_lds_dwordx4 v192, s[44:45] offset:1024 sc1
	v_exp_f32_e32 v203, v35
	v_add_f32_e32 v202, 1.0, v202
	s_waitcnt lgkmcnt(4)
	v_mfma_f32_32x32x16_f16 v[64:79], a[8:11], v[176:179], v[64:79]
	ds_read_b128 v[176:179], v192 offset:12288
	v_exp_f32_e32 v204, v36
	v_add_f32_e32 v203, 1.0, v203
	v_mfma_f32_32x32x16_f16 v[80:95], a[8:11], v[180:183], v[80:95]
	ds_read_b128 v[180:183], v192 offset:13312
	v_exp_f32_e32 v205, v37
	v_add_f32_e32 v204, 1.0, v204
	v_mfma_f32_32x32x16_f16 v[64:79], a[12:15], v[184:187], v[64:79]
	ds_read_b128 v[184:187], v192 offset:14336
	v_exp_f32_e32 v206, v38
	v_add_f32_e32 v205, 1.0, v205
	v_mfma_f32_32x32x16_f16 v[80:95], a[12:15], v[188:191], v[80:95]
	ds_read_b128 v[188:191], v192 offset:15360
	global_load_lds_dwordx4 v192, s[44:45] offset:2048 sc1
	v_exp_f32_e32 v207, v39
	v_add_f32_e32 v206, 1.0, v206
	s_waitcnt lgkmcnt(4)
	v_mfma_f32_32x32x16_f16 v[64:79], a[16:19], v[160:163], v[64:79]
	ds_read_b128 v[160:163], v192 offset:16384
	v_exp_f32_e32 v208, v40
	v_add_f32_e32 v207, 1.0, v207
	v_mfma_f32_32x32x16_f16 v[80:95], a[16:19], v[164:167], v[80:95]
	ds_read_b128 v[164:167], v192 offset:17408
	v_exp_f32_e32 v209, v41
	v_add_f32_e32 v208, 1.0, v208
	v_mfma_f32_32x32x16_f16 v[64:79], a[20:23], v[168:171], v[64:79]
	ds_read_b128 v[168:171], v192 offset:18432
	v_exp_f32_e32 v210, v42
	v_add_f32_e32 v209, 1.0, v209
	v_mfma_f32_32x32x16_f16 v[80:95], a[20:23], v[172:175], v[80:95]
	ds_read_b128 v[172:175], v192 offset:19456
	global_load_lds_dwordx4 v192, s[44:45] offset:3072 sc1
	v_exp_f32_e32 v211, v43
	v_add_f32_e32 v210, 1.0, v210
	s_waitcnt lgkmcnt(4)
	v_mfma_f32_32x32x16_f16 v[64:79], a[24:27], v[176:179], v[64:79]
	ds_read_b128 v[176:179], v192 offset:20480
	v_exp_f32_e32 v212, v44
	v_add_f32_e32 v211, 1.0, v211
	v_mfma_f32_32x32x16_f16 v[80:95], a[24:27], v[180:183], v[80:95]
	ds_read_b128 v[180:183], v192 offset:21504
	v_exp_f32_e32 v213, v45
	v_add_f32_e32 v212, 1.0, v212
	v_mfma_f32_32x32x16_f16 v[64:79], a[28:31], v[184:187], v[64:79]
	ds_read_b128 v[184:187], v192 offset:22528
	v_exp_f32_e32 v214, v46
	v_add_f32_e32 v213, 1.0, v213
	v_mfma_f32_32x32x16_f16 v[80:95], a[28:31], v[188:191], v[80:95]
	ds_read_b128 v[188:191], v192 offset:23552
	s_add_u32 s44, s34, 0x11000
	s_addc_u32 s45, s35, 0
	s_mov_b32 m0, s57
	s_nop 0
	global_load_lds_dwordx4 v192, s[44:45] sc1
	v_exp_f32_e32 v215, v47
	v_add_f32_e32 v214, 1.0, v214
	s_waitcnt lgkmcnt(4)
	v_mfma_f32_32x32x16_f16 v[64:79], a[32:35], v[160:163], v[64:79]
	ds_read_b128 v[160:163], v192 offset:24576
	v_add_f32_e32 v215, 1.0, v215
	v_rcp_f32_e32 v200, v200
	v_mfma_f32_32x32x16_f16 v[80:95], a[32:35], v[164:167], v[80:95]
	ds_read_b128 v[164:167], v192 offset:25600
	v_rcp_f32_e32 v201, v201
	v_mfma_f32_32x32x16_f16 v[64:79], a[36:39], v[168:171], v[64:79]
	ds_read_b128 v[168:171], v192 offset:26624
	v_rcp_f32_e32 v202, v202
	v_mfma_f32_32x32x16_f16 v[80:95], a[36:39], v[172:175], v[80:95]
	ds_read_b128 v[172:175], v192 offset:27648
	global_load_lds_dwordx4 v192, s[44:45] offset:1024 sc1
	v_rcp_f32_e32 v203, v203
	s_waitcnt lgkmcnt(4)
	v_mfma_f32_32x32x16_f16 v[64:79], a[40:43], v[176:179], v[64:79]
	ds_read_b128 v[176:179], v192 offset:28672
	v_rcp_f32_e32 v204, v204
	v_mfma_f32_32x32x16_f16 v[80:95], a[40:43], v[180:183], v[80:95]
	ds_read_b128 v[180:183], v192 offset:29696
	v_rcp_f32_e32 v205, v205
	v_mul_f32_e32 v204, v204, v136
	v_mfma_f32_32x32x16_f16 v[64:79], a[44:47], v[184:187], v[64:79]
	ds_read_b128 v[184:187], v192 offset:30720
	v_rcp_f32_e32 v206, v206
	v_mul_f32_e32 v205, v205, v137
	v_mfma_f32_32x32x16_f16 v[80:95], a[44:47], v[188:191], v[80:95]
	ds_read_b128 v[188:191], v192 offset:31744
	global_load_lds_dwordx4 v192, s[44:45] offset:2048 sc1
	v_rcp_f32_e32 v207, v207
	v_mul_f32_e32 v206, v206, v138
	s_waitcnt vmcnt(9)
	s_barrier
	s_waitcnt lgkmcnt(4)
	v_mfma_f32_32x32x16_f16 v[64:79], a[48:51], v[160:163], v[64:79]
	ds_read_b128 v[160:163], v192 offset:32768
	v_rcp_f32_e32 v208, v208
	v_mul_f32_e32 v207, v207, v139
	v_mfma_f32_32x32x16_f16 v[80:95], a[48:51], v[164:167], v[80:95]
	ds_read_b128 v[164:167], v192 offset:33792
	v_rcp_f32_e32 v209, v209
	v_fmamk_f32 v208, v208, 0xc0b8aa3b, v198
	v_mfma_f32_32x32x16_f16 v[64:79], a[52:55], v[168:171], v[64:79]
	ds_read_b128 v[168:171], v192 offset:34816
	v_rcp_f32_e32 v210, v210
	v_fmamk_f32 v209, v209, 0xc0b8aa3b, v198
	v_fma_f32 v136, v200, v208, v204
	v_mfma_f32_32x32x16_f16 v[80:95], a[52:55], v[172:175], v[80:95]
	ds_read_b128 v[172:175], v192 offset:35840
	global_load_lds_dwordx4 v192, s[44:45] offset:3072 sc1
	v_rcp_f32_e32 v211, v211
	v_fmamk_f32 v210, v210, 0xc0b8aa3b, v198
	v_fma_f32 v137, v201, v209, v205
	s_waitcnt lgkmcnt(4)
	v_mfma_f32_32x32x16_f16 v[64:79], a[56:59], v[176:179], v[64:79]
	ds_read_b128 v[176:179], v192 offset:36864
	v_rcp_f32_e32 v212, v212
	v_fmamk_f32 v211, v211, 0xc0b8aa3b, v198
	v_fma_f32 v138, v202, v210, v206
	v_mfma_f32_32x32x16_f16 v[80:95], a[56:59], v[180:183], v[80:95]
	ds_read_b128 v[180:183], v192 offset:37888
	v_rcp_f32_e32 v213, v213
	v_fma_f32 v139, v203, v211, v207
	v_mfma_f32_32x32x16_f16 v[64:79], a[60:63], v[184:187], v[64:79]
	ds_read_b128 v[184:187], v192 offset:38912
	v_rcp_f32_e32 v214, v214
	v_mfma_f32_32x32x16_f16 v[80:95], a[60:63], v[188:191], v[80:95]
	ds_read_b128 v[188:191], v192 offset:39936
	s_add_u32 s44, s34, 0x18000
	s_addc_u32 s45, s35, 0
	s_mov_b32 m0, s58
	s_nop 0
	global_load_lds_dwordx4 v192, s[44:45] sc1
	v_rcp_f32_e32 v215, v215
	s_waitcnt lgkmcnt(4)
	v_mfma_f32_32x32x16_f16 v[64:79], a[64:67], v[160:163], v[64:79]
	ds_read_b128 v[160:163], v192 offset:40960
	v_exp_f32_e32 v200, v136
	v_mfma_f32_32x32x16_f16 v[80:95], a[64:67], v[164:167], v[80:95]
	ds_read_b128 v[164:167], v192 offset:41984
	v_exp_f32_e32 v201, v137
	v_add_f32_e32 v200, 1.0, v200
	v_mfma_f32_32x32x16_f16 v[64:79], a[68:71], v[168:171], v[64:79]
	ds_read_b128 v[168:171], v192 offset:43008
	v_exp_f32_e32 v202, v138
	v_add_f32_e32 v201, 1.0, v201
	v_mfma_f32_32x32x16_f16 v[80:95], a[68:71], v[172:175], v[80:95]
	ds_read_b128 v[172:175], v192 offset:44032
	global_load_lds_dwordx4 v192, s[44:45] offset:1024 sc1
	v_exp_f32_e32 v203, v139
	v_add_f32_e32 v202, 1.0, v202
	s_waitcnt lgkmcnt(4)
	v_mfma_f32_32x32x16_f16 v[64:79], a[72:75], v[176:179], v[64:79]
	ds_read_b128 v[176:179], v192 offset:45056
	v_add_f32_e32 v203, 1.0, v203
	v_rcp_f32_e32 v200, v200
	v_mfma_f32_32x32x16_f16 v[80:95], a[72:75], v[180:183], v[80:95]
	ds_read_b128 v[180:183], v192 offset:46080
	v_rcp_f32_e32 v201, v201
	v_fma_f32 v200, v200, 2.0, -1.0
	v_mfma_f32_32x32x16_f16 v[64:79], a[76:79], v[184:187], v[64:79]
	ds_read_b128 v[184:187], v192 offset:47104
	v_rcp_f32_e32 v202, v202
	v_fma_f32 v201, v201, 2.0, -1.0
	v_mul_f32_e32 v216, v212, v200
	v_mfma_f32_32x32x16_f16 v[80:95], a[76:79], v[188:191], v[80:95]
	ds_read_b128 v[188:191], v192 offset:48128
	global_load_lds_dwordx4 v192, s[44:45] offset:2048 sc1
	v_rcp_f32_e32 v203, v203
	v_fma_f32 v202, v202, 2.0, -1.0
	v_mul_f32_e32 v217, v213, v201
	s_waitcnt lgkmcnt(4)
	v_mfma_f32_32x32x16_f16 v[64:79], a[80:83], v[160:163], v[64:79]
	ds_read_b128 v[160:163], v192 offset:49152
	v_fma_f32 v203, v203, 2.0, -1.0
	v_mul_f32_e32 v218, v214, v202
	v_exp_f32_e32 v200, v48
	v_mfma_f32_32x32x16_f16 v[80:95], a[80:83], v[164:167], v[80:95]
	ds_read_b128 v[164:167], v192 offset:50176
	v_mul_f32_e32 v219, v215, v203
	v_cvt_pk_f16_f32 v220, v216, v217
	v_exp_f32_e32 v201, v49
	v_mfma_f32_32x32x16_f16 v[64:79], a[84:87], v[168:171], v[64:79]
	ds_read_b128 v[168:171], v192 offset:51200
	v_cvt_pk_f16_f32 v221, v218, v219
	v_exp_f32_e32 v202, v50
	v_add_f32_e32 v200, 1.0, v200
	v_mfma_f32_32x32x16_f16 v[80:95], a[84:87], v[172:175], v[80:95]
	ds_read_b128 v[172:175], v192 offset:52224
	global_load_lds_dwordx4 v192, s[44:45] offset:3072 sc1
	s_cmp_lg_u32 s33, s60
	s_cbranch_scc1 .LE_nht34
	s_add_u32 s46, s62, 0x40000
	s_addc_u32 s47, s63, 0
	global_store_dwordx4 v250, v[216:219], s[46:47]
	s_waitcnt vmcnt(0)
.LE_nht34:
	v_exp_f32_e32 v203, v51
	s_waitcnt lgkmcnt(4)
	v_mfma_f32_32x32x16_f16 v[64:79], a[88:91], v[176:179], v[64:79]
	ds_read_b128 v[176:179], v192 offset:53248
	v_exp_f32_e32 v204, v52
	v_add_f32_e32 v201, 1.0, v201
	v_add_f32_e32 v202, 1.0, v202
	v_mfma_f32_32x32x16_f16 v[80:95], a[88:91], v[180:183], v[80:95]
	ds_read_b128 v[180:183], v192 offset:54272
	v_exp_f32_e32 v205, v53
	v_add_f32_e32 v203, 1.0, v203
	v_add_f32_e32 v204, 1.0, v204
	v_mfma_f32_32x32x16_f16 v[64:79], a[92:95], v[184:187], v[64:79]
	ds_read_b128 v[184:187], v192 offset:55296
	v_exp_f32_e32 v206, v54
	v_add_f32_e32 v205, 1.0, v205
	v_mfma_f32_32x32x16_f16 v[80:95], a[92:95], v[188:191], v[80:95]
	ds_read_b128 v[188:191], v192 offset:56320
	s_add_u32 s44, s34, 0x19000
	s_addc_u32 s45, s35, 0
	s_mov_b32 m0, s59
	s_nop 0
	global_load_lds_dwordx4 v192, s[44:45] sc1
	s_lshl_b32 s64, s71, 3
	s_add_u32 s64, s64, s29
	s_lshl_b32 s64, s64, 7
	s_add_u32 s38, s8, s64
	s_addc_u32 s39, s9, 0
	global_load_dword v251, v196, s[38:39] sc1
	v_exp_f32_e32 v207, v55
	v_add_f32_e32 v206, 1.0, v206
	s_waitcnt lgkmcnt(4)
	v_mfma_f32_32x32x16_f16 v[64:79], a[96:99], v[160:163], v[64:79]
	ds_read_b128 v[160:163], v192 offset:57344
	v_exp_f32_e32 v208, v56
	v_add_f32_e32 v207, 1.0, v207
	v_mfma_f32_32x32x16_f16 v[80:95], a[96:99], v[164:167], v[80:95]
	ds_read_b128 v[164:167], v192 offset:58368
	v_exp_f32_e32 v209, v57
	v_add_f32_e32 v208, 1.0, v208
	v_mfma_f32_32x32x16_f16 v[64:79], a[100:103], v[168:171], v[64:79]
	ds_read_b128 v[168:171], v192 offset:59392
	v_exp_f32_e32 v210, v58
	v_add_f32_e32 v209, 1.0, v209
	v_mfma_f32_32x32x16_f16 v[80:95], a[100:103], v[172:175], v[80:95]
	ds_read_b128 v[172:175], v192 offset:60416
	global_load_lds_dwordx4 v192, s[44:45] offset:1024 sc1
	v_exp_f32_e32 v211, v59
	v_add_f32_e32 v210, 1.0, v210
	s_waitcnt lgkmcnt(4)
	v_mfma_f32_32x32x16_f16 v[64:79], a[104:107], v[176:179], v[64:79]
	ds_read_b128 v[176:179], v192 offset:61440
	v_exp_f32_e32 v212, v60
	v_add_f32_e32 v211, 1.0, v211
	v_mfma_f32_32x32x16_f16 v[80:95], a[104:107], v[180:183], v[80:95]
	ds_read_b128 v[180:183], v192 offset:62464
	v_exp_f32_e32 v213, v61
	v_add_f32_e32 v212, 1.0, v212
	v_mfma_f32_32x32x16_f16 v[64:79], a[108:111], v[184:187], v[64:79]
	ds_read_b128 v[184:187], v192 offset:63488
	v_exp_f32_e32 v214, v62
	v_add_f32_e32 v213, 1.0, v213
	v_mfma_f32_32x32x16_f16 v[80:95], a[108:111], v[188:191], v[80:95]
	ds_read_b128 v[188:191], v192 offset:64512
	global_load_lds_dwordx4 v192, s[44:45] offset:2048 sc1
	v_exp_f32_e32 v215, v63
	v_add_f32_e32 v214, 1.0, v214
	s_waitcnt vmcnt(8)
	s_barrier
	s_waitcnt lgkmcnt(4)
	v_mfma_f32_32x32x16_f16 v[64:79], a[112:115], v[160:163], v[64:79]
	ds_read_b128 v[160:163], v193 offset:0
	v_add_f32_e32 v215, 1.0, v215
	v_rcp_f32_e32 v200, v200
	v_mfma_f32_32x32x16_f16 v[80:95], a[112:115], v[164:167], v[80:95]
	ds_read_b128 v[164:167], v193 offset:1024
	v_rcp_f32_e32 v201, v201
	v_mfma_f32_32x32x16_f16 v[64:79], a[116:119], v[168:171], v[64:79]
	ds_read_b128 v[168:171], v193 offset:2048
	v_rcp_f32_e32 v202, v202
	v_mfma_f32_32x32x16_f16 v[80:95], a[116:119], v[172:175], v[80:95]
	ds_read_b128 v[172:175], v193 offset:3072
	global_load_lds_dwordx4 v192, s[44:45] offset:3072 sc1
	v_rcp_f32_e32 v203, v203
	s_waitcnt lgkmcnt(4)
	v_mfma_f32_32x32x16_f16 v[64:79], a[120:123], v[176:179], v[64:79]
	ds_read_b128 v[176:179], v193 offset:4096
	v_rcp_f32_e32 v204, v204
	ds_read_b128 v[236:239], v248 offset:0
	ds_read_b64 v[240:241], v248 offset:32
	ds_read_b128 v[242:245], v248 offset:16
	ds_read_b64 v[246:247], v248 offset:40
	v_mfma_f32_32x32x16_f16 v[80:95], a[120:123], v[180:183], v[80:95]
	ds_read_b128 v[180:183], v193 offset:5120
	v_rcp_f32_e32 v205, v205
	v_mul_f32_e32 v204, v204, v140
	s_waitcnt lgkmcnt(3)
	v_fma_f32 v0, v229, v237, v240
	v_mfma_f32_32x32x16_f16 v[64:79], a[124:127], v[184:187], v[64:79]
	ds_read_b128 v[184:187], v193 offset:6144
	v_rcp_f32_e32 v206, v206
	v_mul_f32_e32 v205, v205, v141
	v_fma_f32 v1, v229, v239, v241
	v_fmac_f32_e32 v0, v228, v236
	v_mfma_f32_32x32x16_f16 v[80:95], a[124:127], v[188:191], v[80:95]
	ds_read_b128 v[188:191], v193 offset:7168
	s_waitcnt vmcnt(3)
	v_cmp_gt_u32_e32 vcc, 4, v251
	s_cbranch_vccz .LE_tok35

.LE_tok35:
	s_and_b32 s64, s71, 1
	s_lshl_b32 s64, s64, 22
	s_add_u32 s64, s64, s49
	s_add_u32 s64, s64, 0x60000
	s_add_u32 s34, s6, s64
	s_addc_u32 s35, s7, 0
	s_add_u32 s44, s34, 0x0
	s_addc_u32 s45, s35, 0
	s_mov_b32 m0, s52
	s_nop 0
	global_load_lds_dwordx4 v192, s[44:45] sc1
	v_rcp_f32_e32 v207, v207
	v_mul_f32_e32 v206, v206, v142
	v_fmac_f32_e32 v1, v228, v238
	v_fma_f32 v16, v231, v237, v240
	v_mfma_f32_32x32x16_f16 v[64:79], a[128:131], v[160:163], v[64:79]
	ds_read_b128 v[160:163], v193 offset:8192
	v_rcp_f32_e32 v208, v208
	v_mul_f32_e32 v207, v207, v143
	v_fma_f32 v17, v231, v239, v241
	v_fmac_f32_e32 v16, v230, v236
	v_mfma_f32_32x32x16_f16 v[80:95], a[128:131], v[164:167], v[80:95]
	ds_read_b128 v[164:167], v193 offset:9216
	v_rcp_f32_e32 v209, v209
	v_fmamk_f32 v208, v208, 0xc0b8aa3b, v198
	v_fmac_f32_e32 v17, v230, v238
	ds_read_b128 v[236:239], v248 offset:48
	ds_read_b64 v[240:241], v248 offset:80
	v_mfma_f32_32x32x16_f16 v[64:79], a[132:135], v[168:171], v[64:79]
	ds_read_b128 v[168:171], v193 offset:10240
	v_rcp_f32_e32 v210, v210
	v_fmamk_f32 v209, v209, 0xc0b8aa3b, v198
	v_fma_f32 v140, v200, v208, v204
	s_waitcnt lgkmcnt(8)
	v_fma_f32 v2, v229, v243, v246
	v_mfma_f32_32x32x16_f16 v[80:95], a[132:135], v[172:175], v[80:95]
	ds_read_b128 v[172:175], v193 offset:11264
	global_load_lds_dwordx4 v192, s[44:45] offset:1024 sc1
	v_rcp_f32_e32 v211, v211
	v_fmamk_f32 v210, v210, 0xc0b8aa3b, v198
	v_fma_f32 v141, v201, v209, v205
	v_fma_f32 v3, v229, v245, v247
	v_fmac_f32_e32 v2, v228, v242
	s_waitcnt lgkmcnt(6)
	v_mfma_f32_32x32x16_f16 v[64:79], a[136:139], v[176:179], v[64:79]
	ds_read_b128 v[176:179], v193 offset:12288
	v_rcp_f32_e32 v212, v212
	v_fmamk_f32 v211, v211, 0xc0b8aa3b, v198
	v_fma_f32 v142, v202, v210, v206
	v_fmac_f32_e32 v3, v228, v244
	v_fma_f32 v18, v231, v243, v246
	v_mfma_f32_32x32x16_f16 v[80:95], a[136:139], v[180:183], v[80:95]
	ds_read_b128 v[180:183], v193 offset:13312
	v_rcp_f32_e32 v213, v213
	v_fma_f32 v143, v203, v211, v207
	v_fma_f32 v19, v231, v245, v247
	v_fmac_f32_e32 v18, v230, v242
	v_mfma_f32_32x32x16_f16 v[64:79], a[140:143], v[184:187], v[64:79]
	ds_read_b128 v[184:187], v193 offset:14336
	v_rcp_f32_e32 v214, v214
	v_fmac_f32_e32 v19, v230, v244
	ds_read_b128 v[242:245], v248 offset:64
	ds_read_b64 v[246:247], v248 offset:88
	v_mfma_f32_32x32x16_f16 v[80:95], a[140:143], v[188:191], v[80:95]
	ds_read_b128 v[188:191], v193 offset:15360
	global_load_lds_dwordx4 v192, s[44:45] offset:2048 sc1
	v_rcp_f32_e32 v215, v215
	s_waitcnt lgkmcnt(8)
	v_fma_f32 v4, v229, v237, v240
	s_waitcnt lgkmcnt(6)
	v_mfma_f32_32x32x16_f16 v[64:79], a[144:147], v[160:163], v[64:79]
	ds_read_b128 v[160:163], v193 offset:16384
	v_exp_f32_e32 v200, v140
	v_fma_f32 v5, v229, v239, v241
	v_fmac_f32_e32 v4, v228, v236
	v_mfma_f32_32x32x16_f16 v[80:95], a[144:147], v[164:167], v[80:95]
	ds_read_b128 v[164:167], v193 offset:17408
	v_exp_f32_e32 v201, v141
	v_add_f32_e32 v200, 1.0, v200
	v_fmac_f32_e32 v5, v228, v238
	v_fma_f32 v20, v231, v237, v240
	v_mfma_f32_32x32x16_f16 v[64:79], a[148:151], v[168:171], v[64:79]
	ds_read_b128 v[168:171], v193 offset:18432
	v_exp_f32_e32 v202, v142
	v_add_f32_e32 v201, 1.0, v201
	v_fma_f32 v21, v231, v239, v241
	v_fmac_f32_e32 v20, v230, v236
	v_mfma_f32_32x32x16_f16 v[80:95], a[148:151], v[172:175], v[80:95]
	ds_read_b128 v[172:175], v193 offset:19456
	global_load_lds_dwordx4 v192, s[44:45] offset:3072 sc1
	v_exp_f32_e32 v203, v143
	v_add_f32_e32 v202, 1.0, v202
	v_fmac_f32_e32 v21, v230, v238
	ds_read_b128 v[236:239], v248 offset:96
	ds_read_b64 v[240:241], v248 offset:128
	s_waitcnt lgkmcnt(6)
	v_mfma_f32_32x32x16_f16 v[64:79], a[152:155], v[176:179], v[64:79]
	ds_read_b128 v[176:179], v193 offset:20480
	v_add_f32_e32 v203, 1.0, v203
	v_rcp_f32_e32 v200, v200
	v_fma_f32 v6, v229, v243, v246
	v_mfma_f32_32x32x16_f16 v[80:95], a[152:155], v[180:183], v[80:95]
	ds_read_b128 v[180:183], v193 offset:21504
	v_rcp_f32_e32 v201, v201
	v_fma_f32 v200, v200, 2.0, -1.0
	v_fma_f32 v7, v229, v245, v247
	v_fmac_f32_e32 v6, v228, v242
	v_mfma_f32_32x32x16_f16 v[64:79], a[156:159], v[184:187], v[64:79]
	ds_read_b128 v[184:187], v193 offset:22528
	v_rcp_f32_e32 v202, v202
	v_fma_f32 v201, v201, 2.0, -1.0
	v_mul_f32_e32 v216, v212, v200
	v_fmac_f32_e32 v7, v228, v244
	v_fma_f32 v22, v231, v243, v246
	v_mfma_f32_32x32x16_f16 v[80:95], a[156:159], v[188:191], v[80:95]
	ds_read_b128 v[188:191], v193 offset:23552
	s_add_u32 s44, s34, 0x1000
	s_addc_u32 s45, s35, 0
	s_mov_b32 m0, s53
	s_nop 0
	global_load_lds_dwordx4 v192, s[44:45] sc1
	v_rcp_f32_e32 v203, v203
	v_fma_f32 v202, v202, 2.0, -1.0
	v_mul_f32_e32 v217, v213, v201
	v_fma_f32 v23, v231, v245, v247
	v_fmac_f32_e32 v22, v230, v242
	s_waitcnt lgkmcnt(6)
	v_mfma_f32_32x32x16_f16 v[64:79], a[160:163], v[160:163], v[64:79]
	ds_read_b128 v[160:163], v193 offset:24576
	v_fma_f32 v203, v203, 2.0, -1.0
	v_mul_f32_e32 v218, v214, v202
	v_fmac_f32_e32 v23, v230, v244
	ds_read_b128 v[242:245], v248 offset:112
	ds_read_b64 v[246:247], v248 offset:136
	v_mfma_f32_32x32x16_f16 v[80:95], a[160:163], v[164:167], v[80:95]
	ds_read_b128 v[164:167], v193 offset:25600
	v_mul_f32_e32 v219, v215, v203
	v_cvt_pk_f16_f32 v222, v216, v217
	s_waitcnt lgkmcnt(8)
	v_fma_f32 v8, v229, v237, v240
	v_mfma_f32_32x32x16_f16 v[64:79], a[164:167], v[168:171], v[64:79]
	ds_read_b128 v[168:171], v193 offset:26624
	v_cvt_pk_f16_f32 v223, v218, v219
	v_fma_f32 v9, v229, v239, v241
	v_fmac_f32_e32 v8, v228, v236
	v_mfma_f32_32x32x16_f16 v[80:95], a[164:167], v[172:175], v[80:95]
	ds_read_b128 v[172:175], v193 offset:27648
	global_load_lds_dwordx4 v192, s[44:45] offset:1024 sc1
	s_cmp_lg_u32 s33, s60
	s_cbranch_scc1 .LE_nht37
	s_add_u32 s46, s62, 0x60000
	s_addc_u32 s47, s63, 0
	global_store_dwordx4 v250, v[216:219], s[46:47]
	s_waitcnt vmcnt(0)
.LE_nht37:
	v_fmac_f32_e32 v9, v228, v238
	v_fma_f32 v24, v231, v237, v240
	s_waitcnt lgkmcnt(6)
	v_mfma_f32_32x32x16_f16 v[64:79], a[168:171], v[176:179], v[64:79]
	ds_read_b128 v[176:179], v193 offset:28672
	s_nop 1
	v_permlane32_swap_b32_e32 v220, v222
	v_permlane32_swap_b32_e32 v221, v223
	s_cmp_eq_u32 s31, 0
	s_cbranch_scc1 .LE_slow38
	global_store_dwordx4 v195, v[220:223], s[36:37] offset:0
	s_branch .LE_join39

.LE_join39:
	v_fma_f32 v25, v231, v239, v241
	v_fmac_f32_e32 v24, v230, v236
	v_mfma_f32_32x32x16_f16 v[80:95], a[168:171], v[180:183], v[80:95]
	ds_read_b128 v[180:183], v193 offset:29696
	v_fmac_f32_e32 v25, v230, v238
	ds_read_b128 v[236:239], v248 offset:144
	ds_read_b64 v[240:241], v248 offset:176
	v_mfma_f32_32x32x16_f16 v[64:79], a[172:175], v[184:187], v[64:79]
	ds_read_b128 v[184:187], v193 offset:30720
	s_waitcnt lgkmcnt(8)
	v_fma_f32 v10, v229, v243, v246
	v_mfma_f32_32x32x16_f16 v[80:95], a[172:175], v[188:191], v[80:95]
	ds_read_b128 v[188:191], v193 offset:31744
	global_load_lds_dwordx4 v192, s[44:45] offset:2048 sc1
	v_fma_f32 v11, v229, v245, v247
	v_fmac_f32_e32 v10, v228, v242
	s_waitcnt vmcnt(8)
	s_barrier
	s_waitcnt lgkmcnt(6)
	v_mfma_f32_32x32x16_f16 v[64:79], a[176:179], v[160:163], v[64:79]
	ds_read_b128 v[160:163], v193 offset:32768
	v_fmac_f32_e32 v11, v228, v244
	v_fma_f32 v26, v231, v243, v246
	v_mfma_f32_32x32x16_f16 v[80:95], a[176:179], v[164:167], v[80:95]
	ds_read_b128 v[164:167], v193 offset:33792
	v_fma_f32 v27, v231, v245, v247
	v_fmac_f32_e32 v26, v230, v242
	v_mfma_f32_32x32x16_f16 v[64:79], a[180:183], v[168:171], v[64:79]
	ds_read_b128 v[168:171], v193 offset:34816
	v_fmac_f32_e32 v27, v230, v244
	ds_read_b128 v[242:245], v248 offset:160
	ds_read_b64 v[246:247], v248 offset:184
	v_mfma_f32_32x32x16_f16 v[80:95], a[180:183], v[172:175], v[80:95]
	ds_read_b128 v[172:175], v193 offset:35840
	global_load_lds_dwordx4 v192, s[44:45] offset:3072 sc1
	s_waitcnt lgkmcnt(8)
	v_fma_f32 v12, v229, v237, v240
	s_waitcnt lgkmcnt(6)
	v_mfma_f32_32x32x16_f16 v[64:79], a[184:187], v[176:179], v[64:79]
	ds_read_b128 v[176:179], v193 offset:36864
	v_fma_f32 v13, v229, v239, v241
	v_fmac_f32_e32 v12, v228, v236
	v_mfma_f32_32x32x16_f16 v[80:95], a[184:187], v[180:183], v[80:95]
	ds_read_b128 v[180:183], v193 offset:37888
	v_fmac_f32_e32 v13, v228, v238
	v_fma_f32 v28, v231, v237, v240
	v_mfma_f32_32x32x16_f16 v[64:79], a[188:191], v[184:187], v[64:79]
	ds_read_b128 v[184:187], v193 offset:38912
	v_fma_f32 v29, v231, v239, v241
	v_fmac_f32_e32 v28, v230, v236
	v_mfma_f32_32x32x16_f16 v[80:95], a[188:191], v[188:191], v[80:95]
	ds_read_b128 v[188:191], v193 offset:39936
	s_add_u32 s44, s34, 0x8000
	s_addc_u32 s45, s35, 0
	s_mov_b32 m0, s54
	s_nop 0
	global_load_lds_dwordx4 v192, s[44:45] sc1
	v_fmac_f32_e32 v29, v230, v238
	s_waitcnt lgkmcnt(5)
	s_waitcnt lgkmcnt(4)
	v_mfma_f32_32x32x16_f16 v[64:79], a[192:195], v[160:163], v[64:79]
	ds_read_b128 v[160:163], v193 offset:40960
	v_fma_f32 v14, v229, v243, v246
	v_fma_f32 v15, v229, v245, v247
	v_mfma_f32_32x32x16_f16 v[80:95], a[192:195], v[164:167], v[80:95]
	ds_read_b128 v[164:167], v193 offset:41984
	v_fmac_f32_e32 v14, v228, v242
	v_fmac_f32_e32 v15, v228, v244
	s_waitcnt vmcnt(3)
	s_barrier
	v_mov_b32_e32 v199, 2
	s_cmp_eq_u32 s31, 0
	s_cbranch_scc1 .LE_slow40
	global_store_dword v197, v199, s[40:41]
	s_branch .LE_join41

.LE_join41:
	v_mfma_f32_32x32x16_f16 v[64:79], a[196:199], v[168:171], v[64:79]
	ds_read_b128 v[168:171], v193 offset:43008
	v_fma_f32 v30, v231, v243, v246
	v_fma_f32 v31, v231, v245, v247
	v_mfma_f32_32x32x16_f16 v[80:95], a[196:199], v[172:175], v[80:95]
	ds_read_b128 v[172:175], v193 offset:44032
	global_load_lds_dwordx4 v192, s[44:45] offset:1024 sc1
	v_fmac_f32_e32 v30, v230, v242
	v_fmac_f32_e32 v31, v230, v244
	s_waitcnt lgkmcnt(4)
	v_mfma_f32_32x32x16_f16 v[64:79], a[200:203], v[176:179], v[64:79]
	ds_read_b128 v[176:179], v193 offset:45056
	v_mfma_f32_32x32x16_f16 v[80:95], a[200:203], v[180:183], v[80:95]
	ds_read_b128 v[180:183], v193 offset:46080
	v_mfma_f32_32x32x16_f16 v[64:79], a[204:207], v[184:187], v[64:79]
	ds_read_b128 v[184:187], v193 offset:47104
	v_mfma_f32_32x32x16_f16 v[80:95], a[204:207], v[188:191], v[80:95]
	ds_read_b128 v[188:191], v193 offset:48128
	global_load_lds_dwordx4 v192, s[44:45] offset:2048 sc1
	s_waitcnt lgkmcnt(4)
	v_mfma_f32_32x32x16_f16 v[64:79], a[208:211], v[160:163], v[64:79]
	ds_read_b128 v[160:163], v193 offset:49152
	v_mfma_f32_32x32x16_f16 v[80:95], a[208:211], v[164:167], v[80:95]
	ds_read_b128 v[164:167], v193 offset:50176
	v_mfma_f32_32x32x16_f16 v[64:79], a[212:215], v[168:171], v[64:79]
	ds_read_b128 v[168:171], v193 offset:51200
	v_mfma_f32_32x32x16_f16 v[80:95], a[212:215], v[172:175], v[80:95]
	ds_read_b128 v[172:175], v193 offset:52224
	global_load_lds_dwordx4 v192, s[44:45] offset:3072 sc1
	s_waitcnt lgkmcnt(4)
	v_mfma_f32_32x32x16_f16 v[64:79], a[216:219], v[176:179], v[64:79]
	ds_read_b128 v[176:179], v193 offset:53248
	v_mfma_f32_32x32x16_f16 v[80:95], a[216:219], v[180:183], v[80:95]
	ds_read_b128 v[180:183], v193 offset:54272
	v_mfma_f32_32x32x16_f16 v[64:79], a[220:223], v[184:187], v[64:79]
	ds_read_b128 v[184:187], v193 offset:55296
	v_mfma_f32_32x32x16_f16 v[80:95], a[220:223], v[188:191], v[80:95]
	ds_read_b128 v[188:191], v193 offset:56320
	s_add_u32 s44, s34, 0x9000
	s_addc_u32 s45, s35, 0
	s_mov_b32 m0, s55
	s_nop 0
	global_load_lds_dwordx4 v192, s[44:45] sc1
	s_waitcnt lgkmcnt(4)
	v_mfma_f32_32x32x16_f16 v[64:79], a[224:227], v[160:163], v[64:79]
	ds_read_b128 v[160:163], v193 offset:57344
	v_mfma_f32_32x32x16_f16 v[80:95], a[224:227], v[164:167], v[80:95]
	ds_read_b128 v[164:167], v193 offset:58368
	v_mfma_f32_32x32x16_f16 v[64:79], a[228:231], v[168:171], v[64:79]
	ds_read_b128 v[168:171], v193 offset:59392
	v_mfma_f32_32x32x16_f16 v[80:95], a[228:231], v[172:175], v[80:95]
	ds_read_b128 v[172:175], v193 offset:60416
	global_load_lds_dwordx4 v192, s[44:45] offset:1024 sc1
	s_waitcnt lgkmcnt(4)
	v_mfma_f32_32x32x16_f16 v[64:79], a[232:235], v[176:179], v[64:79]
	ds_read_b128 v[176:179], v193 offset:61440
	v_mfma_f32_32x32x16_f16 v[80:95], a[232:235], v[180:183], v[80:95]
	ds_read_b128 v[180:183], v193 offset:62464
	v_mfma_f32_32x32x16_f16 v[64:79], a[236:239], v[184:187], v[64:79]
	ds_read_b128 v[184:187], v193 offset:63488
	v_mfma_f32_32x32x16_f16 v[80:95], a[236:239], v[188:191], v[80:95]
	ds_read_b128 v[188:191], v193 offset:64512
	global_load_lds_dwordx4 v192, s[44:45] offset:2048 sc1
	s_waitcnt vmcnt(8)
	s_barrier
	s_waitcnt lgkmcnt(4)
	v_mfma_f32_32x32x16_f16 v[64:79], a[240:243], v[160:163], v[64:79]
	ds_read_b128 v[160:163], v192 offset:0
	v_mfma_f32_32x32x16_f16 v[80:95], a[240:243], v[164:167], v[80:95]
	ds_read_b128 v[164:167], v192 offset:1024
	v_mfma_f32_32x32x16_f16 v[64:79], a[244:247], v[168:171], v[64:79]
	ds_read_b128 v[168:171], v192 offset:2048
	v_mfma_f32_32x32x16_f16 v[80:95], a[244:247], v[172:175], v[80:95]
	ds_read_b128 v[172:175], v192 offset:3072
	global_load_lds_dwordx4 v192, s[44:45] offset:3072 sc1
	s_waitcnt lgkmcnt(4)
	v_mfma_f32_32x32x16_f16 v[64:79], a[248:251], v[176:179], v[64:79]
	ds_read_b128 v[176:179], v192 offset:4096
	v_mfma_f32_32x32x16_f16 v[80:95], a[248:251], v[180:183], v[80:95]
	ds_read_b128 v[180:183], v192 offset:5120
	v_mfma_f32_32x32x16_f16 v[64:79], a[252:255], v[184:187], v[64:79]
	ds_read_b128 v[184:187], v192 offset:6144
	v_mfma_f32_32x32x16_f16 v[80:95], a[252:255], v[188:191], v[80:95]
	ds_read_b128 v[188:191], v192 offset:7168
	s_add_u32 s44, s34, 0x10000
	s_addc_u32 s45, s35, 0
	s_mov_b32 m0, s56
	s_nop 0
	global_load_lds_dwordx4 v192, s[44:45] sc1
	s_and_b32 s64, s33, 1
	s_lshl_b32 s64, s64, 22
	s_add_u32 s64, s64, s50
	s_add_u32 s64, s64, 0x40000
	s_add_u32 s36, s6, s64
	s_addc_u32 s37, s7, 0
	s_lshl_b32 s64, s33, 3
	s_add_u32 s64, s64, s29
	s_lshl_b32 s64, s64, 5
	s_add_u32 s64, s64, s30
	s_lshl_b32 s64, s64, 2
	s_add_u32 s40, s8, s64
	s_addc_u32 s41, s9, 0
	s_lshl_b32 s64, s61, 11
	s_lshl_b32 s65, s29, 8
	s_add_u32 s64, s64, s65
	s_add_u32 s64, s64, 64
	s_lshl_b32 s64, s64, 3
	s_add_u32 s42, s12, s64
	s_addc_u32 s43, s13, 0
	s_nop 3
	global_load_dwordx2 v[228:229], v249, s[42:43] offset:0
	global_load_dwordx2 v[230:231], v249, s[42:43] offset:256
	s_waitcnt lgkmcnt(4)
	v_mfma_f32_32x32x16_f16 v[96:111], a[0:3], v[160:163], v[96:111]
	ds_read_b128 v[160:163], v192 offset:8192
	v_exp_f32_e32 v200, v64
	v_mfma_f32_32x32x16_f16 v[112:127], a[0:3], v[164:167], v[112:127]
	ds_read_b128 v[164:167], v192 offset:9216
	v_exp_f32_e32 v201, v65
	v_add_f32_e32 v200, 1.0, v200
	v_mfma_f32_32x32x16_f16 v[96:111], a[4:7], v[168:171], v[96:111]
	ds_read_b128 v[168:171], v192 offset:10240
	v_exp_f32_e32 v202, v66
	v_add_f32_e32 v201, 1.0, v201
	v_mfma_f32_32x32x16_f16 v[112:127], a[4:7], v[172:175], v[112:127]
	ds_read_b128 v[172:175], v192 offset:11264
	global_load_lds_dwordx4 v192, s[44:45] offset:1024 sc1
	v_exp_f32_e32 v203, v67
	v_add_f32_e32 v202, 1.0, v202
	s_waitcnt lgkmcnt(4)
	v_mfma_f32_32x32x16_f16 v[96:111], a[8:11], v[176:179], v[96:111]
	ds_read_b128 v[176:179], v192 offset:12288
	v_exp_f32_e32 v204, v68
	v_add_f32_e32 v203, 1.0, v203
	v_mfma_f32_32x32x16_f16 v[112:127], a[8:11], v[180:183], v[112:127]
	ds_read_b128 v[180:183], v192 offset:13312
	v_exp_f32_e32 v205, v69
	v_add_f32_e32 v204, 1.0, v204
	v_mfma_f32_32x32x16_f16 v[96:111], a[12:15], v[184:187], v[96:111]
	ds_read_b128 v[184:187], v192 offset:14336
	v_exp_f32_e32 v206, v70
	v_add_f32_e32 v205, 1.0, v205
	v_mfma_f32_32x32x16_f16 v[112:127], a[12:15], v[188:191], v[112:127]
	ds_read_b128 v[188:191], v192 offset:15360
	global_load_lds_dwordx4 v192, s[44:45] offset:2048 sc1
	v_exp_f32_e32 v207, v71
	v_add_f32_e32 v206, 1.0, v206
	s_waitcnt lgkmcnt(4)
	v_mfma_f32_32x32x16_f16 v[96:111], a[16:19], v[160:163], v[96:111]
	ds_read_b128 v[160:163], v192 offset:16384
	v_exp_f32_e32 v208, v72
	v_add_f32_e32 v207, 1.0, v207
	v_mfma_f32_32x32x16_f16 v[112:127], a[16:19], v[164:167], v[112:127]
	ds_read_b128 v[164:167], v192 offset:17408
	v_exp_f32_e32 v209, v73
	v_add_f32_e32 v208, 1.0, v208
	v_mfma_f32_32x32x16_f16 v[96:111], a[20:23], v[168:171], v[96:111]
	ds_read_b128 v[168:171], v192 offset:18432
	v_exp_f32_e32 v210, v74
	v_add_f32_e32 v209, 1.0, v209
	v_mfma_f32_32x32x16_f16 v[112:127], a[20:23], v[172:175], v[112:127]
	ds_read_b128 v[172:175], v192 offset:19456
	global_load_lds_dwordx4 v192, s[44:45] offset:3072 sc1
	v_exp_f32_e32 v211, v75
	v_add_f32_e32 v210, 1.0, v210
	s_waitcnt lgkmcnt(4)
	v_mfma_f32_32x32x16_f16 v[96:111], a[24:27], v[176:179], v[96:111]
	ds_read_b128 v[176:179], v192 offset:20480
	v_exp_f32_e32 v212, v76
	v_add_f32_e32 v211, 1.0, v211
	v_mfma_f32_32x32x16_f16 v[112:127], a[24:27], v[180:183], v[112:127]
	ds_read_b128 v[180:183], v192 offset:21504
	v_exp_f32_e32 v213, v77
	v_add_f32_e32 v212, 1.0, v212
	v_mfma_f32_32x32x16_f16 v[96:111], a[28:31], v[184:187], v[96:111]
	ds_read_b128 v[184:187], v192 offset:22528
	v_exp_f32_e32 v214, v78
	v_add_f32_e32 v213, 1.0, v213
	v_mfma_f32_32x32x16_f16 v[112:127], a[28:31], v[188:191], v[112:127]
	ds_read_b128 v[188:191], v192 offset:23552
	s_add_u32 s44, s34, 0x11000
	s_addc_u32 s45, s35, 0
	s_mov_b32 m0, s57
	s_nop 0
	global_load_lds_dwordx4 v192, s[44:45] sc1
	v_exp_f32_e32 v215, v79
	v_add_f32_e32 v214, 1.0, v214
	s_waitcnt lgkmcnt(4)
	v_mfma_f32_32x32x16_f16 v[96:111], a[32:35], v[160:163], v[96:111]
	ds_read_b128 v[160:163], v192 offset:24576
	v_add_f32_e32 v215, 1.0, v215
	v_rcp_f32_e32 v200, v200
	v_mfma_f32_32x32x16_f16 v[112:127], a[32:35], v[164:167], v[112:127]
	ds_read_b128 v[164:167], v192 offset:25600
	v_rcp_f32_e32 v201, v201
	v_mfma_f32_32x32x16_f16 v[96:111], a[36:39], v[168:171], v[96:111]
	ds_read_b128 v[168:171], v192 offset:26624
	v_rcp_f32_e32 v202, v202
	v_mfma_f32_32x32x16_f16 v[112:127], a[36:39], v[172:175], v[112:127]
	ds_read_b128 v[172:175], v192 offset:27648
	global_load_lds_dwordx4 v192, s[44:45] offset:1024 sc1
	v_rcp_f32_e32 v203, v203
	s_waitcnt lgkmcnt(4)
	v_mfma_f32_32x32x16_f16 v[96:111], a[40:43], v[176:179], v[96:111]
	ds_read_b128 v[176:179], v192 offset:28672
	v_rcp_f32_e32 v204, v204
	v_mfma_f32_32x32x16_f16 v[112:127], a[40:43], v[180:183], v[112:127]
	ds_read_b128 v[180:183], v192 offset:29696
	v_rcp_f32_e32 v205, v205
	v_mul_f32_e32 v204, v204, v144
	v_mfma_f32_32x32x16_f16 v[96:111], a[44:47], v[184:187], v[96:111]
	ds_read_b128 v[184:187], v192 offset:30720
	v_rcp_f32_e32 v206, v206
	v_mul_f32_e32 v205, v205, v145
	v_mfma_f32_32x32x16_f16 v[112:127], a[44:47], v[188:191], v[112:127]
	ds_read_b128 v[188:191], v192 offset:31744
	global_load_lds_dwordx4 v192, s[44:45] offset:2048 sc1
	v_rcp_f32_e32 v207, v207
	v_mul_f32_e32 v206, v206, v146
	s_waitcnt vmcnt(9)
	s_barrier
	s_waitcnt lgkmcnt(4)
	v_mfma_f32_32x32x16_f16 v[96:111], a[48:51], v[160:163], v[96:111]
	ds_read_b128 v[160:163], v192 offset:32768
	v_rcp_f32_e32 v208, v208
	v_mul_f32_e32 v207, v207, v147
	v_mfma_f32_32x32x16_f16 v[112:127], a[48:51], v[164:167], v[112:127]
	ds_read_b128 v[164:167], v192 offset:33792
	v_rcp_f32_e32 v209, v209
	v_fmamk_f32 v208, v208, 0xc0b8aa3b, v198
	v_mfma_f32_32x32x16_f16 v[96:111], a[52:55], v[168:171], v[96:111]
	ds_read_b128 v[168:171], v192 offset:34816
	v_rcp_f32_e32 v210, v210
	v_fmamk_f32 v209, v209, 0xc0b8aa3b, v198
	v_fma_f32 v144, v200, v208, v204
	v_mfma_f32_32x32x16_f16 v[112:127], a[52:55], v[172:175], v[112:127]
	ds_read_b128 v[172:175], v192 offset:35840
	global_load_lds_dwordx4 v192, s[44:45] offset:3072 sc1
	v_rcp_f32_e32 v211, v211
	v_fmamk_f32 v210, v210, 0xc0b8aa3b, v198
	v_fma_f32 v145, v201, v209, v205
	s_waitcnt lgkmcnt(4)
	v_mfma_f32_32x32x16_f16 v[96:111], a[56:59], v[176:179], v[96:111]
	ds_read_b128 v[176:179], v192 offset:36864
	v_rcp_f32_e32 v212, v212
	v_fmamk_f32 v211, v211, 0xc0b8aa3b, v198
	v_fma_f32 v146, v202, v210, v206
	v_mfma_f32_32x32x16_f16 v[112:127], a[56:59], v[180:183], v[112:127]
	ds_read_b128 v[180:183], v192 offset:37888
	v_rcp_f32_e32 v213, v213
	v_fma_f32 v147, v203, v211, v207
	v_mfma_f32_32x32x16_f16 v[96:111], a[60:63], v[184:187], v[96:111]
	ds_read_b128 v[184:187], v192 offset:38912
	v_rcp_f32_e32 v214, v214
	v_mfma_f32_32x32x16_f16 v[112:127], a[60:63], v[188:191], v[112:127]
	ds_read_b128 v[188:191], v192 offset:39936
	s_add_u32 s44, s34, 0x18000
	s_addc_u32 s45, s35, 0
	s_mov_b32 m0, s58
	s_nop 0
	global_load_lds_dwordx4 v192, s[44:45] sc1
	v_rcp_f32_e32 v215, v215
	s_waitcnt lgkmcnt(4)
	v_mfma_f32_32x32x16_f16 v[96:111], a[64:67], v[160:163], v[96:111]
	ds_read_b128 v[160:163], v192 offset:40960
	v_exp_f32_e32 v200, v144
	v_mfma_f32_32x32x16_f16 v[112:127], a[64:67], v[164:167], v[112:127]
	ds_read_b128 v[164:167], v192 offset:41984
	v_exp_f32_e32 v201, v145
	v_add_f32_e32 v200, 1.0, v200
	v_mfma_f32_32x32x16_f16 v[96:111], a[68:71], v[168:171], v[96:111]
	ds_read_b128 v[168:171], v192 offset:43008
	v_exp_f32_e32 v202, v146
	v_add_f32_e32 v201, 1.0, v201
	v_mfma_f32_32x32x16_f16 v[112:127], a[68:71], v[172:175], v[112:127]
	ds_read_b128 v[172:175], v192 offset:44032
	global_load_lds_dwordx4 v192, s[44:45] offset:1024 sc1
	v_exp_f32_e32 v203, v147
	v_add_f32_e32 v202, 1.0, v202
	s_waitcnt lgkmcnt(4)
	v_mfma_f32_32x32x16_f16 v[96:111], a[72:75], v[176:179], v[96:111]
	ds_read_b128 v[176:179], v192 offset:45056
	v_add_f32_e32 v203, 1.0, v203
	v_rcp_f32_e32 v200, v200
	v_mfma_f32_32x32x16_f16 v[112:127], a[72:75], v[180:183], v[112:127]
	ds_read_b128 v[180:183], v192 offset:46080
	v_rcp_f32_e32 v201, v201
	v_fma_f32 v200, v200, 2.0, -1.0
	v_mfma_f32_32x32x16_f16 v[96:111], a[76:79], v[184:187], v[96:111]
	ds_read_b128 v[184:187], v192 offset:47104
	v_rcp_f32_e32 v202, v202
	v_fma_f32 v201, v201, 2.0, -1.0
	v_mul_f32_e32 v216, v212, v200
	v_mfma_f32_32x32x16_f16 v[112:127], a[76:79], v[188:191], v[112:127]
	ds_read_b128 v[188:191], v192 offset:48128
	global_load_lds_dwordx4 v192, s[44:45] offset:2048 sc1
	v_rcp_f32_e32 v203, v203
	v_fma_f32 v202, v202, 2.0, -1.0
	v_mul_f32_e32 v217, v213, v201
	s_waitcnt lgkmcnt(4)
	v_mfma_f32_32x32x16_f16 v[96:111], a[80:83], v[160:163], v[96:111]
	ds_read_b128 v[160:163], v192 offset:49152
	v_fma_f32 v203, v203, 2.0, -1.0
	v_mul_f32_e32 v218, v214, v202
	v_exp_f32_e32 v200, v80
	v_mfma_f32_32x32x16_f16 v[112:127], a[80:83], v[164:167], v[112:127]
	ds_read_b128 v[164:167], v192 offset:50176
	v_mul_f32_e32 v219, v215, v203
	v_cvt_pk_f16_f32 v220, v216, v217
	v_exp_f32_e32 v201, v81
	v_mfma_f32_32x32x16_f16 v[96:111], a[84:87], v[168:171], v[96:111]
	ds_read_b128 v[168:171], v192 offset:51200
	v_cvt_pk_f16_f32 v221, v218, v219
	v_exp_f32_e32 v202, v82
	v_add_f32_e32 v200, 1.0, v200
	v_mfma_f32_32x32x16_f16 v[112:127], a[84:87], v[172:175], v[112:127]
	ds_read_b128 v[172:175], v192 offset:52224
	global_load_lds_dwordx4 v192, s[44:45] offset:3072 sc1
	s_cmp_lg_u32 s33, s60
	s_cbranch_scc1 .LE_nht42
	s_add_u32 s46, s62, 0x80000
	s_addc_u32 s47, s63, 0
	global_store_dwordx4 v250, v[216:219], s[46:47]
	s_waitcnt vmcnt(0)
.LE_nht42:
	v_exp_f32_e32 v203, v83
	s_waitcnt lgkmcnt(4)
	v_mfma_f32_32x32x16_f16 v[96:111], a[88:91], v[176:179], v[96:111]
	ds_read_b128 v[176:179], v192 offset:53248
	v_exp_f32_e32 v204, v84
	v_add_f32_e32 v201, 1.0, v201
	v_add_f32_e32 v202, 1.0, v202
	v_mfma_f32_32x32x16_f16 v[112:127], a[88:91], v[180:183], v[112:127]
	ds_read_b128 v[180:183], v192 offset:54272
	v_exp_f32_e32 v205, v85
	v_add_f32_e32 v203, 1.0, v203
	v_add_f32_e32 v204, 1.0, v204
	v_mfma_f32_32x32x16_f16 v[96:111], a[92:95], v[184:187], v[96:111]
	ds_read_b128 v[184:187], v192 offset:55296
	v_exp_f32_e32 v206, v86
	v_add_f32_e32 v205, 1.0, v205
	v_mfma_f32_32x32x16_f16 v[112:127], a[92:95], v[188:191], v[112:127]
	ds_read_b128 v[188:191], v192 offset:56320
	s_add_u32 s44, s34, 0x19000
	s_addc_u32 s45, s35, 0
	s_mov_b32 m0, s59
	s_nop 0
	global_load_lds_dwordx4 v192, s[44:45] sc1
	s_lshl_b32 s64, s33, 3
	s_add_u32 s64, s64, s29
	s_lshl_b32 s64, s64, 7
	s_add_u32 s38, s8, s64
	s_addc_u32 s39, s9, 0
	global_load_dword v251, v196, s[38:39] sc1
	v_exp_f32_e32 v207, v87
	v_add_f32_e32 v206, 1.0, v206
	s_waitcnt lgkmcnt(4)
	v_mfma_f32_32x32x16_f16 v[96:111], a[96:99], v[160:163], v[96:111]
	ds_read_b128 v[160:163], v192 offset:57344
	v_exp_f32_e32 v208, v88
	v_add_f32_e32 v207, 1.0, v207
	v_mfma_f32_32x32x16_f16 v[112:127], a[96:99], v[164:167], v[112:127]
	ds_read_b128 v[164:167], v192 offset:58368
	v_exp_f32_e32 v209, v89
	v_add_f32_e32 v208, 1.0, v208
	v_mfma_f32_32x32x16_f16 v[96:111], a[100:103], v[168:171], v[96:111]
	ds_read_b128 v[168:171], v192 offset:59392
	v_exp_f32_e32 v210, v90
	v_add_f32_e32 v209, 1.0, v209
	v_mfma_f32_32x32x16_f16 v[112:127], a[100:103], v[172:175], v[112:127]
	ds_read_b128 v[172:175], v192 offset:60416
	global_load_lds_dwordx4 v192, s[44:45] offset:1024 sc1
	v_exp_f32_e32 v211, v91
	v_add_f32_e32 v210, 1.0, v210
	s_waitcnt lgkmcnt(4)
	v_mfma_f32_32x32x16_f16 v[96:111], a[104:107], v[176:179], v[96:111]
	ds_read_b128 v[176:179], v192 offset:61440
	v_exp_f32_e32 v212, v92
	v_add_f32_e32 v211, 1.0, v211
	v_mfma_f32_32x32x16_f16 v[112:127], a[104:107], v[180:183], v[112:127]
	ds_read_b128 v[180:183], v192 offset:62464
	v_exp_f32_e32 v213, v93
	v_add_f32_e32 v212, 1.0, v212
	v_mfma_f32_32x32x16_f16 v[96:111], a[108:111], v[184:187], v[96:111]
	ds_read_b128 v[184:187], v192 offset:63488
	v_exp_f32_e32 v214, v94
	v_add_f32_e32 v213, 1.0, v213
	v_mfma_f32_32x32x16_f16 v[112:127], a[108:111], v[188:191], v[112:127]
	ds_read_b128 v[188:191], v192 offset:64512
	global_load_lds_dwordx4 v192, s[44:45] offset:2048 sc1
	v_exp_f32_e32 v215, v95
	v_add_f32_e32 v214, 1.0, v214
	s_waitcnt vmcnt(8)
	s_barrier
	s_waitcnt lgkmcnt(4)
	v_mfma_f32_32x32x16_f16 v[96:111], a[112:115], v[160:163], v[96:111]
	ds_read_b128 v[160:163], v193 offset:0
	v_add_f32_e32 v215, 1.0, v215
	v_rcp_f32_e32 v200, v200
	v_mfma_f32_32x32x16_f16 v[112:127], a[112:115], v[164:167], v[112:127]
	ds_read_b128 v[164:167], v193 offset:1024
	v_rcp_f32_e32 v201, v201
	v_mfma_f32_32x32x16_f16 v[96:111], a[116:119], v[168:171], v[96:111]
	ds_read_b128 v[168:171], v193 offset:2048
	v_rcp_f32_e32 v202, v202
	v_mfma_f32_32x32x16_f16 v[112:127], a[116:119], v[172:175], v[112:127]
	ds_read_b128 v[172:175], v193 offset:3072
	global_load_lds_dwordx4 v192, s[44:45] offset:3072 sc1
	v_rcp_f32_e32 v203, v203
	s_waitcnt lgkmcnt(4)
	v_mfma_f32_32x32x16_f16 v[96:111], a[120:123], v[176:179], v[96:111]
	ds_read_b128 v[176:179], v193 offset:4096
	v_rcp_f32_e32 v204, v204
	ds_read_b128 v[236:239], v248 offset:0
	ds_read_b64 v[240:241], v248 offset:32
	ds_read_b128 v[242:245], v248 offset:16
	ds_read_b64 v[246:247], v248 offset:40
	v_mfma_f32_32x32x16_f16 v[112:127], a[120:123], v[180:183], v[112:127]
	ds_read_b128 v[180:183], v193 offset:5120
	v_rcp_f32_e32 v205, v205
	v_mul_f32_e32 v204, v204, v148
	s_waitcnt lgkmcnt(3)
	v_fma_f32 v32, v229, v237, v240
	v_mfma_f32_32x32x16_f16 v[96:111], a[124:127], v[184:187], v[96:111]
	ds_read_b128 v[184:187], v193 offset:6144
	v_rcp_f32_e32 v206, v206
	v_mul_f32_e32 v205, v205, v149
	v_fma_f32 v33, v229, v239, v241
	v_fmac_f32_e32 v32, v228, v236
	v_mfma_f32_32x32x16_f16 v[112:127], a[124:127], v[188:191], v[112:127]
	ds_read_b128 v[188:191], v193 offset:7168
	s_waitcnt vmcnt(3)
	v_cmp_gt_u32_e32 vcc, 1, v251
	s_cbranch_vccz .LE_tok43

.LE_tok43:
	s_and_b32 s64, s33, 1
	s_lshl_b32 s64, s64, 22
	s_add_u32 s64, s64, s49
	s_add_u32 s34, s6, s64
	s_addc_u32 s35, s7, 0
	s_add_u32 s44, s34, 0x0
	s_addc_u32 s45, s35, 0
	s_mov_b32 m0, s52
	s_nop 0
	global_load_lds_dwordx4 v192, s[44:45] sc1
	v_rcp_f32_e32 v207, v207
	v_mul_f32_e32 v206, v206, v150
	v_fmac_f32_e32 v33, v228, v238
	v_fma_f32 v48, v231, v237, v240
	v_mfma_f32_32x32x16_f16 v[96:111], a[128:131], v[160:163], v[96:111]
	ds_read_b128 v[160:163], v193 offset:8192
	v_rcp_f32_e32 v208, v208
	v_mul_f32_e32 v207, v207, v151
	v_fma_f32 v49, v231, v239, v241
	v_fmac_f32_e32 v48, v230, v236
	v_mfma_f32_32x32x16_f16 v[112:127], a[128:131], v[164:167], v[112:127]
	ds_read_b128 v[164:167], v193 offset:9216
	v_rcp_f32_e32 v209, v209
	v_fmamk_f32 v208, v208, 0xc0b8aa3b, v198
	v_fmac_f32_e32 v49, v230, v238
	ds_read_b128 v[236:239], v248 offset:48
	ds_read_b64 v[240:241], v248 offset:80
	v_mfma_f32_32x32x16_f16 v[96:111], a[132:135], v[168:171], v[96:111]
	ds_read_b128 v[168:171], v193 offset:10240
	v_rcp_f32_e32 v210, v210
	v_fmamk_f32 v209, v209, 0xc0b8aa3b, v198
	v_fma_f32 v148, v200, v208, v204
	s_waitcnt lgkmcnt(8)
	v_fma_f32 v34, v229, v243, v246
	v_mfma_f32_32x32x16_f16 v[112:127], a[132:135], v[172:175], v[112:127]
	ds_read_b128 v[172:175], v193 offset:11264
	global_load_lds_dwordx4 v192, s[44:45] offset:1024 sc1
	v_rcp_f32_e32 v211, v211
	v_fmamk_f32 v210, v210, 0xc0b8aa3b, v198
	v_fma_f32 v149, v201, v209, v205
	v_fma_f32 v35, v229, v245, v247
	v_fmac_f32_e32 v34, v228, v242
	s_waitcnt lgkmcnt(6)
	v_mfma_f32_32x32x16_f16 v[96:111], a[136:139], v[176:179], v[96:111]
	ds_read_b128 v[176:179], v193 offset:12288
	v_rcp_f32_e32 v212, v212
	v_fmamk_f32 v211, v211, 0xc0b8aa3b, v198
	v_fma_f32 v150, v202, v210, v206
	v_fmac_f32_e32 v35, v228, v244
	v_fma_f32 v50, v231, v243, v246
	v_mfma_f32_32x32x16_f16 v[112:127], a[136:139], v[180:183], v[112:127]
	ds_read_b128 v[180:183], v193 offset:13312
	v_rcp_f32_e32 v213, v213
	v_fma_f32 v151, v203, v211, v207
	v_fma_f32 v51, v231, v245, v247
	v_fmac_f32_e32 v50, v230, v242
	v_mfma_f32_32x32x16_f16 v[96:111], a[140:143], v[184:187], v[96:111]
	ds_read_b128 v[184:187], v193 offset:14336
	v_rcp_f32_e32 v214, v214
	v_fmac_f32_e32 v51, v230, v244
	ds_read_b128 v[242:245], v248 offset:64
	ds_read_b64 v[246:247], v248 offset:88
	v_mfma_f32_32x32x16_f16 v[112:127], a[140:143], v[188:191], v[112:127]
	ds_read_b128 v[188:191], v193 offset:15360
	global_load_lds_dwordx4 v192, s[44:45] offset:2048 sc1
	v_rcp_f32_e32 v215, v215
	s_waitcnt lgkmcnt(8)
	v_fma_f32 v36, v229, v237, v240
	s_waitcnt lgkmcnt(6)
	v_mfma_f32_32x32x16_f16 v[96:111], a[144:147], v[160:163], v[96:111]
	ds_read_b128 v[160:163], v193 offset:16384
	v_exp_f32_e32 v200, v148
	v_fma_f32 v37, v229, v239, v241
	v_fmac_f32_e32 v36, v228, v236
	v_mfma_f32_32x32x16_f16 v[112:127], a[144:147], v[164:167], v[112:127]
	ds_read_b128 v[164:167], v193 offset:17408
	v_exp_f32_e32 v201, v149
	v_add_f32_e32 v200, 1.0, v200
	v_fmac_f32_e32 v37, v228, v238
	v_fma_f32 v52, v231, v237, v240
	v_mfma_f32_32x32x16_f16 v[96:111], a[148:151], v[168:171], v[96:111]
	ds_read_b128 v[168:171], v193 offset:18432
	v_exp_f32_e32 v202, v150
	v_add_f32_e32 v201, 1.0, v201
	v_fma_f32 v53, v231, v239, v241
	v_fmac_f32_e32 v52, v230, v236
	v_mfma_f32_32x32x16_f16 v[112:127], a[148:151], v[172:175], v[112:127]
	ds_read_b128 v[172:175], v193 offset:19456
	global_load_lds_dwordx4 v192, s[44:45] offset:3072 sc1
	v_exp_f32_e32 v203, v151
	v_add_f32_e32 v202, 1.0, v202
	v_fmac_f32_e32 v53, v230, v238
	ds_read_b128 v[236:239], v248 offset:96
	ds_read_b64 v[240:241], v248 offset:128
	s_waitcnt lgkmcnt(6)
	v_mfma_f32_32x32x16_f16 v[96:111], a[152:155], v[176:179], v[96:111]
	ds_read_b128 v[176:179], v193 offset:20480
	v_add_f32_e32 v203, 1.0, v203
	v_rcp_f32_e32 v200, v200
	v_fma_f32 v38, v229, v243, v246
	v_mfma_f32_32x32x16_f16 v[112:127], a[152:155], v[180:183], v[112:127]
	ds_read_b128 v[180:183], v193 offset:21504
	v_rcp_f32_e32 v201, v201
	v_fma_f32 v200, v200, 2.0, -1.0
	v_fma_f32 v39, v229, v245, v247
	v_fmac_f32_e32 v38, v228, v242
	v_mfma_f32_32x32x16_f16 v[96:111], a[156:159], v[184:187], v[96:111]
	ds_read_b128 v[184:187], v193 offset:22528
	v_rcp_f32_e32 v202, v202
	v_fma_f32 v201, v201, 2.0, -1.0
	v_mul_f32_e32 v216, v212, v200
	v_fmac_f32_e32 v39, v228, v244
	v_fma_f32 v54, v231, v243, v246
	v_mfma_f32_32x32x16_f16 v[112:127], a[156:159], v[188:191], v[112:127]
	ds_read_b128 v[188:191], v193 offset:23552
	s_add_u32 s44, s34, 0x1000
	s_addc_u32 s45, s35, 0
	s_mov_b32 m0, s53
	s_nop 0
	global_load_lds_dwordx4 v192, s[44:45] sc1
	v_rcp_f32_e32 v203, v203
	v_fma_f32 v202, v202, 2.0, -1.0
	v_mul_f32_e32 v217, v213, v201
	v_fma_f32 v55, v231, v245, v247
	v_fmac_f32_e32 v54, v230, v242
	s_waitcnt lgkmcnt(6)
	v_mfma_f32_32x32x16_f16 v[96:111], a[160:163], v[160:163], v[96:111]
	ds_read_b128 v[160:163], v193 offset:24576
	v_fma_f32 v203, v203, 2.0, -1.0
	v_mul_f32_e32 v218, v214, v202
	v_fmac_f32_e32 v55, v230, v244
	ds_read_b128 v[242:245], v248 offset:112
	ds_read_b64 v[246:247], v248 offset:136
	v_mfma_f32_32x32x16_f16 v[112:127], a[160:163], v[164:167], v[112:127]
	ds_read_b128 v[164:167], v193 offset:25600
	v_mul_f32_e32 v219, v215, v203
	v_cvt_pk_f16_f32 v222, v216, v217
	s_waitcnt lgkmcnt(8)
	v_fma_f32 v40, v229, v237, v240
	v_mfma_f32_32x32x16_f16 v[96:111], a[164:167], v[168:171], v[96:111]
	ds_read_b128 v[168:171], v193 offset:26624
	v_cvt_pk_f16_f32 v223, v218, v219
	v_fma_f32 v41, v229, v239, v241
	v_fmac_f32_e32 v40, v228, v236
	v_mfma_f32_32x32x16_f16 v[112:127], a[164:167], v[172:175], v[112:127]
	ds_read_b128 v[172:175], v193 offset:27648
	global_load_lds_dwordx4 v192, s[44:45] offset:1024 sc1
	s_cmp_lg_u32 s33, s60
	s_cbranch_scc1 .LE_nht45
	s_add_u32 s46, s62, 0xa0000
	s_addc_u32 s47, s63, 0
	global_store_dwordx4 v250, v[216:219], s[46:47]
	s_waitcnt vmcnt(0)
.LE_nht45:
	v_fmac_f32_e32 v41, v228, v238
	v_fma_f32 v56, v231, v237, v240
	s_waitcnt lgkmcnt(6)
	v_mfma_f32_32x32x16_f16 v[96:111], a[168:171], v[176:179], v[96:111]
	ds_read_b128 v[176:179], v193 offset:28672
	s_nop 1
	v_permlane32_swap_b32_e32 v220, v222
	v_permlane32_swap_b32_e32 v221, v223
	s_cmp_eq_u32 s31, 0
	s_cbranch_scc1 .LE_slow46
	global_store_dwordx4 v195, v[220:223], s[36:37] offset:0
	s_branch .LE_join47

.LE_join47:
	v_fma_f32 v57, v231, v239, v241
	v_fmac_f32_e32 v56, v230, v236
	v_mfma_f32_32x32x16_f16 v[112:127], a[168:171], v[180:183], v[112:127]
	ds_read_b128 v[180:183], v193 offset:29696
	v_fmac_f32_e32 v57, v230, v238
	ds_read_b128 v[236:239], v248 offset:144
	ds_read_b64 v[240:241], v248 offset:176
	v_mfma_f32_32x32x16_f16 v[96:111], a[172:175], v[184:187], v[96:111]
	ds_read_b128 v[184:187], v193 offset:30720
	s_waitcnt lgkmcnt(8)
	v_fma_f32 v42, v229, v243, v246
	v_mfma_f32_32x32x16_f16 v[112:127], a[172:175], v[188:191], v[112:127]
	ds_read_b128 v[188:191], v193 offset:31744
	global_load_lds_dwordx4 v192, s[44:45] offset:2048 sc1
	v_fma_f32 v43, v229, v245, v247
	v_fmac_f32_e32 v42, v228, v242
	s_waitcnt vmcnt(8)
	s_barrier
	s_waitcnt lgkmcnt(6)
	v_mfma_f32_32x32x16_f16 v[96:111], a[176:179], v[160:163], v[96:111]
	ds_read_b128 v[160:163], v193 offset:32768
	v_fmac_f32_e32 v43, v228, v244
	v_fma_f32 v58, v231, v243, v246
	v_mfma_f32_32x32x16_f16 v[112:127], a[176:179], v[164:167], v[112:127]
	ds_read_b128 v[164:167], v193 offset:33792
	v_fma_f32 v59, v231, v245, v247
	v_fmac_f32_e32 v58, v230, v242
	v_mfma_f32_32x32x16_f16 v[96:111], a[180:183], v[168:171], v[96:111]
	ds_read_b128 v[168:171], v193 offset:34816
	v_fmac_f32_e32 v59, v230, v244
	ds_read_b128 v[242:245], v248 offset:160
	ds_read_b64 v[246:247], v248 offset:184
	v_mfma_f32_32x32x16_f16 v[112:127], a[180:183], v[172:175], v[112:127]
	ds_read_b128 v[172:175], v193 offset:35840
	global_load_lds_dwordx4 v192, s[44:45] offset:3072 sc1
	s_waitcnt lgkmcnt(8)
	v_fma_f32 v44, v229, v237, v240
	s_waitcnt lgkmcnt(6)
	v_mfma_f32_32x32x16_f16 v[96:111], a[184:187], v[176:179], v[96:111]
	ds_read_b128 v[176:179], v193 offset:36864
	v_fma_f32 v45, v229, v239, v241
	v_fmac_f32_e32 v44, v228, v236
	v_mfma_f32_32x32x16_f16 v[112:127], a[184:187], v[180:183], v[112:127]
	ds_read_b128 v[180:183], v193 offset:37888
	v_fmac_f32_e32 v45, v228, v238
	v_fma_f32 v60, v231, v237, v240
	v_mfma_f32_32x32x16_f16 v[96:111], a[188:191], v[184:187], v[96:111]
	ds_read_b128 v[184:187], v193 offset:38912
	v_fma_f32 v61, v231, v239, v241
	v_fmac_f32_e32 v60, v230, v236
	v_mfma_f32_32x32x16_f16 v[112:127], a[188:191], v[188:191], v[112:127]
	ds_read_b128 v[188:191], v193 offset:39936
	s_add_u32 s44, s34, 0x8000
	s_addc_u32 s45, s35, 0
	s_mov_b32 m0, s54
	s_nop 0
	global_load_lds_dwordx4 v192, s[44:45] sc1
	v_fmac_f32_e32 v61, v230, v238
	s_waitcnt lgkmcnt(5)
	s_waitcnt lgkmcnt(4)
	v_mfma_f32_32x32x16_f16 v[96:111], a[192:195], v[160:163], v[96:111]
	ds_read_b128 v[160:163], v193 offset:40960
	v_fma_f32 v46, v229, v243, v246
	v_fma_f32 v47, v229, v245, v247
	v_mfma_f32_32x32x16_f16 v[112:127], a[192:195], v[164:167], v[112:127]
	ds_read_b128 v[164:167], v193 offset:41984
	v_fmac_f32_e32 v46, v228, v242
	v_fmac_f32_e32 v47, v228, v244
	s_waitcnt vmcnt(3)
	s_barrier
	v_mov_b32_e32 v199, 3
	s_cmp_eq_u32 s31, 0
	s_cbranch_scc1 .LE_slow48
	global_store_dword v197, v199, s[40:41]
	s_branch .LE_join49

.LE_join49:
	v_mfma_f32_32x32x16_f16 v[96:111], a[196:199], v[168:171], v[96:111]
	ds_read_b128 v[168:171], v193 offset:43008
	v_fma_f32 v62, v231, v243, v246
	v_fma_f32 v63, v231, v245, v247
	v_mfma_f32_32x32x16_f16 v[112:127], a[196:199], v[172:175], v[112:127]
	ds_read_b128 v[172:175], v193 offset:44032
	global_load_lds_dwordx4 v192, s[44:45] offset:1024 sc1
	v_fmac_f32_e32 v62, v230, v242
	v_fmac_f32_e32 v63, v230, v244
	s_waitcnt lgkmcnt(4)
	v_mfma_f32_32x32x16_f16 v[96:111], a[200:203], v[176:179], v[96:111]
	ds_read_b128 v[176:179], v193 offset:45056
	v_mfma_f32_32x32x16_f16 v[112:127], a[200:203], v[180:183], v[112:127]
	ds_read_b128 v[180:183], v193 offset:46080
	v_mfma_f32_32x32x16_f16 v[96:111], a[204:207], v[184:187], v[96:111]
	ds_read_b128 v[184:187], v193 offset:47104
	v_mfma_f32_32x32x16_f16 v[112:127], a[204:207], v[188:191], v[112:127]
	ds_read_b128 v[188:191], v193 offset:48128
	global_load_lds_dwordx4 v192, s[44:45] offset:2048 sc1
	s_waitcnt lgkmcnt(4)
	v_mfma_f32_32x32x16_f16 v[96:111], a[208:211], v[160:163], v[96:111]
	ds_read_b128 v[160:163], v193 offset:49152
	v_mfma_f32_32x32x16_f16 v[112:127], a[208:211], v[164:167], v[112:127]
	ds_read_b128 v[164:167], v193 offset:50176
	v_mfma_f32_32x32x16_f16 v[96:111], a[212:215], v[168:171], v[96:111]
	ds_read_b128 v[168:171], v193 offset:51200
	v_mfma_f32_32x32x16_f16 v[112:127], a[212:215], v[172:175], v[112:127]
	ds_read_b128 v[172:175], v193 offset:52224
	global_load_lds_dwordx4 v192, s[44:45] offset:3072 sc1
	s_waitcnt lgkmcnt(4)
	v_mfma_f32_32x32x16_f16 v[96:111], a[216:219], v[176:179], v[96:111]
	ds_read_b128 v[176:179], v193 offset:53248
	v_mfma_f32_32x32x16_f16 v[112:127], a[216:219], v[180:183], v[112:127]
	ds_read_b128 v[180:183], v193 offset:54272
	v_mfma_f32_32x32x16_f16 v[96:111], a[220:223], v[184:187], v[96:111]
	ds_read_b128 v[184:187], v193 offset:55296
	v_mfma_f32_32x32x16_f16 v[112:127], a[220:223], v[188:191], v[112:127]
	ds_read_b128 v[188:191], v193 offset:56320
	s_add_u32 s44, s34, 0x9000
	s_addc_u32 s45, s35, 0
	s_mov_b32 m0, s55
	s_nop 0
	global_load_lds_dwordx4 v192, s[44:45] sc1
	s_waitcnt lgkmcnt(4)
	v_mfma_f32_32x32x16_f16 v[96:111], a[224:227], v[160:163], v[96:111]
	ds_read_b128 v[160:163], v193 offset:57344
	v_mfma_f32_32x32x16_f16 v[112:127], a[224:227], v[164:167], v[112:127]
	ds_read_b128 v[164:167], v193 offset:58368
	v_mfma_f32_32x32x16_f16 v[96:111], a[228:231], v[168:171], v[96:111]
	ds_read_b128 v[168:171], v193 offset:59392
	v_mfma_f32_32x32x16_f16 v[112:127], a[228:231], v[172:175], v[112:127]
	ds_read_b128 v[172:175], v193 offset:60416
	global_load_lds_dwordx4 v192, s[44:45] offset:1024 sc1
	s_waitcnt lgkmcnt(4)
	v_mfma_f32_32x32x16_f16 v[96:111], a[232:235], v[176:179], v[96:111]
	ds_read_b128 v[176:179], v193 offset:61440
	v_mfma_f32_32x32x16_f16 v[112:127], a[232:235], v[180:183], v[112:127]
	ds_read_b128 v[180:183], v193 offset:62464
	v_mfma_f32_32x32x16_f16 v[96:111], a[236:239], v[184:187], v[96:111]
	ds_read_b128 v[184:187], v193 offset:63488
	v_mfma_f32_32x32x16_f16 v[112:127], a[236:239], v[188:191], v[112:127]
	ds_read_b128 v[188:191], v193 offset:64512
	global_load_lds_dwordx4 v192, s[44:45] offset:2048 sc1
	s_waitcnt vmcnt(8)
	s_barrier
	s_waitcnt lgkmcnt(4)
	v_mfma_f32_32x32x16_f16 v[96:111], a[240:243], v[160:163], v[96:111]
	ds_read_b128 v[160:163], v192 offset:0
	v_mfma_f32_32x32x16_f16 v[112:127], a[240:243], v[164:167], v[112:127]
	ds_read_b128 v[164:167], v192 offset:1024
	v_mfma_f32_32x32x16_f16 v[96:111], a[244:247], v[168:171], v[96:111]
	ds_read_b128 v[168:171], v192 offset:2048
	v_mfma_f32_32x32x16_f16 v[112:127], a[244:247], v[172:175], v[112:127]
	ds_read_b128 v[172:175], v192 offset:3072
	global_load_lds_dwordx4 v192, s[44:45] offset:3072 sc1
	s_waitcnt lgkmcnt(4)
	v_mfma_f32_32x32x16_f16 v[96:111], a[248:251], v[176:179], v[96:111]
	ds_read_b128 v[176:179], v192 offset:4096
	v_mfma_f32_32x32x16_f16 v[112:127], a[248:251], v[180:183], v[112:127]
	ds_read_b128 v[180:183], v192 offset:5120
	v_mfma_f32_32x32x16_f16 v[96:111], a[252:255], v[184:187], v[96:111]
	ds_read_b128 v[184:187], v192 offset:6144
	v_mfma_f32_32x32x16_f16 v[112:127], a[252:255], v[188:191], v[112:127]
	ds_read_b128 v[188:191], v192 offset:7168
	s_add_u32 s44, s34, 0x10000
	s_addc_u32 s45, s35, 0
	s_mov_b32 m0, s56
	s_nop 0
	global_load_lds_dwordx4 v192, s[44:45] sc1
	s_add_u32 s33, s33, 1
	s_cmp_lt_u32 s33, s28
	s_cbranch_scc1 .LE_loop16

.LD_loop16:
	s_sub_u32 s71, s33, 1
	s_add_u32 s61, s33, 1
	s_min_u32 s61, s61, s60
	s_and_b32 s64, s71, 1
	s_lshl_b32 s64, s64, 22
	s_add_u32 s64, s64, s50
	s_add_u32 s64, s64, 0x60000
	s_add_u32 s36, s6, s64
	s_addc_u32 s37, s7, 0
	s_lshl_b32 s64, s71, 3
	s_add_u32 s64, s64, s29
	s_lshl_b32 s64, s64, 5
	s_add_u32 s64, s64, s30
	s_lshl_b32 s64, s64, 2
	s_add_u32 s40, s8, s64
	s_addc_u32 s41, s9, 0
	s_lshl_b32 s64, s71, 19
	s_add_u32 s64, s64, 0x600
	s_add_u32 s72, s62, s64
	s_addc_u32 s73, s63, 0
	s_nop 3
	s_waitcnt lgkmcnt(4)
	v_mfma_f32_32x32x16_f16 v[0:15], a[0:3], v[160:163], v[0:15]
	ds_read_b128 v[160:163], v192 offset:8192
	v_exp_f32_e32 v200, v96
	v_mfma_f32_32x32x16_f16 v[16:31], a[0:3], v[164:167], v[16:31]
	ds_read_b128 v[164:167], v192 offset:9216
	v_exp_f32_e32 v201, v97
	v_add_f32_e32 v200, 1.0, v200
	v_mfma_f32_32x32x16_f16 v[0:15], a[4:7], v[168:171], v[0:15]
	ds_read_b128 v[168:171], v192 offset:10240
	v_exp_f32_e32 v202, v98
	v_add_f32_e32 v201, 1.0, v201
	v_mfma_f32_32x32x16_f16 v[16:31], a[4:7], v[172:175], v[16:31]
	ds_read_b128 v[172:175], v192 offset:11264
	global_load_lds_dwordx4 v192, s[44:45] offset:1024 sc1
	v_exp_f32_e32 v203, v99
	v_add_f32_e32 v202, 1.0, v202
	s_waitcnt lgkmcnt(4)
	v_mfma_f32_32x32x16_f16 v[0:15], a[8:11], v[176:179], v[0:15]
	ds_read_b128 v[176:179], v192 offset:12288
	v_exp_f32_e32 v204, v100
	v_add_f32_e32 v203, 1.0, v203
	v_mfma_f32_32x32x16_f16 v[16:31], a[8:11], v[180:183], v[16:31]
	ds_read_b128 v[180:183], v192 offset:13312
	v_exp_f32_e32 v205, v101
	v_add_f32_e32 v204, 1.0, v204
	v_mfma_f32_32x32x16_f16 v[0:15], a[12:15], v[184:187], v[0:15]
	ds_read_b128 v[184:187], v192 offset:14336
	v_exp_f32_e32 v206, v102
	v_add_f32_e32 v205, 1.0, v205
	v_mfma_f32_32x32x16_f16 v[16:31], a[12:15], v[188:191], v[16:31]
	ds_read_b128 v[188:191], v192 offset:15360
	global_load_lds_dwordx4 v192, s[44:45] offset:2048 sc1
	v_exp_f32_e32 v207, v103
	v_add_f32_e32 v206, 1.0, v206
	s_waitcnt lgkmcnt(4)
	v_mfma_f32_32x32x16_f16 v[0:15], a[16:19], v[160:163], v[0:15]
	ds_read_b128 v[160:163], v192 offset:16384
	v_exp_f32_e32 v208, v104
	v_add_f32_e32 v207, 1.0, v207
	v_mfma_f32_32x32x16_f16 v[16:31], a[16:19], v[164:167], v[16:31]
	ds_read_b128 v[164:167], v192 offset:17408
	v_exp_f32_e32 v209, v105
	v_add_f32_e32 v208, 1.0, v208
	v_mfma_f32_32x32x16_f16 v[0:15], a[20:23], v[168:171], v[0:15]
	ds_read_b128 v[168:171], v192 offset:18432
	v_exp_f32_e32 v210, v106
	v_add_f32_e32 v209, 1.0, v209
	v_mfma_f32_32x32x16_f16 v[16:31], a[20:23], v[172:175], v[16:31]
	ds_read_b128 v[172:175], v192 offset:19456
	global_load_lds_dwordx4 v192, s[44:45] offset:3072 sc1
	v_exp_f32_e32 v211, v107
	v_add_f32_e32 v210, 1.0, v210
	s_waitcnt lgkmcnt(4)
	v_mfma_f32_32x32x16_f16 v[0:15], a[24:27], v[176:179], v[0:15]
	ds_read_b128 v[176:179], v192 offset:20480
	v_exp_f32_e32 v212, v108
	v_add_f32_e32 v211, 1.0, v211
	v_mfma_f32_32x32x16_f16 v[16:31], a[24:27], v[180:183], v[16:31]
	ds_read_b128 v[180:183], v192 offset:21504
	v_exp_f32_e32 v213, v109
	v_add_f32_e32 v212, 1.0, v212
	v_mfma_f32_32x32x16_f16 v[0:15], a[28:31], v[184:187], v[0:15]
	ds_read_b128 v[184:187], v192 offset:22528
	v_exp_f32_e32 v214, v110
	v_add_f32_e32 v213, 1.0, v213
	v_mfma_f32_32x32x16_f16 v[16:31], a[28:31], v[188:191], v[16:31]
	ds_read_b128 v[188:191], v192 offset:23552
	s_add_u32 s44, s34, 0x11000
	s_addc_u32 s45, s35, 0
	s_mov_b32 m0, s57
	s_nop 0
	global_load_lds_dwordx4 v192, s[44:45] sc1
	v_exp_f32_e32 v215, v111
	v_add_f32_e32 v214, 1.0, v214
	s_waitcnt lgkmcnt(4)
	v_mfma_f32_32x32x16_f16 v[0:15], a[32:35], v[160:163], v[0:15]
	ds_read_b128 v[160:163], v192 offset:24576
	v_add_f32_e32 v215, 1.0, v215
	v_rcp_f32_e32 v200, v200
	v_mfma_f32_32x32x16_f16 v[16:31], a[32:35], v[164:167], v[16:31]
	ds_read_b128 v[164:167], v192 offset:25600
	v_rcp_f32_e32 v201, v201
	v_mfma_f32_32x32x16_f16 v[0:15], a[36:39], v[168:171], v[0:15]
	ds_read_b128 v[168:171], v192 offset:26624
	v_rcp_f32_e32 v202, v202
	v_mfma_f32_32x32x16_f16 v[16:31], a[36:39], v[172:175], v[16:31]
	ds_read_b128 v[172:175], v192 offset:27648
	global_load_lds_dwordx4 v192, s[44:45] offset:1024 sc1
	v_rcp_f32_e32 v203, v203
	s_waitcnt lgkmcnt(4)
	v_mfma_f32_32x32x16_f16 v[0:15], a[40:43], v[176:179], v[0:15]
	ds_read_b128 v[176:179], v192 offset:28672
	v_rcp_f32_e32 v204, v204
	v_mfma_f32_32x32x16_f16 v[16:31], a[40:43], v[180:183], v[16:31]
	ds_read_b128 v[180:183], v192 offset:29696
	v_rcp_f32_e32 v205, v205
	v_mul_f32_e32 v204, v204, v152
	v_mfma_f32_32x32x16_f16 v[0:15], a[44:47], v[184:187], v[0:15]
	ds_read_b128 v[184:187], v192 offset:30720
	v_rcp_f32_e32 v206, v206
	v_mul_f32_e32 v205, v205, v153
	v_mfma_f32_32x32x16_f16 v[16:31], a[44:47], v[188:191], v[16:31]
	ds_read_b128 v[188:191], v192 offset:31744
	global_load_lds_dwordx4 v192, s[44:45] offset:2048 sc1
	v_rcp_f32_e32 v207, v207
	v_mul_f32_e32 v206, v206, v154
	s_waitcnt vmcnt(7)
	s_barrier
	s_waitcnt lgkmcnt(4)
	v_mfma_f32_32x32x16_f16 v[0:15], a[48:51], v[160:163], v[0:15]
	ds_read_b128 v[160:163], v192 offset:32768
	v_rcp_f32_e32 v208, v208
	v_mul_f32_e32 v207, v207, v155
	v_mfma_f32_32x32x16_f16 v[16:31], a[48:51], v[164:167], v[16:31]
	ds_read_b128 v[164:167], v192 offset:33792
	v_rcp_f32_e32 v209, v209
	v_fmamk_f32 v208, v208, 0xc0b8aa3b, v198
	v_mfma_f32_32x32x16_f16 v[0:15], a[52:55], v[168:171], v[0:15]
	ds_read_b128 v[168:171], v192 offset:34816
	v_rcp_f32_e32 v210, v210
	v_fmamk_f32 v209, v209, 0xc0b8aa3b, v198
	v_fma_f32 v152, v200, v208, v204
	v_mfma_f32_32x32x16_f16 v[16:31], a[52:55], v[172:175], v[16:31]
	ds_read_b128 v[172:175], v192 offset:35840
	global_load_lds_dwordx4 v192, s[44:45] offset:3072 sc1
	v_rcp_f32_e32 v211, v211
	v_fmamk_f32 v210, v210, 0xc0b8aa3b, v198
	v_fma_f32 v153, v201, v209, v205
	s_waitcnt lgkmcnt(4)
	v_mfma_f32_32x32x16_f16 v[0:15], a[56:59], v[176:179], v[0:15]
	ds_read_b128 v[176:179], v192 offset:36864
	v_rcp_f32_e32 v212, v212
	v_fmamk_f32 v211, v211, 0xc0b8aa3b, v198
	v_fma_f32 v154, v202, v210, v206
	v_mfma_f32_32x32x16_f16 v[16:31], a[56:59], v[180:183], v[16:31]
	ds_read_b128 v[180:183], v192 offset:37888
	v_rcp_f32_e32 v213, v213
	v_fma_f32 v155, v203, v211, v207
	v_mfma_f32_32x32x16_f16 v[0:15], a[60:63], v[184:187], v[0:15]
	ds_read_b128 v[184:187], v192 offset:38912
	v_rcp_f32_e32 v214, v214
	v_mfma_f32_32x32x16_f16 v[16:31], a[60:63], v[188:191], v[16:31]
	ds_read_b128 v[188:191], v192 offset:39936
	s_add_u32 s44, s34, 0x18000
	s_addc_u32 s45, s35, 0
	s_mov_b32 m0, s58
	s_nop 0
	global_load_lds_dwordx4 v192, s[44:45] sc1
	v_rcp_f32_e32 v215, v215
	s_waitcnt lgkmcnt(4)
	v_mfma_f32_32x32x16_f16 v[0:15], a[64:67], v[160:163], v[0:15]
	ds_read_b128 v[160:163], v192 offset:40960
	v_exp_f32_e32 v200, v152
	v_mfma_f32_32x32x16_f16 v[16:31], a[64:67], v[164:167], v[16:31]
	ds_read_b128 v[164:167], v192 offset:41984
	v_exp_f32_e32 v201, v153
	v_add_f32_e32 v200, 1.0, v200
	v_mfma_f32_32x32x16_f16 v[0:15], a[68:71], v[168:171], v[0:15]
	ds_read_b128 v[168:171], v192 offset:43008
	v_exp_f32_e32 v202, v154
	v_add_f32_e32 v201, 1.0, v201
	v_mfma_f32_32x32x16_f16 v[16:31], a[68:71], v[172:175], v[16:31]
	ds_read_b128 v[172:175], v192 offset:44032
	global_load_lds_dwordx4 v192, s[44:45] offset:1024 sc1
	v_exp_f32_e32 v203, v155
	v_add_f32_e32 v202, 1.0, v202
	s_waitcnt lgkmcnt(4)
	v_mfma_f32_32x32x16_f16 v[0:15], a[72:75], v[176:179], v[0:15]
	ds_read_b128 v[176:179], v192 offset:45056
	v_add_f32_e32 v203, 1.0, v203
	v_rcp_f32_e32 v200, v200
	v_mfma_f32_32x32x16_f16 v[16:31], a[72:75], v[180:183], v[16:31]
	ds_read_b128 v[180:183], v192 offset:46080
	v_rcp_f32_e32 v201, v201
	v_fma_f32 v200, v200, 2.0, -1.0
	v_mfma_f32_32x32x16_f16 v[0:15], a[76:79], v[184:187], v[0:15]
	ds_read_b128 v[184:187], v192 offset:47104
	v_rcp_f32_e32 v202, v202
	v_fma_f32 v201, v201, 2.0, -1.0
	v_mul_f32_e32 v216, v212, v200
	v_mfma_f32_32x32x16_f16 v[16:31], a[76:79], v[188:191], v[16:31]
	ds_read_b128 v[188:191], v192 offset:48128
	global_load_lds_dwordx4 v192, s[44:45] offset:2048 sc1
	v_rcp_f32_e32 v203, v203
	v_fma_f32 v202, v202, 2.0, -1.0
	v_mul_f32_e32 v217, v213, v201
	s_waitcnt lgkmcnt(4)
	v_mfma_f32_32x32x16_f16 v[0:15], a[80:83], v[160:163], v[0:15]
	ds_read_b128 v[160:163], v192 offset:49152
	v_fma_f32 v203, v203, 2.0, -1.0
	v_mul_f32_e32 v218, v214, v202
	v_exp_f32_e32 v200, v112
	v_mfma_f32_32x32x16_f16 v[16:31], a[80:83], v[164:167], v[16:31]
	ds_read_b128 v[164:167], v192 offset:50176
	v_mul_f32_e32 v219, v215, v203
	v_mul_f32_e32 v236, v216, v228
	v_exp_f32_e32 v201, v113
	v_mfma_f32_32x32x16_f16 v[0:15], a[84:87], v[168:171], v[0:15]
	ds_read_b128 v[168:171], v192 offset:51200
	v_mul_f32_e32 v237, v216, v232
	v_fmac_f32_e32 v236, v217, v229
	v_exp_f32_e32 v202, v114
	v_mfma_f32_32x32x16_f16 v[16:31], a[84:87], v[172:175], v[16:31]
	ds_read_b128 v[172:175], v192 offset:52224
	global_load_lds_dwordx4 v192, s[44:45] offset:3072 sc1
	v_fmac_f32_e32 v237, v217, v233
	v_fmac_f32_e32 v236, v218, v230
	v_exp_f32_e32 v203, v115
	s_waitcnt lgkmcnt(4)
	v_mfma_f32_32x32x16_f16 v[0:15], a[88:91], v[176:179], v[0:15]
	ds_read_b128 v[176:179], v192 offset:53248
	v_fmac_f32_e32 v237, v218, v234
	v_fmac_f32_e32 v236, v219, v231
	v_exp_f32_e32 v204, v116
	v_mfma_f32_32x32x16_f16 v[16:31], a[88:91], v[180:183], v[16:31]
	ds_read_b128 v[180:183], v192 offset:54272
	v_fmac_f32_e32 v237, v219, v235
	v_mov_b32_e32 v238, v236
	v_exp_f32_e32 v205, v117
	v_mfma_f32_32x32x16_f16 v[0:15], a[92:95], v[184:187], v[0:15]
	ds_read_b128 v[184:187], v192 offset:55296
	v_mov_b32_e32 v239, v236
	v_mov_b32_e32 v240, v237
	v_exp_f32_e32 v206, v118
	v_mfma_f32_32x32x16_f16 v[16:31], a[92:95], v[188:191], v[16:31]
	ds_read_b128 v[188:191], v192 offset:56320
	s_add_u32 s44, s34, 0x19000
	s_addc_u32 s45, s35, 0
	s_mov_b32 m0, s59
	s_nop 0
	global_load_lds_dwordx4 v192, s[44:45] sc1
	s_lshl_b32 s64, s71, 3
	s_add_u32 s64, s64, s29
	s_lshl_b32 s64, s64, 7
	s_add_u32 s38, s8, s64
	s_addc_u32 s39, s9, 0
	global_load_dword v251, v196, s[38:39] sc1
	v_mov_b32_e32 v241, v237
	v_cvt_pk_f16_f32 v220, v216, v217
	v_exp_f32_e32 v207, v119
	s_waitcnt lgkmcnt(4)
	v_mfma_f32_32x32x16_f16 v[0:15], a[96:99], v[160:163], v[0:15]
	ds_read_b128 v[160:163], v192 offset:57344
	s_nop 1
	v_permlane32_swap_b32_e32 v238, v239
	v_permlane32_swap_b32_e32 v240, v241
	v_add_f32_e32 v238, v238, v239
	v_add_f32_e32 v239, v240, v241
	ds_write_b64 v248, v[238:239] offset:1536
	v_exp_f32_e32 v208, v120
	v_mfma_f32_32x32x16_f16 v[16:31], a[96:99], v[164:167], v[16:31]
	ds_read_b128 v[164:167], v192 offset:58368
	v_cvt_pk_f16_f32 v221, v218, v219
	v_exp_f32_e32 v209, v121
	v_add_f32_e32 v200, 1.0, v200
	v_mfma_f32_32x32x16_f16 v[0:15], a[100:103], v[168:171], v[0:15]
	ds_read_b128 v[168:171], v192 offset:59392
	v_exp_f32_e32 v210, v122
	v_add_f32_e32 v201, 1.0, v201
	v_add_f32_e32 v202, 1.0, v202
	v_mfma_f32_32x32x16_f16 v[16:31], a[100:103], v[172:175], v[16:31]
	ds_read_b128 v[172:175], v192 offset:60416
	global_load_lds_dwordx4 v192, s[44:45] offset:1024 sc1
	v_exp_f32_e32 v211, v123
	v_add_f32_e32 v203, 1.0, v203
	v_add_f32_e32 v204, 1.0, v204
	s_waitcnt lgkmcnt(5)
	v_mfma_f32_32x32x16_f16 v[0:15], a[104:107], v[176:179], v[0:15]
	ds_read_b128 v[176:179], v192 offset:61440
	v_exp_f32_e32 v212, v124
	v_add_f32_e32 v205, 1.0, v205
	v_add_f32_e32 v206, 1.0, v206
	v_mfma_f32_32x32x16_f16 v[16:31], a[104:107], v[180:183], v[16:31]
	ds_read_b128 v[180:183], v192 offset:62464
	v_exp_f32_e32 v213, v125
	v_add_f32_e32 v207, 1.0, v207
	v_add_f32_e32 v208, 1.0, v208
	v_mfma_f32_32x32x16_f16 v[0:15], a[108:111], v[184:187], v[0:15]
	ds_read_b128 v[184:187], v192 offset:63488
	v_exp_f32_e32 v214, v126
	v_add_f32_e32 v209, 1.0, v209
	v_add_f32_e32 v210, 1.0, v210
	v_mfma_f32_32x32x16_f16 v[16:31], a[108:111], v[188:191], v[16:31]
	ds_read_b128 v[188:191], v192 offset:64512
	global_load_lds_dwordx4 v192, s[44:45] offset:2048 sc1
	v_exp_f32_e32 v215, v127
	v_add_f32_e32 v211, 1.0, v211
	v_add_f32_e32 v212, 1.0, v212
	s_waitcnt vmcnt(8)
	s_barrier
	s_waitcnt lgkmcnt(4)
	v_mfma_f32_32x32x16_f16 v[0:15], a[112:115], v[160:163], v[0:15]
	ds_read_b128 v[160:163], v193 offset:0
	v_add_f32_e32 v213, 1.0, v213
	v_add_f32_e32 v214, 1.0, v214
	v_rcp_f32_e32 v200, v200
	v_mfma_f32_32x32x16_f16 v[16:31], a[112:115], v[164:167], v[16:31]
	ds_read_b128 v[164:167], v193 offset:1024
	v_add_f32_e32 v215, 1.0, v215
	v_rcp_f32_e32 v201, v201
	v_mfma_f32_32x32x16_f16 v[0:15], a[116:119], v[168:171], v[0:15]
	ds_read_b128 v[168:171], v193 offset:2048
	v_rcp_f32_e32 v202, v202
	v_mfma_f32_32x32x16_f16 v[16:31], a[116:119], v[172:175], v[16:31]
	ds_read_b128 v[172:175], v193 offset:3072
	global_load_lds_dwordx4 v192, s[44:45] offset:3072 sc1
	v_rcp_f32_e32 v203, v203
	s_waitcnt lgkmcnt(4)
	v_mfma_f32_32x32x16_f16 v[0:15], a[120:123], v[176:179], v[0:15]
	ds_read_b128 v[176:179], v193 offset:4096
	v_rcp_f32_e32 v204, v204
	s_add_u32 s46, s42, 0x4000
	s_addc_u32 s47, s43, 0
	global_load_dwordx4 v[64:67], v192, s[46:47] offset:0
	v_mfma_f32_32x32x16_f16 v[16:31], a[120:123], v[180:183], v[16:31]
	ds_read_b128 v[180:183], v193 offset:5120
	v_rcp_f32_e32 v205, v205
	v_mul_f32_e32 v204, v204, v156
	global_load_dwordx4 v[68:71], v192, s[46:47] offset:1024
	global_load_dwordx4 v[72:75], v192, s[46:47] offset:2048
	v_mfma_f32_32x32x16_f16 v[0:15], a[124:127], v[184:187], v[0:15]
	ds_read_b128 v[184:187], v193 offset:6144
	v_rcp_f32_e32 v206, v206
	v_mul_f32_e32 v205, v205, v157
	global_load_dwordx4 v[76:79], v192, s[46:47] offset:3072
	s_add_u32 s46, s42, 0x5000
	s_addc_u32 s47, s43, 0
	v_mfma_f32_32x32x16_f16 v[16:31], a[124:127], v[188:191], v[16:31]
	ds_read_b128 v[188:191], v193 offset:7168
	s_waitcnt vmcnt(7)
	v_cmp_gt_u32_e32 vcc, 2, v251
	s_cbranch_vccz .LD_tok20

.LD_tok20:
	s_and_b32 s64, s71, 1
	s_lshl_b32 s64, s64, 22
	s_add_u32 s64, s64, s49
	s_add_u32 s64, s64, 0x20000
	s_add_u32 s34, s6, s64
	s_addc_u32 s35, s7, 0
	s_add_u32 s44, s34, 0x0
	s_addc_u32 s45, s35, 0
	s_mov_b32 m0, s52
	s_nop 0
	global_load_lds_dwordx4 v192, s[44:45] sc1
	v_rcp_f32_e32 v207, v207
	v_mul_f32_e32 v206, v206, v158
	global_load_dwordx4 v[80:83], v192, s[46:47] offset:0
	global_load_dwordx4 v[84:87], v192, s[46:47] offset:1024
	s_waitcnt lgkmcnt(4)
	v_mfma_f32_32x32x16_f16 v[0:15], a[128:131], v[160:163], v[0:15]
	ds_read_b128 v[160:163], v193 offset:8192
	v_rcp_f32_e32 v208, v208
	v_mul_f32_e32 v207, v207, v159
	global_load_dwordx4 v[88:91], v192, s[46:47] offset:2048
	global_load_dwordx4 v[92:95], v192, s[46:47] offset:3072
	v_mfma_f32_32x32x16_f16 v[16:31], a[128:131], v[164:167], v[16:31]
	ds_read_b128 v[164:167], v193 offset:9216
	v_rcp_f32_e32 v209, v209
	v_fmamk_f32 v208, v208, 0xc0b8aa3b, v198
	v_mfma_f32_32x32x16_f16 v[0:15], a[132:135], v[168:171], v[0:15]
	ds_read_b128 v[168:171], v193 offset:10240
	v_rcp_f32_e32 v210, v210
	v_fmamk_f32 v209, v209, 0xc0b8aa3b, v198
	v_fma_f32 v156, v200, v208, v204
	v_mfma_f32_32x32x16_f16 v[16:31], a[132:135], v[172:175], v[16:31]
	ds_read_b128 v[172:175], v193 offset:11264
	global_load_lds_dwordx4 v192, s[44:45] offset:1024 sc1
	v_rcp_f32_e32 v211, v211
	v_fmamk_f32 v210, v210, 0xc0b8aa3b, v198
	v_fma_f32 v157, v201, v209, v205
	s_waitcnt lgkmcnt(4)
	v_mfma_f32_32x32x16_f16 v[0:15], a[136:139], v[176:179], v[0:15]
	ds_read_b128 v[176:179], v193 offset:12288
	v_rcp_f32_e32 v212, v212
	v_fmamk_f32 v211, v211, 0xc0b8aa3b, v198
	v_fma_f32 v158, v202, v210, v206
	v_mfma_f32_32x32x16_f16 v[16:31], a[136:139], v[180:183], v[16:31]
	ds_read_b128 v[180:183], v193 offset:13312
	v_rcp_f32_e32 v213, v213
	v_fma_f32 v159, v203, v211, v207
	v_mfma_f32_32x32x16_f16 v[0:15], a[140:143], v[184:187], v[0:15]
	ds_read_b128 v[184:187], v193 offset:14336
	v_rcp_f32_e32 v214, v214
	v_mfma_f32_32x32x16_f16 v[16:31], a[140:143], v[188:191], v[16:31]
	ds_read_b128 v[188:191], v193 offset:15360
	global_load_lds_dwordx4 v192, s[44:45] offset:2048 sc1
	v_rcp_f32_e32 v215, v215
	s_waitcnt lgkmcnt(4)
	v_mfma_f32_32x32x16_f16 v[0:15], a[144:147], v[160:163], v[0:15]
	ds_read_b128 v[160:163], v193 offset:16384
	v_exp_f32_e32 v200, v156
	v_mfma_f32_32x32x16_f16 v[16:31], a[144:147], v[164:167], v[16:31]
	ds_read_b128 v[164:167], v193 offset:17408
	v_exp_f32_e32 v201, v157
	v_add_f32_e32 v200, 1.0, v200
	v_mfma_f32_32x32x16_f16 v[0:15], a[148:151], v[168:171], v[0:15]
	ds_read_b128 v[168:171], v193 offset:18432
	v_exp_f32_e32 v202, v158
	v_add_f32_e32 v201, 1.0, v201
	v_mfma_f32_32x32x16_f16 v[16:31], a[148:151], v[172:175], v[16:31]
	ds_read_b128 v[172:175], v193 offset:19456
	global_load_lds_dwordx4 v192, s[44:45] offset:3072 sc1
	v_exp_f32_e32 v203, v159
	v_add_f32_e32 v202, 1.0, v202
	s_waitcnt lgkmcnt(4)
	v_mfma_f32_32x32x16_f16 v[0:15], a[152:155], v[176:179], v[0:15]
	ds_read_b128 v[176:179], v193 offset:20480
	v_add_f32_e32 v203, 1.0, v203
	v_rcp_f32_e32 v200, v200
	v_mfma_f32_32x32x16_f16 v[16:31], a[152:155], v[180:183], v[16:31]
	ds_read_b128 v[180:183], v193 offset:21504
	v_rcp_f32_e32 v201, v201
	v_fma_f32 v200, v200, 2.0, -1.0
	v_mfma_f32_32x32x16_f16 v[0:15], a[156:159], v[184:187], v[0:15]
	ds_read_b128 v[184:187], v193 offset:22528
	v_rcp_f32_e32 v202, v202
	v_fma_f32 v201, v201, 2.0, -1.0
	v_mul_f32_e32 v216, v212, v200
	v_mfma_f32_32x32x16_f16 v[16:31], a[156:159], v[188:191], v[16:31]
	ds_read_b128 v[188:191], v193 offset:23552
	s_add_u32 s44, s34, 0x1000
	s_addc_u32 s45, s35, 0
	s_mov_b32 m0, s53
	s_nop 0
	global_load_lds_dwordx4 v192, s[44:45] sc1
	v_rcp_f32_e32 v203, v203
	v_fma_f32 v202, v202, 2.0, -1.0
	v_mul_f32_e32 v217, v213, v201
	s_waitcnt lgkmcnt(4)
	v_mfma_f32_32x32x16_f16 v[0:15], a[160:163], v[160:163], v[0:15]
	ds_read_b128 v[160:163], v193 offset:24576
	v_fma_f32 v203, v203, 2.0, -1.0
	v_mul_f32_e32 v218, v214, v202
	v_mfma_f32_32x32x16_f16 v[16:31], a[160:163], v[164:167], v[16:31]
	ds_read_b128 v[164:167], v193 offset:25600
	v_mul_f32_e32 v219, v215, v203
	v_mul_f32_e32 v236, v216, v228
	v_mfma_f32_32x32x16_f16 v[0:15], a[164:167], v[168:171], v[0:15]
	ds_read_b128 v[168:171], v193 offset:26624
	v_mul_f32_e32 v237, v216, v232
	v_fmac_f32_e32 v236, v217, v229
	v_mfma_f32_32x32x16_f16 v[16:31], a[164:167], v[172:175], v[16:31]
	ds_read_b128 v[172:175], v193 offset:27648
	global_load_lds_dwordx4 v192, s[44:45] offset:1024 sc1
	v_fmac_f32_e32 v237, v217, v233
	v_fmac_f32_e32 v236, v218, v230
	s_waitcnt lgkmcnt(4)
	v_mfma_f32_32x32x16_f16 v[0:15], a[168:171], v[176:179], v[0:15]
	ds_read_b128 v[176:179], v193 offset:28672
	v_fmac_f32_e32 v237, v218, v234
	v_fmac_f32_e32 v236, v219, v231
	v_mfma_f32_32x32x16_f16 v[16:31], a[168:171], v[180:183], v[16:31]
	ds_read_b128 v[180:183], v193 offset:29696
	v_fmac_f32_e32 v237, v219, v235
	v_mov_b32_e32 v238, v236
	v_mfma_f32_32x32x16_f16 v[0:15], a[172:175], v[184:187], v[0:15]
	ds_read_b128 v[184:187], v193 offset:30720
	v_mov_b32_e32 v239, v236
	v_mov_b32_e32 v240, v237
	v_mfma_f32_32x32x16_f16 v[16:31], a[172:175], v[188:191], v[16:31]
	ds_read_b128 v[188:191], v193 offset:31744
	global_load_lds_dwordx4 v192, s[44:45] offset:2048 sc1
	v_mov_b32_e32 v241, v237
	v_cvt_pk_f16_f32 v222, v216, v217
	s_waitcnt vmcnt(15)
	s_barrier
	s_waitcnt lgkmcnt(4)
	v_mfma_f32_32x32x16_f16 v[0:15], a[176:179], v[160:163], v[0:15]
	ds_read_b128 v[160:163], v193 offset:32768
	s_nop 1
	v_permlane32_swap_b32_e32 v238, v239
	v_permlane32_swap_b32_e32 v240, v241
	v_add_f32_e32 v238, v238, v239
	v_add_f32_e32 v239, v240, v241
	ds_write_b64 v248, v[238:239] offset:1792
	v_mfma_f32_32x32x16_f16 v[16:31], a[176:179], v[164:167], v[16:31]
	ds_read_b128 v[164:167], v193 offset:33792
	v_cvt_pk_f16_f32 v223, v218, v219
	v_mfma_f32_32x32x16_f16 v[0:15], a[180:183], v[168:171], v[0:15]
	ds_read_b128 v[168:171], v193 offset:34816
	s_nop 1
	v_permlane32_swap_b32_e32 v220, v222
	v_permlane32_swap_b32_e32 v221, v223
	s_cmp_eq_u32 s31, 0
	s_cbranch_scc1 .LD_slow22
	global_store_dwordx4 v195, v[220:223], s[36:37] offset:0
	s_branch .LD_join23

.LD_join25:
	ds_read_b64 v[200:201], v249 offset:1536
	ds_read_b64 v[202:203], v249 offset:3584
	ds_read_b64 v[204:205], v249 offset:5632
	ds_read_b64 v[206:207], v249 offset:7680
	s_waitcnt lgkmcnt(8)
	v_mfma_f32_32x32x16_f16 v[0:15], a[208:211], v[160:163], v[0:15]
	ds_read_b128 v[160:163], v193 offset:49152
	v_mfma_f32_32x32x16_f16 v[16:31], a[208:211], v[164:167], v[16:31]
	ds_read_b128 v[164:167], v193 offset:50176
	v_mfma_f32_32x32x16_f16 v[0:15], a[212:215], v[168:171], v[0:15]
	ds_read_b128 v[168:171], v193 offset:51200
	v_mfma_f32_32x32x16_f16 v[16:31], a[212:215], v[172:175], v[16:31]
	ds_read_b128 v[172:175], v193 offset:52224
	global_load_lds_dwordx4 v192, s[44:45] offset:3072 sc1
	s_waitcnt lgkmcnt(8)
	v_mfma_f32_32x32x16_f16 v[0:15], a[216:219], v[176:179], v[0:15]
	ds_read_b128 v[176:179], v193 offset:53248
	v_mfma_f32_32x32x16_f16 v[16:31], a[216:219], v[180:183], v[16:31]
	ds_read_b128 v[180:183], v193 offset:54272
	v_mfma_f32_32x32x16_f16 v[0:15], a[220:223], v[184:187], v[0:15]
	ds_read_b128 v[184:187], v193 offset:55296
	v_mfma_f32_32x32x16_f16 v[16:31], a[220:223], v[188:191], v[16:31]
	ds_read_b128 v[188:191], v193 offset:56320
	s_add_u32 s44, s34, 0x9000
	s_addc_u32 s45, s35, 0
	s_mov_b32 m0, s55
	s_nop 0
	global_load_lds_dwordx4 v192, s[44:45] sc1
	s_waitcnt lgkmcnt(4)
	v_mfma_f32_32x32x16_f16 v[0:15], a[224:227], v[160:163], v[0:15]
	ds_read_b128 v[160:163], v193 offset:57344
	v_mfma_f32_32x32x16_f16 v[16:31], a[224:227], v[164:167], v[16:31]
	ds_read_b128 v[164:167], v193 offset:58368
	v_mfma_f32_32x32x16_f16 v[0:15], a[228:231], v[168:171], v[0:15]
	ds_read_b128 v[168:171], v193 offset:59392
	v_mfma_f32_32x32x16_f16 v[16:31], a[228:231], v[172:175], v[16:31]
	ds_read_b128 v[172:175], v193 offset:60416
	global_load_lds_dwordx4 v192, s[44:45] offset:1024 sc1
	v_add_f32_e32 v200, v200, v202
	v_add_f32_e32 v201, v201, v203
	v_add_f32_e32 v200, v200, v204
	v_add_f32_e32 v201, v201, v205
	v_add_f32_e32 v200, v200, v206
	v_add_f32_e32 v201, v201, v207
	global_store_dwordx2 v250, v[200:201], s[72:73]
	s_waitcnt lgkmcnt(4)
	v_mfma_f32_32x32x16_f16 v[0:15], a[232:235], v[176:179], v[0:15]
	ds_read_b128 v[176:179], v193 offset:61440
	v_mfma_f32_32x32x16_f16 v[16:31], a[232:235], v[180:183], v[16:31]
	ds_read_b128 v[180:183], v193 offset:62464
	v_mfma_f32_32x32x16_f16 v[0:15], a[236:239], v[184:187], v[0:15]
	ds_read_b128 v[184:187], v193 offset:63488
	v_mfma_f32_32x32x16_f16 v[16:31], a[236:239], v[188:191], v[16:31]
	ds_read_b128 v[188:191], v193 offset:64512
	global_load_lds_dwordx4 v192, s[44:45] offset:2048 sc1
	s_waitcnt vmcnt(9)
	s_barrier
	s_waitcnt lgkmcnt(4)
	v_mfma_f32_32x32x16_f16 v[0:15], a[240:243], v[160:163], v[0:15]
	ds_read_b128 v[160:163], v192 offset:0
	v_mfma_f32_32x32x16_f16 v[16:31], a[240:243], v[164:167], v[16:31]
	ds_read_b128 v[164:167], v192 offset:1024
	v_mfma_f32_32x32x16_f16 v[0:15], a[244:247], v[168:171], v[0:15]
	ds_read_b128 v[168:171], v192 offset:2048
	v_mfma_f32_32x32x16_f16 v[16:31], a[244:247], v[172:175], v[16:31]
	ds_read_b128 v[172:175], v192 offset:3072
	global_load_lds_dwordx4 v192, s[44:45] offset:3072 sc1
	s_waitcnt lgkmcnt(4)
	v_mfma_f32_32x32x16_f16 v[0:15], a[248:251], v[176:179], v[0:15]
	ds_read_b128 v[176:179], v192 offset:4096
	v_mfma_f32_32x32x16_f16 v[16:31], a[248:251], v[180:183], v[16:31]
	ds_read_b128 v[180:183], v192 offset:5120
	v_mfma_f32_32x32x16_f16 v[0:15], a[252:255], v[184:187], v[0:15]
	ds_read_b128 v[184:187], v192 offset:6144
	v_mfma_f32_32x32x16_f16 v[16:31], a[252:255], v[188:191], v[16:31]
	ds_read_b128 v[188:191], v192 offset:7168
	s_add_u32 s44, s34, 0x10000
	s_addc_u32 s45, s35, 0
	s_mov_b32 m0, s56
	s_nop 0
	global_load_lds_dwordx4 v192, s[44:45] sc1
	s_and_b32 s64, s33, 1
	s_lshl_b32 s64, s64, 22
	s_add_u32 s64, s64, s50
	s_add_u32 s36, s6, s64
	s_addc_u32 s37, s7, 0
	s_lshl_b32 s64, s33, 3
	s_add_u32 s64, s64, s29
	s_lshl_b32 s64, s64, 5
	s_add_u32 s64, s64, s30
	s_lshl_b32 s64, s64, 2
	s_add_u32 s40, s8, s64
	s_addc_u32 s41, s9, 0
	s_lshl_b32 s64, s33, 19
	s_add_u32 s72, s62, s64
	s_addc_u32 s73, s63, 0
	s_nop 3
	s_waitcnt lgkmcnt(4)
	v_mfma_f32_32x32x16_f16 v[32:47], a[0:3], v[160:163], v[32:47]
	ds_read_b128 v[160:163], v192 offset:8192
	v_exp_f32_e32 v200, v0
	v_mfma_f32_32x32x16_f16 v[48:63], a[0:3], v[164:167], v[48:63]
	ds_read_b128 v[164:167], v192 offset:9216
	v_exp_f32_e32 v201, v1
	v_add_f32_e32 v200, 1.0, v200
	v_mfma_f32_32x32x16_f16 v[32:47], a[4:7], v[168:171], v[32:47]
	ds_read_b128 v[168:171], v192 offset:10240
	v_exp_f32_e32 v202, v2
	v_add_f32_e32 v201, 1.0, v201
	v_mfma_f32_32x32x16_f16 v[48:63], a[4:7], v[172:175], v[48:63]
	ds_read_b128 v[172:175], v192 offset:11264
	global_load_lds_dwordx4 v192, s[44:45] offset:1024 sc1
	v_exp_f32_e32 v203, v3
	v_add_f32_e32 v202, 1.0, v202
	s_waitcnt lgkmcnt(4)
	v_mfma_f32_32x32x16_f16 v[32:47], a[8:11], v[176:179], v[32:47]
	ds_read_b128 v[176:179], v192 offset:12288
	v_exp_f32_e32 v204, v4
	v_add_f32_e32 v203, 1.0, v203
	v_mfma_f32_32x32x16_f16 v[48:63], a[8:11], v[180:183], v[48:63]
	ds_read_b128 v[180:183], v192 offset:13312
	v_exp_f32_e32 v205, v5
	v_add_f32_e32 v204, 1.0, v204
	v_mfma_f32_32x32x16_f16 v[32:47], a[12:15], v[184:187], v[32:47]
	ds_read_b128 v[184:187], v192 offset:14336
	v_exp_f32_e32 v206, v6
	v_add_f32_e32 v205, 1.0, v205
	v_mfma_f32_32x32x16_f16 v[48:63], a[12:15], v[188:191], v[48:63]
	ds_read_b128 v[188:191], v192 offset:15360
	global_load_lds_dwordx4 v192, s[44:45] offset:2048 sc1
	v_exp_f32_e32 v207, v7
	v_add_f32_e32 v206, 1.0, v206
	s_waitcnt lgkmcnt(4)
	v_mfma_f32_32x32x16_f16 v[32:47], a[16:19], v[160:163], v[32:47]
	ds_read_b128 v[160:163], v192 offset:16384
	v_exp_f32_e32 v208, v8
	v_add_f32_e32 v207, 1.0, v207
	v_mfma_f32_32x32x16_f16 v[48:63], a[16:19], v[164:167], v[48:63]
	ds_read_b128 v[164:167], v192 offset:17408
	v_exp_f32_e32 v209, v9
	v_add_f32_e32 v208, 1.0, v208
	v_mfma_f32_32x32x16_f16 v[32:47], a[20:23], v[168:171], v[32:47]
	ds_read_b128 v[168:171], v192 offset:18432
	v_exp_f32_e32 v210, v10
	v_add_f32_e32 v209, 1.0, v209
	v_mfma_f32_32x32x16_f16 v[48:63], a[20:23], v[172:175], v[48:63]
	ds_read_b128 v[172:175], v192 offset:19456
	global_load_lds_dwordx4 v192, s[44:45] offset:3072 sc1
	v_exp_f32_e32 v211, v11
	v_add_f32_e32 v210, 1.0, v210
	s_waitcnt lgkmcnt(4)
	v_mfma_f32_32x32x16_f16 v[32:47], a[24:27], v[176:179], v[32:47]
	ds_read_b128 v[176:179], v192 offset:20480
	v_exp_f32_e32 v212, v12
	v_add_f32_e32 v211, 1.0, v211
	v_mfma_f32_32x32x16_f16 v[48:63], a[24:27], v[180:183], v[48:63]
	ds_read_b128 v[180:183], v192 offset:21504
	v_exp_f32_e32 v213, v13
	v_add_f32_e32 v212, 1.0, v212
	v_mfma_f32_32x32x16_f16 v[32:47], a[28:31], v[184:187], v[32:47]
	ds_read_b128 v[184:187], v192 offset:22528
	v_exp_f32_e32 v214, v14
	v_add_f32_e32 v213, 1.0, v213
	v_mfma_f32_32x32x16_f16 v[48:63], a[28:31], v[188:191], v[48:63]
	ds_read_b128 v[188:191], v192 offset:23552
	s_add_u32 s44, s34, 0x11000
	s_addc_u32 s45, s35, 0
	s_mov_b32 m0, s57
	s_nop 0
	global_load_lds_dwordx4 v192, s[44:45] sc1
	v_exp_f32_e32 v215, v15
	v_add_f32_e32 v214, 1.0, v214
	s_waitcnt lgkmcnt(4)
	v_mfma_f32_32x32x16_f16 v[32:47], a[32:35], v[160:163], v[32:47]
	ds_read_b128 v[160:163], v192 offset:24576
	v_add_f32_e32 v215, 1.0, v215
	v_rcp_f32_e32 v200, v200
	v_mfma_f32_32x32x16_f16 v[48:63], a[32:35], v[164:167], v[48:63]
	ds_read_b128 v[164:167], v192 offset:25600
	v_rcp_f32_e32 v201, v201
	v_mfma_f32_32x32x16_f16 v[32:47], a[36:39], v[168:171], v[32:47]
	ds_read_b128 v[168:171], v192 offset:26624
	v_rcp_f32_e32 v202, v202
	v_mfma_f32_32x32x16_f16 v[48:63], a[36:39], v[172:175], v[48:63]
	ds_read_b128 v[172:175], v192 offset:27648
	global_load_lds_dwordx4 v192, s[44:45] offset:1024 sc1
	v_rcp_f32_e32 v203, v203
	s_waitcnt lgkmcnt(4)
	v_mfma_f32_32x32x16_f16 v[32:47], a[40:43], v[176:179], v[32:47]
	ds_read_b128 v[176:179], v192 offset:28672
	v_rcp_f32_e32 v204, v204
	v_mfma_f32_32x32x16_f16 v[48:63], a[40:43], v[180:183], v[48:63]
	ds_read_b128 v[180:183], v192 offset:29696
	v_rcp_f32_e32 v205, v205
	v_mul_f32_e32 v204, v204, v128
	v_mfma_f32_32x32x16_f16 v[32:47], a[44:47], v[184:187], v[32:47]
	ds_read_b128 v[184:187], v192 offset:30720
	v_rcp_f32_e32 v206, v206
	v_mul_f32_e32 v205, v205, v129
	v_mfma_f32_32x32x16_f16 v[48:63], a[44:47], v[188:191], v[48:63]
	ds_read_b128 v[188:191], v192 offset:31744
	global_load_lds_dwordx4 v192, s[44:45] offset:2048 sc1
	v_rcp_f32_e32 v207, v207
	v_mul_f32_e32 v206, v206, v130
	s_waitcnt vmcnt(7)
	s_barrier
	s_waitcnt lgkmcnt(4)
	v_mfma_f32_32x32x16_f16 v[32:47], a[48:51], v[160:163], v[32:47]
	ds_read_b128 v[160:163], v192 offset:32768
	v_rcp_f32_e32 v208, v208
	v_mul_f32_e32 v207, v207, v131
	v_mfma_f32_32x32x16_f16 v[48:63], a[48:51], v[164:167], v[48:63]
	ds_read_b128 v[164:167], v192 offset:33792
	v_rcp_f32_e32 v209, v209
	v_fmamk_f32 v208, v208, 0xc0b8aa3b, v198
	v_mfma_f32_32x32x16_f16 v[32:47], a[52:55], v[168:171], v[32:47]
	ds_read_b128 v[168:171], v192 offset:34816
	v_rcp_f32_e32 v210, v210
	v_fmamk_f32 v209, v209, 0xc0b8aa3b, v198
	v_fma_f32 v128, v200, v208, v204
	v_mfma_f32_32x32x16_f16 v[48:63], a[52:55], v[172:175], v[48:63]
	ds_read_b128 v[172:175], v192 offset:35840
	global_load_lds_dwordx4 v192, s[44:45] offset:3072 sc1
	v_rcp_f32_e32 v211, v211
	v_fmamk_f32 v210, v210, 0xc0b8aa3b, v198
	v_fma_f32 v129, v201, v209, v205
	s_waitcnt lgkmcnt(4)
	v_mfma_f32_32x32x16_f16 v[32:47], a[56:59], v[176:179], v[32:47]
	ds_read_b128 v[176:179], v192 offset:36864
	v_rcp_f32_e32 v212, v212
	v_fmamk_f32 v211, v211, 0xc0b8aa3b, v198
	v_fma_f32 v130, v202, v210, v206
	v_mfma_f32_32x32x16_f16 v[48:63], a[56:59], v[180:183], v[48:63]
	ds_read_b128 v[180:183], v192 offset:37888
	v_rcp_f32_e32 v213, v213
	v_fma_f32 v131, v203, v211, v207
	v_mfma_f32_32x32x16_f16 v[32:47], a[60:63], v[184:187], v[32:47]
	ds_read_b128 v[184:187], v192 offset:38912
	v_rcp_f32_e32 v214, v214
	v_mfma_f32_32x32x16_f16 v[48:63], a[60:63], v[188:191], v[48:63]
	ds_read_b128 v[188:191], v192 offset:39936
	s_add_u32 s44, s34, 0x18000
	s_addc_u32 s45, s35, 0
	s_mov_b32 m0, s58
	s_nop 0
	global_load_lds_dwordx4 v192, s[44:45] sc1
	v_rcp_f32_e32 v215, v215
	s_waitcnt lgkmcnt(4)
	v_mfma_f32_32x32x16_f16 v[32:47], a[64:67], v[160:163], v[32:47]
	ds_read_b128 v[160:163], v192 offset:40960
	v_exp_f32_e32 v200, v128
	v_mfma_f32_32x32x16_f16 v[48:63], a[64:67], v[164:167], v[48:63]
	ds_read_b128 v[164:167], v192 offset:41984
	v_exp_f32_e32 v201, v129
	v_add_f32_e32 v200, 1.0, v200
	v_mfma_f32_32x32x16_f16 v[32:47], a[68:71], v[168:171], v[32:47]
	ds_read_b128 v[168:171], v192 offset:43008
	v_exp_f32_e32 v202, v130
	v_add_f32_e32 v201, 1.0, v201
	v_mfma_f32_32x32x16_f16 v[48:63], a[68:71], v[172:175], v[48:63]
	ds_read_b128 v[172:175], v192 offset:44032
	global_load_lds_dwordx4 v192, s[44:45] offset:1024 sc1
	v_exp_f32_e32 v203, v131
	v_add_f32_e32 v202, 1.0, v202
	s_waitcnt lgkmcnt(4)
	v_mfma_f32_32x32x16_f16 v[32:47], a[72:75], v[176:179], v[32:47]
	ds_read_b128 v[176:179], v192 offset:45056
	v_add_f32_e32 v203, 1.0, v203
	v_rcp_f32_e32 v200, v200
	v_mfma_f32_32x32x16_f16 v[48:63], a[72:75], v[180:183], v[48:63]
	ds_read_b128 v[180:183], v192 offset:46080
	v_rcp_f32_e32 v201, v201
	v_fma_f32 v200, v200, 2.0, -1.0
	v_mfma_f32_32x32x16_f16 v[32:47], a[76:79], v[184:187], v[32:47]
	ds_read_b128 v[184:187], v192 offset:47104
	v_rcp_f32_e32 v202, v202
	v_fma_f32 v201, v201, 2.0, -1.0
	v_mul_f32_e32 v216, v212, v200
	v_mfma_f32_32x32x16_f16 v[48:63], a[76:79], v[188:191], v[48:63]
	ds_read_b128 v[188:191], v192 offset:48128
	global_load_lds_dwordx4 v192, s[44:45] offset:2048 sc1
	v_rcp_f32_e32 v203, v203
	v_fma_f32 v202, v202, 2.0, -1.0
	v_mul_f32_e32 v217, v213, v201
	s_waitcnt lgkmcnt(4)
	v_mfma_f32_32x32x16_f16 v[32:47], a[80:83], v[160:163], v[32:47]
	ds_read_b128 v[160:163], v192 offset:49152
	v_fma_f32 v203, v203, 2.0, -1.0
	v_mul_f32_e32 v218, v214, v202
	v_exp_f32_e32 v200, v16
	v_mfma_f32_32x32x16_f16 v[48:63], a[80:83], v[164:167], v[48:63]
	ds_read_b128 v[164:167], v192 offset:50176
	v_mul_f32_e32 v219, v215, v203
	v_mul_f32_e32 v236, v216, v228
	v_exp_f32_e32 v201, v17
	v_mfma_f32_32x32x16_f16 v[32:47], a[84:87], v[168:171], v[32:47]
	ds_read_b128 v[168:171], v192 offset:51200
	v_mul_f32_e32 v237, v216, v232
	v_fmac_f32_e32 v236, v217, v229
	v_exp_f32_e32 v202, v18
	v_mfma_f32_32x32x16_f16 v[48:63], a[84:87], v[172:175], v[48:63]
	ds_read_b128 v[172:175], v192 offset:52224
	global_load_lds_dwordx4 v192, s[44:45] offset:3072 sc1
	v_fmac_f32_e32 v237, v217, v233
	v_fmac_f32_e32 v236, v218, v230
	v_exp_f32_e32 v203, v19
	s_waitcnt lgkmcnt(4)
	v_mfma_f32_32x32x16_f16 v[32:47], a[88:91], v[176:179], v[32:47]
	ds_read_b128 v[176:179], v192 offset:53248
	v_fmac_f32_e32 v237, v218, v234
	v_fmac_f32_e32 v236, v219, v231
	v_exp_f32_e32 v204, v20
	v_mfma_f32_32x32x16_f16 v[48:63], a[88:91], v[180:183], v[48:63]
	ds_read_b128 v[180:183], v192 offset:54272
	v_fmac_f32_e32 v237, v219, v235
	v_mov_b32_e32 v238, v236
	v_exp_f32_e32 v205, v21
	v_mfma_f32_32x32x16_f16 v[32:47], a[92:95], v[184:187], v[32:47]
	ds_read_b128 v[184:187], v192 offset:55296
	v_mov_b32_e32 v239, v236
	v_mov_b32_e32 v240, v237
	v_exp_f32_e32 v206, v22
	v_mfma_f32_32x32x16_f16 v[48:63], a[92:95], v[188:191], v[48:63]
	ds_read_b128 v[188:191], v192 offset:56320
	s_add_u32 s44, s34, 0x19000
	s_addc_u32 s45, s35, 0
	s_mov_b32 m0, s59
	s_nop 0
	global_load_lds_dwordx4 v192, s[44:45] sc1
	s_lshl_b32 s64, s71, 3
	s_add_u32 s64, s64, s29
	s_lshl_b32 s64, s64, 7
	s_add_u32 s38, s8, s64
	s_addc_u32 s39, s9, 0
	global_load_dword v251, v196, s[38:39] sc1
	v_mov_b32_e32 v241, v237
	v_cvt_pk_f16_f32 v220, v216, v217
	v_exp_f32_e32 v207, v23
	s_waitcnt lgkmcnt(4)
	v_mfma_f32_32x32x16_f16 v[32:47], a[96:99], v[160:163], v[32:47]
	ds_read_b128 v[160:163], v192 offset:57344
	s_nop 1
	v_permlane32_swap_b32_e32 v238, v239
	v_permlane32_swap_b32_e32 v240, v241
	v_add_f32_e32 v238, v238, v239
	v_add_f32_e32 v239, v240, v241
	ds_write_b64 v248, v[238:239] offset:0
	v_exp_f32_e32 v208, v24
	v_mfma_f32_32x32x16_f16 v[48:63], a[96:99], v[164:167], v[48:63]
	ds_read_b128 v[164:167], v192 offset:58368
	v_cvt_pk_f16_f32 v221, v218, v219
	v_exp_f32_e32 v209, v25
	v_add_f32_e32 v200, 1.0, v200
	v_mfma_f32_32x32x16_f16 v[32:47], a[100:103], v[168:171], v[32:47]
	ds_read_b128 v[168:171], v192 offset:59392
	v_exp_f32_e32 v210, v26
	v_add_f32_e32 v201, 1.0, v201
	v_add_f32_e32 v202, 1.0, v202
	v_mfma_f32_32x32x16_f16 v[48:63], a[100:103], v[172:175], v[48:63]
	ds_read_b128 v[172:175], v192 offset:60416
	global_load_lds_dwordx4 v192, s[44:45] offset:1024 sc1
	v_exp_f32_e32 v211, v27
	v_add_f32_e32 v203, 1.0, v203
	v_add_f32_e32 v204, 1.0, v204
	s_waitcnt lgkmcnt(5)
	v_mfma_f32_32x32x16_f16 v[32:47], a[104:107], v[176:179], v[32:47]
	ds_read_b128 v[176:179], v192 offset:61440
	v_exp_f32_e32 v212, v28
	v_add_f32_e32 v205, 1.0, v205
	v_add_f32_e32 v206, 1.0, v206
	v_mfma_f32_32x32x16_f16 v[48:63], a[104:107], v[180:183], v[48:63]
	ds_read_b128 v[180:183], v192 offset:62464
	v_exp_f32_e32 v213, v29
	v_add_f32_e32 v207, 1.0, v207
	v_add_f32_e32 v208, 1.0, v208
	v_mfma_f32_32x32x16_f16 v[32:47], a[108:111], v[184:187], v[32:47]
	ds_read_b128 v[184:187], v192 offset:63488
	v_exp_f32_e32 v214, v30
	v_add_f32_e32 v209, 1.0, v209
	v_add_f32_e32 v210, 1.0, v210
	v_mfma_f32_32x32x16_f16 v[48:63], a[108:111], v[188:191], v[48:63]
	ds_read_b128 v[188:191], v192 offset:64512
	global_load_lds_dwordx4 v192, s[44:45] offset:2048 sc1
	v_exp_f32_e32 v215, v31
	v_add_f32_e32 v211, 1.0, v211
	v_add_f32_e32 v212, 1.0, v212
	s_waitcnt vmcnt(8)
	s_barrier
	s_waitcnt lgkmcnt(4)
	v_mfma_f32_32x32x16_f16 v[32:47], a[112:115], v[160:163], v[32:47]
	ds_read_b128 v[160:163], v193 offset:0
	v_add_f32_e32 v213, 1.0, v213
	v_add_f32_e32 v214, 1.0, v214
	v_rcp_f32_e32 v200, v200
	v_mfma_f32_32x32x16_f16 v[48:63], a[112:115], v[164:167], v[48:63]
	ds_read_b128 v[164:167], v193 offset:1024
	v_add_f32_e32 v215, 1.0, v215
	v_rcp_f32_e32 v201, v201
	v_mfma_f32_32x32x16_f16 v[32:47], a[116:119], v[168:171], v[32:47]
	ds_read_b128 v[168:171], v193 offset:2048
	v_rcp_f32_e32 v202, v202
	v_mfma_f32_32x32x16_f16 v[48:63], a[116:119], v[172:175], v[48:63]
	ds_read_b128 v[172:175], v193 offset:3072
	global_load_lds_dwordx4 v192, s[44:45] offset:3072 sc1
	v_rcp_f32_e32 v203, v203
	s_waitcnt lgkmcnt(4)
	v_mfma_f32_32x32x16_f16 v[32:47], a[120:123], v[176:179], v[32:47]
	ds_read_b128 v[176:179], v193 offset:4096
	v_rcp_f32_e32 v204, v204
	s_add_u32 s46, s42, 0x6000
	s_addc_u32 s47, s43, 0
	global_load_dwordx4 v[96:99], v192, s[46:47] offset:0
	v_mfma_f32_32x32x16_f16 v[48:63], a[120:123], v[180:183], v[48:63]
	ds_read_b128 v[180:183], v193 offset:5120
	v_rcp_f32_e32 v205, v205
	v_mul_f32_e32 v204, v204, v132
	global_load_dwordx4 v[100:103], v192, s[46:47] offset:1024
	global_load_dwordx4 v[104:107], v192, s[46:47] offset:2048
	v_mfma_f32_32x32x16_f16 v[32:47], a[124:127], v[184:187], v[32:47]
	ds_read_b128 v[184:187], v193 offset:6144
	v_rcp_f32_e32 v206, v206
	v_mul_f32_e32 v205, v205, v133
	global_load_dwordx4 v[108:111], v192, s[46:47] offset:3072
	s_add_u32 s46, s42, 0x7000
	s_addc_u32 s47, s43, 0
	v_mfma_f32_32x32x16_f16 v[48:63], a[124:127], v[188:191], v[48:63]
	ds_read_b128 v[188:191], v193 offset:7168
	s_waitcnt vmcnt(7)
	v_cmp_gt_u32_e32 vcc, 3, v251
	s_cbranch_vccz .LD_tok26

.LD_tok26:
	s_and_b32 s64, s71, 1
	s_lshl_b32 s64, s64, 22
	s_add_u32 s64, s64, s49
	s_add_u32 s64, s64, 0x40000
	s_add_u32 s34, s6, s64
	s_addc_u32 s35, s7, 0
	s_add_u32 s44, s34, 0x0
	s_addc_u32 s45, s35, 0
	s_mov_b32 m0, s52
	s_nop 0
	global_load_lds_dwordx4 v192, s[44:45] sc1
	v_rcp_f32_e32 v207, v207
	v_mul_f32_e32 v206, v206, v134
	global_load_dwordx4 v[112:115], v192, s[46:47] offset:0
	global_load_dwordx4 v[116:119], v192, s[46:47] offset:1024
	s_waitcnt lgkmcnt(4)
	v_mfma_f32_32x32x16_f16 v[32:47], a[128:131], v[160:163], v[32:47]
	ds_read_b128 v[160:163], v193 offset:8192
	v_rcp_f32_e32 v208, v208
	v_mul_f32_e32 v207, v207, v135
	global_load_dwordx4 v[120:123], v192, s[46:47] offset:2048
	global_load_dwordx4 v[124:127], v192, s[46:47] offset:3072
	v_mfma_f32_32x32x16_f16 v[48:63], a[128:131], v[164:167], v[48:63]
	ds_read_b128 v[164:167], v193 offset:9216
	v_rcp_f32_e32 v209, v209
	v_fmamk_f32 v208, v208, 0xc0b8aa3b, v198
	v_mfma_f32_32x32x16_f16 v[32:47], a[132:135], v[168:171], v[32:47]
	ds_read_b128 v[168:171], v193 offset:10240
	v_rcp_f32_e32 v210, v210
	v_fmamk_f32 v209, v209, 0xc0b8aa3b, v198
	v_fma_f32 v132, v200, v208, v204
	v_mfma_f32_32x32x16_f16 v[48:63], a[132:135], v[172:175], v[48:63]
	ds_read_b128 v[172:175], v193 offset:11264
	global_load_lds_dwordx4 v192, s[44:45] offset:1024 sc1
	v_rcp_f32_e32 v211, v211
	v_fmamk_f32 v210, v210, 0xc0b8aa3b, v198
	v_fma_f32 v133, v201, v209, v205
	s_waitcnt lgkmcnt(4)
	v_mfma_f32_32x32x16_f16 v[32:47], a[136:139], v[176:179], v[32:47]
	ds_read_b128 v[176:179], v193 offset:12288
	v_rcp_f32_e32 v212, v212
	v_fmamk_f32 v211, v211, 0xc0b8aa3b, v198
	v_fma_f32 v134, v202, v210, v206
	v_mfma_f32_32x32x16_f16 v[48:63], a[136:139], v[180:183], v[48:63]
	ds_read_b128 v[180:183], v193 offset:13312
	v_rcp_f32_e32 v213, v213
	v_fma_f32 v135, v203, v211, v207
	v_mfma_f32_32x32x16_f16 v[32:47], a[140:143], v[184:187], v[32:47]
	ds_read_b128 v[184:187], v193 offset:14336
	v_rcp_f32_e32 v214, v214
	v_mfma_f32_32x32x16_f16 v[48:63], a[140:143], v[188:191], v[48:63]
	ds_read_b128 v[188:191], v193 offset:15360
	global_load_lds_dwordx4 v192, s[44:45] offset:2048 sc1
	v_rcp_f32_e32 v215, v215
	s_waitcnt lgkmcnt(4)
	v_mfma_f32_32x32x16_f16 v[32:47], a[144:147], v[160:163], v[32:47]
	ds_read_b128 v[160:163], v193 offset:16384
	v_exp_f32_e32 v200, v132
	v_mfma_f32_32x32x16_f16 v[48:63], a[144:147], v[164:167], v[48:63]
	ds_read_b128 v[164:167], v193 offset:17408
	v_exp_f32_e32 v201, v133
	v_add_f32_e32 v200, 1.0, v200
	v_mfma_f32_32x32x16_f16 v[32:47], a[148:151], v[168:171], v[32:47]
	ds_read_b128 v[168:171], v193 offset:18432
	v_exp_f32_e32 v202, v134
	v_add_f32_e32 v201, 1.0, v201
	v_mfma_f32_32x32x16_f16 v[48:63], a[148:151], v[172:175], v[48:63]
	ds_read_b128 v[172:175], v193 offset:19456
	global_load_lds_dwordx4 v192, s[44:45] offset:3072 sc1
	v_exp_f32_e32 v203, v135
	v_add_f32_e32 v202, 1.0, v202
	s_waitcnt lgkmcnt(4)
	v_mfma_f32_32x32x16_f16 v[32:47], a[152:155], v[176:179], v[32:47]
	ds_read_b128 v[176:179], v193 offset:20480
	v_add_f32_e32 v203, 1.0, v203
	v_rcp_f32_e32 v200, v200
	v_mfma_f32_32x32x16_f16 v[48:63], a[152:155], v[180:183], v[48:63]
	ds_read_b128 v[180:183], v193 offset:21504
	v_rcp_f32_e32 v201, v201
	v_fma_f32 v200, v200, 2.0, -1.0
	v_mfma_f32_32x32x16_f16 v[32:47], a[156:159], v[184:187], v[32:47]
	ds_read_b128 v[184:187], v193 offset:22528
	v_rcp_f32_e32 v202, v202
	v_fma_f32 v201, v201, 2.0, -1.0
	v_mul_f32_e32 v216, v212, v200
	v_mfma_f32_32x32x16_f16 v[48:63], a[156:159], v[188:191], v[48:63]
	ds_read_b128 v[188:191], v193 offset:23552
	s_add_u32 s44, s34, 0x1000
	s_addc_u32 s45, s35, 0
	s_mov_b32 m0, s53
	s_nop 0
	global_load_lds_dwordx4 v192, s[44:45] sc1
	v_rcp_f32_e32 v203, v203
	v_fma_f32 v202, v202, 2.0, -1.0
	v_mul_f32_e32 v217, v213, v201
	s_waitcnt lgkmcnt(4)
	v_mfma_f32_32x32x16_f16 v[32:47], a[160:163], v[160:163], v[32:47]
	ds_read_b128 v[160:163], v193 offset:24576
	v_fma_f32 v203, v203, 2.0, -1.0
	v_mul_f32_e32 v218, v214, v202
	v_mfma_f32_32x32x16_f16 v[48:63], a[160:163], v[164:167], v[48:63]
	ds_read_b128 v[164:167], v193 offset:25600
	v_mul_f32_e32 v219, v215, v203
	v_mul_f32_e32 v236, v216, v228
	v_mfma_f32_32x32x16_f16 v[32:47], a[164:167], v[168:171], v[32:47]
	ds_read_b128 v[168:171], v193 offset:26624
	v_mul_f32_e32 v237, v216, v232
	v_fmac_f32_e32 v236, v217, v229
	v_mfma_f32_32x32x16_f16 v[48:63], a[164:167], v[172:175], v[48:63]
	ds_read_b128 v[172:175], v193 offset:27648
	global_load_lds_dwordx4 v192, s[44:45] offset:1024 sc1
	v_fmac_f32_e32 v237, v217, v233
	v_fmac_f32_e32 v236, v218, v230
	s_waitcnt lgkmcnt(4)
	v_mfma_f32_32x32x16_f16 v[32:47], a[168:171], v[176:179], v[32:47]
	ds_read_b128 v[176:179], v193 offset:28672
	v_fmac_f32_e32 v237, v218, v234
	v_fmac_f32_e32 v236, v219, v231
	v_mfma_f32_32x32x16_f16 v[48:63], a[168:171], v[180:183], v[48:63]
	ds_read_b128 v[180:183], v193 offset:29696
	v_fmac_f32_e32 v237, v219, v235
	v_mov_b32_e32 v238, v236
	v_mfma_f32_32x32x16_f16 v[32:47], a[172:175], v[184:187], v[32:47]
	ds_read_b128 v[184:187], v193 offset:30720
	v_mov_b32_e32 v239, v236
	v_mov_b32_e32 v240, v237
	v_mfma_f32_32x32x16_f16 v[48:63], a[172:175], v[188:191], v[48:63]
	ds_read_b128 v[188:191], v193 offset:31744
	global_load_lds_dwordx4 v192, s[44:45] offset:2048 sc1
	v_mov_b32_e32 v241, v237
	v_cvt_pk_f16_f32 v222, v216, v217
	s_waitcnt vmcnt(15)
	s_barrier
	s_waitcnt lgkmcnt(4)
	v_mfma_f32_32x32x16_f16 v[32:47], a[176:179], v[160:163], v[32:47]
	ds_read_b128 v[160:163], v193 offset:32768
	s_nop 1
	v_permlane32_swap_b32_e32 v238, v239
	v_permlane32_swap_b32_e32 v240, v241
	v_add_f32_e32 v238, v238, v239
	v_add_f32_e32 v239, v240, v241
	ds_write_b64 v248, v[238:239] offset:256
	v_mfma_f32_32x32x16_f16 v[48:63], a[176:179], v[164:167], v[48:63]
	ds_read_b128 v[164:167], v193 offset:33792
	v_cvt_pk_f16_f32 v223, v218, v219
	v_mfma_f32_32x32x16_f16 v[32:47], a[180:183], v[168:171], v[32:47]
	ds_read_b128 v[168:171], v193 offset:34816
	s_nop 1
	v_permlane32_swap_b32_e32 v220, v222
	v_permlane32_swap_b32_e32 v221, v223
	s_cmp_eq_u32 s31, 0
	s_cbranch_scc1 .LD_slow28
	global_store_dwordx4 v195, v[220:223], s[36:37] offset:0
	s_branch .LD_join29

.LD_join31:
	ds_read_b64 v[200:201], v249 offset:0
	ds_read_b64 v[202:203], v249 offset:2048
	ds_read_b64 v[204:205], v249 offset:4096
	ds_read_b64 v[206:207], v249 offset:6144
	s_waitcnt lgkmcnt(8)
	v_mfma_f32_32x32x16_f16 v[32:47], a[208:211], v[160:163], v[32:47]
	ds_read_b128 v[160:163], v193 offset:49152
	v_mfma_f32_32x32x16_f16 v[48:63], a[208:211], v[164:167], v[48:63]
	ds_read_b128 v[164:167], v193 offset:50176
	v_mfma_f32_32x32x16_f16 v[32:47], a[212:215], v[168:171], v[32:47]
	ds_read_b128 v[168:171], v193 offset:51200
	v_mfma_f32_32x32x16_f16 v[48:63], a[212:215], v[172:175], v[48:63]
	ds_read_b128 v[172:175], v193 offset:52224
	global_load_lds_dwordx4 v192, s[44:45] offset:3072 sc1
	s_waitcnt lgkmcnt(8)
	v_mfma_f32_32x32x16_f16 v[32:47], a[216:219], v[176:179], v[32:47]
	ds_read_b128 v[176:179], v193 offset:53248
	v_mfma_f32_32x32x16_f16 v[48:63], a[216:219], v[180:183], v[48:63]
	ds_read_b128 v[180:183], v193 offset:54272
	v_mfma_f32_32x32x16_f16 v[32:47], a[220:223], v[184:187], v[32:47]
	ds_read_b128 v[184:187], v193 offset:55296
	v_mfma_f32_32x32x16_f16 v[48:63], a[220:223], v[188:191], v[48:63]
	ds_read_b128 v[188:191], v193 offset:56320
	s_add_u32 s44, s34, 0x9000
	s_addc_u32 s45, s35, 0
	s_mov_b32 m0, s55
	s_nop 0
	global_load_lds_dwordx4 v192, s[44:45] sc1
	s_waitcnt lgkmcnt(4)
	v_mfma_f32_32x32x16_f16 v[32:47], a[224:227], v[160:163], v[32:47]
	ds_read_b128 v[160:163], v193 offset:57344
	v_mfma_f32_32x32x16_f16 v[48:63], a[224:227], v[164:167], v[48:63]
	ds_read_b128 v[164:167], v193 offset:58368
	v_mfma_f32_32x32x16_f16 v[32:47], a[228:231], v[168:171], v[32:47]
	ds_read_b128 v[168:171], v193 offset:59392
	v_mfma_f32_32x32x16_f16 v[48:63], a[228:231], v[172:175], v[48:63]
	ds_read_b128 v[172:175], v193 offset:60416
	global_load_lds_dwordx4 v192, s[44:45] offset:1024 sc1
	v_add_f32_e32 v200, v200, v202
	v_add_f32_e32 v201, v201, v203
	v_add_f32_e32 v200, v200, v204
	v_add_f32_e32 v201, v201, v205
	v_add_f32_e32 v200, v200, v206
	v_add_f32_e32 v201, v201, v207
	global_store_dwordx2 v250, v[200:201], s[72:73]
	s_waitcnt lgkmcnt(4)
	v_mfma_f32_32x32x16_f16 v[32:47], a[232:235], v[176:179], v[32:47]
	ds_read_b128 v[176:179], v193 offset:61440
	v_mfma_f32_32x32x16_f16 v[48:63], a[232:235], v[180:183], v[48:63]
	ds_read_b128 v[180:183], v193 offset:62464
	v_mfma_f32_32x32x16_f16 v[32:47], a[236:239], v[184:187], v[32:47]
	ds_read_b128 v[184:187], v193 offset:63488
	v_mfma_f32_32x32x16_f16 v[48:63], a[236:239], v[188:191], v[48:63]
	ds_read_b128 v[188:191], v193 offset:64512
	global_load_lds_dwordx4 v192, s[44:45] offset:2048 sc1
	s_waitcnt vmcnt(9)
	s_barrier
	s_waitcnt lgkmcnt(4)
	v_mfma_f32_32x32x16_f16 v[32:47], a[240:243], v[160:163], v[32:47]
	ds_read_b128 v[160:163], v192 offset:0
	v_mfma_f32_32x32x16_f16 v[48:63], a[240:243], v[164:167], v[48:63]
	ds_read_b128 v[164:167], v192 offset:1024
	v_mfma_f32_32x32x16_f16 v[32:47], a[244:247], v[168:171], v[32:47]
	ds_read_b128 v[168:171], v192 offset:2048
	v_mfma_f32_32x32x16_f16 v[48:63], a[244:247], v[172:175], v[48:63]
	ds_read_b128 v[172:175], v192 offset:3072
	global_load_lds_dwordx4 v192, s[44:45] offset:3072 sc1
	s_waitcnt lgkmcnt(4)
	v_mfma_f32_32x32x16_f16 v[32:47], a[248:251], v[176:179], v[32:47]
	ds_read_b128 v[176:179], v192 offset:4096
	v_mfma_f32_32x32x16_f16 v[48:63], a[248:251], v[180:183], v[48:63]
	ds_read_b128 v[180:183], v192 offset:5120
	v_mfma_f32_32x32x16_f16 v[32:47], a[252:255], v[184:187], v[32:47]
	ds_read_b128 v[184:187], v192 offset:6144
	v_mfma_f32_32x32x16_f16 v[48:63], a[252:255], v[188:191], v[48:63]
	ds_read_b128 v[188:191], v192 offset:7168
	s_add_u32 s44, s34, 0x10000
	s_addc_u32 s45, s35, 0
	s_mov_b32 m0, s56
	s_nop 0
	global_load_lds_dwordx4 v192, s[44:45] sc1
	s_and_b32 s64, s33, 1
	s_lshl_b32 s64, s64, 22
	s_add_u32 s64, s64, s50
	s_add_u32 s64, s64, 0x20000
	s_add_u32 s36, s6, s64
	s_addc_u32 s37, s7, 0
	s_lshl_b32 s64, s33, 3
	s_add_u32 s64, s64, s29
	s_lshl_b32 s64, s64, 5
	s_add_u32 s64, s64, s30
	s_lshl_b32 s64, s64, 2
	s_add_u32 s40, s8, s64
	s_addc_u32 s41, s9, 0
	s_lshl_b32 s64, s33, 19
	s_add_u32 s64, s64, 0x200
	s_add_u32 s72, s62, s64
	s_addc_u32 s73, s63, 0
	s_nop 3
	s_waitcnt lgkmcnt(4)
	v_mfma_f32_32x32x16_f16 v[64:79], a[0:3], v[160:163], v[64:79]
	ds_read_b128 v[160:163], v192 offset:8192
	v_exp_f32_e32 v200, v32
	v_mfma_f32_32x32x16_f16 v[80:95], a[0:3], v[164:167], v[80:95]
	ds_read_b128 v[164:167], v192 offset:9216
	v_exp_f32_e32 v201, v33
	v_add_f32_e32 v200, 1.0, v200
	v_mfma_f32_32x32x16_f16 v[64:79], a[4:7], v[168:171], v[64:79]
	ds_read_b128 v[168:171], v192 offset:10240
	v_exp_f32_e32 v202, v34
	v_add_f32_e32 v201, 1.0, v201
	v_mfma_f32_32x32x16_f16 v[80:95], a[4:7], v[172:175], v[80:95]
	ds_read_b128 v[172:175], v192 offset:11264
	global_load_lds_dwordx4 v192, s[44:45] offset:1024 sc1
	v_exp_f32_e32 v203, v35
	v_add_f32_e32 v202, 1.0, v202
	s_waitcnt lgkmcnt(4)
	v_mfma_f32_32x32x16_f16 v[64:79], a[8:11], v[176:179], v[64:79]
	ds_read_b128 v[176:179], v192 offset:12288
	v_exp_f32_e32 v204, v36
	v_add_f32_e32 v203, 1.0, v203
	v_mfma_f32_32x32x16_f16 v[80:95], a[8:11], v[180:183], v[80:95]
	ds_read_b128 v[180:183], v192 offset:13312
	v_exp_f32_e32 v205, v37
	v_add_f32_e32 v204, 1.0, v204
	v_mfma_f32_32x32x16_f16 v[64:79], a[12:15], v[184:187], v[64:79]
	ds_read_b128 v[184:187], v192 offset:14336
	v_exp_f32_e32 v206, v38
	v_add_f32_e32 v205, 1.0, v205
	v_mfma_f32_32x32x16_f16 v[80:95], a[12:15], v[188:191], v[80:95]
	ds_read_b128 v[188:191], v192 offset:15360
	global_load_lds_dwordx4 v192, s[44:45] offset:2048 sc1
	v_exp_f32_e32 v207, v39
	v_add_f32_e32 v206, 1.0, v206
	s_waitcnt lgkmcnt(4)
	v_mfma_f32_32x32x16_f16 v[64:79], a[16:19], v[160:163], v[64:79]
	ds_read_b128 v[160:163], v192 offset:16384
	v_exp_f32_e32 v208, v40
	v_add_f32_e32 v207, 1.0, v207
	v_mfma_f32_32x32x16_f16 v[80:95], a[16:19], v[164:167], v[80:95]
	ds_read_b128 v[164:167], v192 offset:17408
	v_exp_f32_e32 v209, v41
	v_add_f32_e32 v208, 1.0, v208
	v_mfma_f32_32x32x16_f16 v[64:79], a[20:23], v[168:171], v[64:79]
	ds_read_b128 v[168:171], v192 offset:18432
	v_exp_f32_e32 v210, v42
	v_add_f32_e32 v209, 1.0, v209
	v_mfma_f32_32x32x16_f16 v[80:95], a[20:23], v[172:175], v[80:95]
	ds_read_b128 v[172:175], v192 offset:19456
	global_load_lds_dwordx4 v192, s[44:45] offset:3072 sc1
	v_exp_f32_e32 v211, v43
	v_add_f32_e32 v210, 1.0, v210
	s_waitcnt lgkmcnt(4)
	v_mfma_f32_32x32x16_f16 v[64:79], a[24:27], v[176:179], v[64:79]
	ds_read_b128 v[176:179], v192 offset:20480
	v_exp_f32_e32 v212, v44
	v_add_f32_e32 v211, 1.0, v211
	v_mfma_f32_32x32x16_f16 v[80:95], a[24:27], v[180:183], v[80:95]
	ds_read_b128 v[180:183], v192 offset:21504
	v_exp_f32_e32 v213, v45
	v_add_f32_e32 v212, 1.0, v212
	v_mfma_f32_32x32x16_f16 v[64:79], a[28:31], v[184:187], v[64:79]
	ds_read_b128 v[184:187], v192 offset:22528
	v_exp_f32_e32 v214, v46
	v_add_f32_e32 v213, 1.0, v213
	v_mfma_f32_32x32x16_f16 v[80:95], a[28:31], v[188:191], v[80:95]
	ds_read_b128 v[188:191], v192 offset:23552
	s_add_u32 s44, s34, 0x11000
	s_addc_u32 s45, s35, 0
	s_mov_b32 m0, s57
	s_nop 0
	global_load_lds_dwordx4 v192, s[44:45] sc1
	v_exp_f32_e32 v215, v47
	v_add_f32_e32 v214, 1.0, v214
	s_waitcnt lgkmcnt(4)
	v_mfma_f32_32x32x16_f16 v[64:79], a[32:35], v[160:163], v[64:79]
	ds_read_b128 v[160:163], v192 offset:24576
	v_add_f32_e32 v215, 1.0, v215
	v_rcp_f32_e32 v200, v200
	v_mfma_f32_32x32x16_f16 v[80:95], a[32:35], v[164:167], v[80:95]
	ds_read_b128 v[164:167], v192 offset:25600
	v_rcp_f32_e32 v201, v201
	v_mfma_f32_32x32x16_f16 v[64:79], a[36:39], v[168:171], v[64:79]
	ds_read_b128 v[168:171], v192 offset:26624
	v_rcp_f32_e32 v202, v202
	v_mfma_f32_32x32x16_f16 v[80:95], a[36:39], v[172:175], v[80:95]
	ds_read_b128 v[172:175], v192 offset:27648
	global_load_lds_dwordx4 v192, s[44:45] offset:1024 sc1
	v_rcp_f32_e32 v203, v203
	s_waitcnt lgkmcnt(4)
	v_mfma_f32_32x32x16_f16 v[64:79], a[40:43], v[176:179], v[64:79]
	ds_read_b128 v[176:179], v192 offset:28672
	v_rcp_f32_e32 v204, v204
	v_mfma_f32_32x32x16_f16 v[80:95], a[40:43], v[180:183], v[80:95]
	ds_read_b128 v[180:183], v192 offset:29696
	v_rcp_f32_e32 v205, v205
	v_mul_f32_e32 v204, v204, v136
	v_mfma_f32_32x32x16_f16 v[64:79], a[44:47], v[184:187], v[64:79]
	ds_read_b128 v[184:187], v192 offset:30720
	v_rcp_f32_e32 v206, v206
	v_mul_f32_e32 v205, v205, v137
	v_mfma_f32_32x32x16_f16 v[80:95], a[44:47], v[188:191], v[80:95]
	ds_read_b128 v[188:191], v192 offset:31744
	global_load_lds_dwordx4 v192, s[44:45] offset:2048 sc1
	v_rcp_f32_e32 v207, v207
	v_mul_f32_e32 v206, v206, v138
	s_waitcnt vmcnt(7)
	s_barrier
	s_waitcnt lgkmcnt(4)
	v_mfma_f32_32x32x16_f16 v[64:79], a[48:51], v[160:163], v[64:79]
	ds_read_b128 v[160:163], v192 offset:32768
	v_rcp_f32_e32 v208, v208
	v_mul_f32_e32 v207, v207, v139
	v_mfma_f32_32x32x16_f16 v[80:95], a[48:51], v[164:167], v[80:95]
	ds_read_b128 v[164:167], v192 offset:33792
	v_rcp_f32_e32 v209, v209
	v_fmamk_f32 v208, v208, 0xc0b8aa3b, v198
	v_mfma_f32_32x32x16_f16 v[64:79], a[52:55], v[168:171], v[64:79]
	ds_read_b128 v[168:171], v192 offset:34816
	v_rcp_f32_e32 v210, v210
	v_fmamk_f32 v209, v209, 0xc0b8aa3b, v198
	v_fma_f32 v136, v200, v208, v204
	v_mfma_f32_32x32x16_f16 v[80:95], a[52:55], v[172:175], v[80:95]
	ds_read_b128 v[172:175], v192 offset:35840
	global_load_lds_dwordx4 v192, s[44:45] offset:3072 sc1
	v_rcp_f32_e32 v211, v211
	v_fmamk_f32 v210, v210, 0xc0b8aa3b, v198
	v_fma_f32 v137, v201, v209, v205
	s_waitcnt lgkmcnt(4)
	v_mfma_f32_32x32x16_f16 v[64:79], a[56:59], v[176:179], v[64:79]
	ds_read_b128 v[176:179], v192 offset:36864
	v_rcp_f32_e32 v212, v212
	v_fmamk_f32 v211, v211, 0xc0b8aa3b, v198
	v_fma_f32 v138, v202, v210, v206
	v_mfma_f32_32x32x16_f16 v[80:95], a[56:59], v[180:183], v[80:95]
	ds_read_b128 v[180:183], v192 offset:37888
	v_rcp_f32_e32 v213, v213
	v_fma_f32 v139, v203, v211, v207
	v_mfma_f32_32x32x16_f16 v[64:79], a[60:63], v[184:187], v[64:79]
	ds_read_b128 v[184:187], v192 offset:38912
	v_rcp_f32_e32 v214, v214
	v_mfma_f32_32x32x16_f16 v[80:95], a[60:63], v[188:191], v[80:95]
	ds_read_b128 v[188:191], v192 offset:39936
	s_add_u32 s44, s34, 0x18000
	s_addc_u32 s45, s35, 0
	s_mov_b32 m0, s58
	s_nop 0
	global_load_lds_dwordx4 v192, s[44:45] sc1
	v_rcp_f32_e32 v215, v215
	s_waitcnt lgkmcnt(4)
	v_mfma_f32_32x32x16_f16 v[64:79], a[64:67], v[160:163], v[64:79]
	ds_read_b128 v[160:163], v192 offset:40960
	v_exp_f32_e32 v200, v136
	v_mfma_f32_32x32x16_f16 v[80:95], a[64:67], v[164:167], v[80:95]
	ds_read_b128 v[164:167], v192 offset:41984
	v_exp_f32_e32 v201, v137
	v_add_f32_e32 v200, 1.0, v200
	v_mfma_f32_32x32x16_f16 v[64:79], a[68:71], v[168:171], v[64:79]
	ds_read_b128 v[168:171], v192 offset:43008
	v_exp_f32_e32 v202, v138
	v_add_f32_e32 v201, 1.0, v201
	v_mfma_f32_32x32x16_f16 v[80:95], a[68:71], v[172:175], v[80:95]
	ds_read_b128 v[172:175], v192 offset:44032
	global_load_lds_dwordx4 v192, s[44:45] offset:1024 sc1
	v_exp_f32_e32 v203, v139
	v_add_f32_e32 v202, 1.0, v202
	s_waitcnt lgkmcnt(4)
	v_mfma_f32_32x32x16_f16 v[64:79], a[72:75], v[176:179], v[64:79]
	ds_read_b128 v[176:179], v192 offset:45056
	v_add_f32_e32 v203, 1.0, v203
	v_rcp_f32_e32 v200, v200
	v_mfma_f32_32x32x16_f16 v[80:95], a[72:75], v[180:183], v[80:95]
	ds_read_b128 v[180:183], v192 offset:46080
	v_rcp_f32_e32 v201, v201
	v_fma_f32 v200, v200, 2.0, -1.0
	v_mfma_f32_32x32x16_f16 v[64:79], a[76:79], v[184:187], v[64:79]
	ds_read_b128 v[184:187], v192 offset:47104
	v_rcp_f32_e32 v202, v202
	v_fma_f32 v201, v201, 2.0, -1.0
	v_mul_f32_e32 v216, v212, v200
	v_mfma_f32_32x32x16_f16 v[80:95], a[76:79], v[188:191], v[80:95]
	ds_read_b128 v[188:191], v192 offset:48128
	global_load_lds_dwordx4 v192, s[44:45] offset:2048 sc1
	v_rcp_f32_e32 v203, v203
	v_fma_f32 v202, v202, 2.0, -1.0
	v_mul_f32_e32 v217, v213, v201
	s_waitcnt lgkmcnt(4)
	v_mfma_f32_32x32x16_f16 v[64:79], a[80:83], v[160:163], v[64:79]
	ds_read_b128 v[160:163], v192 offset:49152
	v_fma_f32 v203, v203, 2.0, -1.0
	v_mul_f32_e32 v218, v214, v202
	v_exp_f32_e32 v200, v48
	v_mfma_f32_32x32x16_f16 v[80:95], a[80:83], v[164:167], v[80:95]
	ds_read_b128 v[164:167], v192 offset:50176
	v_mul_f32_e32 v219, v215, v203
	v_mul_f32_e32 v236, v216, v228
	v_exp_f32_e32 v201, v49
	v_mfma_f32_32x32x16_f16 v[64:79], a[84:87], v[168:171], v[64:79]
	ds_read_b128 v[168:171], v192 offset:51200
	v_mul_f32_e32 v237, v216, v232
	v_fmac_f32_e32 v236, v217, v229
	v_exp_f32_e32 v202, v50
	v_mfma_f32_32x32x16_f16 v[80:95], a[84:87], v[172:175], v[80:95]
	ds_read_b128 v[172:175], v192 offset:52224
	global_load_lds_dwordx4 v192, s[44:45] offset:3072 sc1
	v_fmac_f32_e32 v237, v217, v233
	v_fmac_f32_e32 v236, v218, v230
	v_exp_f32_e32 v203, v51
	s_waitcnt lgkmcnt(4)
	v_mfma_f32_32x32x16_f16 v[64:79], a[88:91], v[176:179], v[64:79]
	ds_read_b128 v[176:179], v192 offset:53248
	v_fmac_f32_e32 v237, v218, v234
	v_fmac_f32_e32 v236, v219, v231
	v_exp_f32_e32 v204, v52
	v_mfma_f32_32x32x16_f16 v[80:95], a[88:91], v[180:183], v[80:95]
	ds_read_b128 v[180:183], v192 offset:54272
	v_fmac_f32_e32 v237, v219, v235
	v_mov_b32_e32 v238, v236
	v_exp_f32_e32 v205, v53
	v_mfma_f32_32x32x16_f16 v[64:79], a[92:95], v[184:187], v[64:79]
	ds_read_b128 v[184:187], v192 offset:55296
	v_mov_b32_e32 v239, v236
	v_mov_b32_e32 v240, v237
	v_exp_f32_e32 v206, v54
	v_mfma_f32_32x32x16_f16 v[80:95], a[92:95], v[188:191], v[80:95]
	ds_read_b128 v[188:191], v192 offset:56320
	s_add_u32 s44, s34, 0x19000
	s_addc_u32 s45, s35, 0
	s_mov_b32 m0, s59
	s_nop 0
	global_load_lds_dwordx4 v192, s[44:45] sc1
	s_lshl_b32 s64, s71, 3
	s_add_u32 s64, s64, s29
	s_lshl_b32 s64, s64, 7
	s_add_u32 s38, s8, s64
	s_addc_u32 s39, s9, 0
	global_load_dword v251, v196, s[38:39] sc1
	v_mov_b32_e32 v241, v237
	v_cvt_pk_f16_f32 v220, v216, v217
	v_exp_f32_e32 v207, v55
	s_waitcnt lgkmcnt(4)
	v_mfma_f32_32x32x16_f16 v[64:79], a[96:99], v[160:163], v[64:79]
	ds_read_b128 v[160:163], v192 offset:57344
	s_nop 1
	v_permlane32_swap_b32_e32 v238, v239
	v_permlane32_swap_b32_e32 v240, v241
	v_add_f32_e32 v238, v238, v239
	v_add_f32_e32 v239, v240, v241
	ds_write_b64 v248, v[238:239] offset:512
	v_exp_f32_e32 v208, v56
	v_mfma_f32_32x32x16_f16 v[80:95], a[96:99], v[164:167], v[80:95]
	ds_read_b128 v[164:167], v192 offset:58368
	v_cvt_pk_f16_f32 v221, v218, v219
	v_exp_f32_e32 v209, v57
	v_add_f32_e32 v200, 1.0, v200
	v_mfma_f32_32x32x16_f16 v[64:79], a[100:103], v[168:171], v[64:79]
	ds_read_b128 v[168:171], v192 offset:59392
	v_exp_f32_e32 v210, v58
	v_add_f32_e32 v201, 1.0, v201
	v_add_f32_e32 v202, 1.0, v202
	v_mfma_f32_32x32x16_f16 v[80:95], a[100:103], v[172:175], v[80:95]
	ds_read_b128 v[172:175], v192 offset:60416
	global_load_lds_dwordx4 v192, s[44:45] offset:1024 sc1
	v_exp_f32_e32 v211, v59
	v_add_f32_e32 v203, 1.0, v203
	v_add_f32_e32 v204, 1.0, v204
	s_waitcnt lgkmcnt(5)
	v_mfma_f32_32x32x16_f16 v[64:79], a[104:107], v[176:179], v[64:79]
	ds_read_b128 v[176:179], v192 offset:61440
	v_exp_f32_e32 v212, v60
	v_add_f32_e32 v205, 1.0, v205
	v_add_f32_e32 v206, 1.0, v206
	v_mfma_f32_32x32x16_f16 v[80:95], a[104:107], v[180:183], v[80:95]
	ds_read_b128 v[180:183], v192 offset:62464
	v_exp_f32_e32 v213, v61
	v_add_f32_e32 v207, 1.0, v207
	v_add_f32_e32 v208, 1.0, v208
	v_mfma_f32_32x32x16_f16 v[64:79], a[108:111], v[184:187], v[64:79]
	ds_read_b128 v[184:187], v192 offset:63488
	v_exp_f32_e32 v214, v62
	v_add_f32_e32 v209, 1.0, v209
	v_add_f32_e32 v210, 1.0, v210
	v_mfma_f32_32x32x16_f16 v[80:95], a[108:111], v[188:191], v[80:95]
	ds_read_b128 v[188:191], v192 offset:64512
	global_load_lds_dwordx4 v192, s[44:45] offset:2048 sc1
	v_exp_f32_e32 v215, v63
	v_add_f32_e32 v211, 1.0, v211
	v_add_f32_e32 v212, 1.0, v212
	s_waitcnt vmcnt(8)
	s_barrier
	s_waitcnt lgkmcnt(4)
	v_mfma_f32_32x32x16_f16 v[64:79], a[112:115], v[160:163], v[64:79]
	ds_read_b128 v[160:163], v193 offset:0
	v_add_f32_e32 v213, 1.0, v213
	v_add_f32_e32 v214, 1.0, v214
	v_rcp_f32_e32 v200, v200
	v_mfma_f32_32x32x16_f16 v[80:95], a[112:115], v[164:167], v[80:95]
	ds_read_b128 v[164:167], v193 offset:1024
	v_add_f32_e32 v215, 1.0, v215
	v_rcp_f32_e32 v201, v201
	v_mfma_f32_32x32x16_f16 v[64:79], a[116:119], v[168:171], v[64:79]
	ds_read_b128 v[168:171], v193 offset:2048
	v_rcp_f32_e32 v202, v202
	v_mfma_f32_32x32x16_f16 v[80:95], a[116:119], v[172:175], v[80:95]
	ds_read_b128 v[172:175], v193 offset:3072
	global_load_lds_dwordx4 v192, s[44:45] offset:3072 sc1
	v_rcp_f32_e32 v203, v203
	s_waitcnt lgkmcnt(4)
	v_mfma_f32_32x32x16_f16 v[64:79], a[120:123], v[176:179], v[64:79]
	ds_read_b128 v[176:179], v193 offset:4096
	v_rcp_f32_e32 v204, v204
	s_add_u32 s46, s42, 0x0
	s_addc_u32 s47, s43, 0
	global_load_dwordx4 v[0:3], v192, s[46:47] offset:0
	v_mfma_f32_32x32x16_f16 v[80:95], a[120:123], v[180:183], v[80:95]
	ds_read_b128 v[180:183], v193 offset:5120
	v_rcp_f32_e32 v205, v205
	v_mul_f32_e32 v204, v204, v140
	global_load_dwordx4 v[4:7], v192, s[46:47] offset:1024
	global_load_dwordx4 v[8:11], v192, s[46:47] offset:2048
	v_mfma_f32_32x32x16_f16 v[64:79], a[124:127], v[184:187], v[64:79]
	ds_read_b128 v[184:187], v193 offset:6144
	v_rcp_f32_e32 v206, v206
	v_mul_f32_e32 v205, v205, v141
	global_load_dwordx4 v[12:15], v192, s[46:47] offset:3072
	s_add_u32 s46, s42, 0x1000
	s_addc_u32 s47, s43, 0
	v_mfma_f32_32x32x16_f16 v[80:95], a[124:127], v[188:191], v[80:95]
	ds_read_b128 v[188:191], v193 offset:7168
	s_waitcnt vmcnt(7)
	v_cmp_gt_u32_e32 vcc, 4, v251
	s_cbranch_vccz .LD_tok32

.LD_tok32:
	s_and_b32 s64, s71, 1
	s_lshl_b32 s64, s64, 22
	s_add_u32 s64, s64, s49
	s_add_u32 s64, s64, 0x60000
	s_add_u32 s34, s6, s64
	s_addc_u32 s35, s7, 0
	s_add_u32 s44, s34, 0x0
	s_addc_u32 s45, s35, 0
	s_mov_b32 m0, s52
	s_nop 0
	global_load_lds_dwordx4 v192, s[44:45] sc1
	v_rcp_f32_e32 v207, v207
	v_mul_f32_e32 v206, v206, v142
	global_load_dwordx4 v[16:19], v192, s[46:47] offset:0
	global_load_dwordx4 v[20:23], v192, s[46:47] offset:1024
	s_waitcnt lgkmcnt(4)
	v_mfma_f32_32x32x16_f16 v[64:79], a[128:131], v[160:163], v[64:79]
	ds_read_b128 v[160:163], v193 offset:8192
	v_rcp_f32_e32 v208, v208
	v_mul_f32_e32 v207, v207, v143
	global_load_dwordx4 v[24:27], v192, s[46:47] offset:2048
	global_load_dwordx4 v[28:31], v192, s[46:47] offset:3072
	v_mfma_f32_32x32x16_f16 v[80:95], a[128:131], v[164:167], v[80:95]
	ds_read_b128 v[164:167], v193 offset:9216
	v_rcp_f32_e32 v209, v209
	v_fmamk_f32 v208, v208, 0xc0b8aa3b, v198
	v_mfma_f32_32x32x16_f16 v[64:79], a[132:135], v[168:171], v[64:79]
	ds_read_b128 v[168:171], v193 offset:10240
	v_rcp_f32_e32 v210, v210
	v_fmamk_f32 v209, v209, 0xc0b8aa3b, v198
	v_fma_f32 v140, v200, v208, v204
	v_mfma_f32_32x32x16_f16 v[80:95], a[132:135], v[172:175], v[80:95]
	ds_read_b128 v[172:175], v193 offset:11264
	global_load_lds_dwordx4 v192, s[44:45] offset:1024 sc1
	v_rcp_f32_e32 v211, v211
	v_fmamk_f32 v210, v210, 0xc0b8aa3b, v198
	v_fma_f32 v141, v201, v209, v205
	s_waitcnt lgkmcnt(4)
	v_mfma_f32_32x32x16_f16 v[64:79], a[136:139], v[176:179], v[64:79]
	ds_read_b128 v[176:179], v193 offset:12288
	v_rcp_f32_e32 v212, v212
	v_fmamk_f32 v211, v211, 0xc0b8aa3b, v198
	v_fma_f32 v142, v202, v210, v206
	v_mfma_f32_32x32x16_f16 v[80:95], a[136:139], v[180:183], v[80:95]
	ds_read_b128 v[180:183], v193 offset:13312
	v_rcp_f32_e32 v213, v213
	v_fma_f32 v143, v203, v211, v207
	v_mfma_f32_32x32x16_f16 v[64:79], a[140:143], v[184:187], v[64:79]
	ds_read_b128 v[184:187], v193 offset:14336
	v_rcp_f32_e32 v214, v214
	v_mfma_f32_32x32x16_f16 v[80:95], a[140:143], v[188:191], v[80:95]
	ds_read_b128 v[188:191], v193 offset:15360
	global_load_lds_dwordx4 v192, s[44:45] offset:2048 sc1
	v_rcp_f32_e32 v215, v215
	s_waitcnt lgkmcnt(4)
	v_mfma_f32_32x32x16_f16 v[64:79], a[144:147], v[160:163], v[64:79]
	ds_read_b128 v[160:163], v193 offset:16384
	v_exp_f32_e32 v200, v140
	v_mfma_f32_32x32x16_f16 v[80:95], a[144:147], v[164:167], v[80:95]
	ds_read_b128 v[164:167], v193 offset:17408
	v_exp_f32_e32 v201, v141
	v_add_f32_e32 v200, 1.0, v200
	v_mfma_f32_32x32x16_f16 v[64:79], a[148:151], v[168:171], v[64:79]
	ds_read_b128 v[168:171], v193 offset:18432
	v_exp_f32_e32 v202, v142
	v_add_f32_e32 v201, 1.0, v201
	v_mfma_f32_32x32x16_f16 v[80:95], a[148:151], v[172:175], v[80:95]
	ds_read_b128 v[172:175], v193 offset:19456
	global_load_lds_dwordx4 v192, s[44:45] offset:3072 sc1
	v_exp_f32_e32 v203, v143
	v_add_f32_e32 v202, 1.0, v202
	s_waitcnt lgkmcnt(4)
	v_mfma_f32_32x32x16_f16 v[64:79], a[152:155], v[176:179], v[64:79]
	ds_read_b128 v[176:179], v193 offset:20480
	v_add_f32_e32 v203, 1.0, v203
	v_rcp_f32_e32 v200, v200
	v_mfma_f32_32x32x16_f16 v[80:95], a[152:155], v[180:183], v[80:95]
	ds_read_b128 v[180:183], v193 offset:21504
	v_rcp_f32_e32 v201, v201
	v_fma_f32 v200, v200, 2.0, -1.0
	v_mfma_f32_32x32x16_f16 v[64:79], a[156:159], v[184:187], v[64:79]
	ds_read_b128 v[184:187], v193 offset:22528
	v_rcp_f32_e32 v202, v202
	v_fma_f32 v201, v201, 2.0, -1.0
	v_mul_f32_e32 v216, v212, v200
	v_mfma_f32_32x32x16_f16 v[80:95], a[156:159], v[188:191], v[80:95]
	ds_read_b128 v[188:191], v193 offset:23552
	s_add_u32 s44, s34, 0x1000
	s_addc_u32 s45, s35, 0
	s_mov_b32 m0, s53
	s_nop 0
	global_load_lds_dwordx4 v192, s[44:45] sc1
	v_rcp_f32_e32 v203, v203
	v_fma_f32 v202, v202, 2.0, -1.0
	v_mul_f32_e32 v217, v213, v201
	s_waitcnt lgkmcnt(4)
	v_mfma_f32_32x32x16_f16 v[64:79], a[160:163], v[160:163], v[64:79]
	ds_read_b128 v[160:163], v193 offset:24576
	v_fma_f32 v203, v203, 2.0, -1.0
	v_mul_f32_e32 v218, v214, v202
	v_mfma_f32_32x32x16_f16 v[80:95], a[160:163], v[164:167], v[80:95]
	ds_read_b128 v[164:167], v193 offset:25600
	v_mul_f32_e32 v219, v215, v203
	v_mul_f32_e32 v236, v216, v228
	v_mfma_f32_32x32x16_f16 v[64:79], a[164:167], v[168:171], v[64:79]
	ds_read_b128 v[168:171], v193 offset:26624
	v_mul_f32_e32 v237, v216, v232
	v_fmac_f32_e32 v236, v217, v229
	v_mfma_f32_32x32x16_f16 v[80:95], a[164:167], v[172:175], v[80:95]
	ds_read_b128 v[172:175], v193 offset:27648
	global_load_lds_dwordx4 v192, s[44:45] offset:1024 sc1
	v_fmac_f32_e32 v237, v217, v233
	v_fmac_f32_e32 v236, v218, v230
	s_waitcnt lgkmcnt(4)
	v_mfma_f32_32x32x16_f16 v[64:79], a[168:171], v[176:179], v[64:79]
	ds_read_b128 v[176:179], v193 offset:28672
	v_fmac_f32_e32 v237, v218, v234
	v_fmac_f32_e32 v236, v219, v231
	v_mfma_f32_32x32x16_f16 v[80:95], a[168:171], v[180:183], v[80:95]
	ds_read_b128 v[180:183], v193 offset:29696
	v_fmac_f32_e32 v237, v219, v235
	v_mov_b32_e32 v238, v236
	v_mfma_f32_32x32x16_f16 v[64:79], a[172:175], v[184:187], v[64:79]
	ds_read_b128 v[184:187], v193 offset:30720
	v_mov_b32_e32 v239, v236
	v_mov_b32_e32 v240, v237
	v_mfma_f32_32x32x16_f16 v[80:95], a[172:175], v[188:191], v[80:95]
	ds_read_b128 v[188:191], v193 offset:31744
	global_load_lds_dwordx4 v192, s[44:45] offset:2048 sc1
	v_mov_b32_e32 v241, v237
	v_cvt_pk_f16_f32 v222, v216, v217
	s_waitcnt vmcnt(15)
	s_barrier
	s_waitcnt lgkmcnt(4)
	v_mfma_f32_32x32x16_f16 v[64:79], a[176:179], v[160:163], v[64:79]
	ds_read_b128 v[160:163], v193 offset:32768
	s_nop 1
	v_permlane32_swap_b32_e32 v238, v239
	v_permlane32_swap_b32_e32 v240, v241
	v_add_f32_e32 v238, v238, v239
	v_add_f32_e32 v239, v240, v241
	ds_write_b64 v248, v[238:239] offset:768
	v_mfma_f32_32x32x16_f16 v[80:95], a[176:179], v[164:167], v[80:95]
	ds_read_b128 v[164:167], v193 offset:33792
	v_cvt_pk_f16_f32 v223, v218, v219
	v_mfma_f32_32x32x16_f16 v[64:79], a[180:183], v[168:171], v[64:79]
	ds_read_b128 v[168:171], v193 offset:34816
	s_nop 1
	v_permlane32_swap_b32_e32 v220, v222
	v_permlane32_swap_b32_e32 v221, v223
	s_cmp_eq_u32 s31, 0
	s_cbranch_scc1 .LD_slow34
	global_store_dwordx4 v195, v[220:223], s[36:37] offset:0
	s_branch .LD_join35

.LD_join37:
	ds_read_b64 v[200:201], v249 offset:512
	ds_read_b64 v[202:203], v249 offset:2560
	ds_read_b64 v[204:205], v249 offset:4608
	ds_read_b64 v[206:207], v249 offset:6656
	s_waitcnt lgkmcnt(8)
	v_mfma_f32_32x32x16_f16 v[64:79], a[208:211], v[160:163], v[64:79]
	ds_read_b128 v[160:163], v193 offset:49152
	v_mfma_f32_32x32x16_f16 v[80:95], a[208:211], v[164:167], v[80:95]
	ds_read_b128 v[164:167], v193 offset:50176
	v_mfma_f32_32x32x16_f16 v[64:79], a[212:215], v[168:171], v[64:79]
	ds_read_b128 v[168:171], v193 offset:51200
	v_mfma_f32_32x32x16_f16 v[80:95], a[212:215], v[172:175], v[80:95]
	ds_read_b128 v[172:175], v193 offset:52224
	global_load_lds_dwordx4 v192, s[44:45] offset:3072 sc1
	s_waitcnt lgkmcnt(8)
	v_mfma_f32_32x32x16_f16 v[64:79], a[216:219], v[176:179], v[64:79]
	ds_read_b128 v[176:179], v193 offset:53248
	v_mfma_f32_32x32x16_f16 v[80:95], a[216:219], v[180:183], v[80:95]
	ds_read_b128 v[180:183], v193 offset:54272
	v_mfma_f32_32x32x16_f16 v[64:79], a[220:223], v[184:187], v[64:79]
	ds_read_b128 v[184:187], v193 offset:55296
	v_mfma_f32_32x32x16_f16 v[80:95], a[220:223], v[188:191], v[80:95]
	ds_read_b128 v[188:191], v193 offset:56320
	s_add_u32 s44, s34, 0x9000
	s_addc_u32 s45, s35, 0
	s_mov_b32 m0, s55
	s_nop 0
	global_load_lds_dwordx4 v192, s[44:45] sc1
	s_waitcnt lgkmcnt(4)
	v_mfma_f32_32x32x16_f16 v[64:79], a[224:227], v[160:163], v[64:79]
	ds_read_b128 v[160:163], v193 offset:57344
	v_mfma_f32_32x32x16_f16 v[80:95], a[224:227], v[164:167], v[80:95]
	ds_read_b128 v[164:167], v193 offset:58368
	v_mfma_f32_32x32x16_f16 v[64:79], a[228:231], v[168:171], v[64:79]
	ds_read_b128 v[168:171], v193 offset:59392
	v_mfma_f32_32x32x16_f16 v[80:95], a[228:231], v[172:175], v[80:95]
	ds_read_b128 v[172:175], v193 offset:60416
	global_load_lds_dwordx4 v192, s[44:45] offset:1024 sc1
	v_add_f32_e32 v200, v200, v202
	v_add_f32_e32 v201, v201, v203
	v_add_f32_e32 v200, v200, v204
	v_add_f32_e32 v201, v201, v205
	v_add_f32_e32 v200, v200, v206
	v_add_f32_e32 v201, v201, v207
	global_store_dwordx2 v250, v[200:201], s[72:73]
	s_waitcnt lgkmcnt(4)
	v_mfma_f32_32x32x16_f16 v[64:79], a[232:235], v[176:179], v[64:79]
	ds_read_b128 v[176:179], v193 offset:61440
	v_mfma_f32_32x32x16_f16 v[80:95], a[232:235], v[180:183], v[80:95]
	ds_read_b128 v[180:183], v193 offset:62464
	v_mfma_f32_32x32x16_f16 v[64:79], a[236:239], v[184:187], v[64:79]
	ds_read_b128 v[184:187], v193 offset:63488
	v_mfma_f32_32x32x16_f16 v[80:95], a[236:239], v[188:191], v[80:95]
	ds_read_b128 v[188:191], v193 offset:64512
	global_load_lds_dwordx4 v192, s[44:45] offset:2048 sc1
	s_waitcnt vmcnt(9)
	s_barrier
	s_waitcnt lgkmcnt(4)
	v_mfma_f32_32x32x16_f16 v[64:79], a[240:243], v[160:163], v[64:79]
	ds_read_b128 v[160:163], v192 offset:0
	v_mfma_f32_32x32x16_f16 v[80:95], a[240:243], v[164:167], v[80:95]
	ds_read_b128 v[164:167], v192 offset:1024
	v_mfma_f32_32x32x16_f16 v[64:79], a[244:247], v[168:171], v[64:79]
	ds_read_b128 v[168:171], v192 offset:2048
	v_mfma_f32_32x32x16_f16 v[80:95], a[244:247], v[172:175], v[80:95]
	ds_read_b128 v[172:175], v192 offset:3072
	global_load_lds_dwordx4 v192, s[44:45] offset:3072 sc1
	s_waitcnt lgkmcnt(4)
	v_mfma_f32_32x32x16_f16 v[64:79], a[248:251], v[176:179], v[64:79]
	ds_read_b128 v[176:179], v192 offset:4096
	v_mfma_f32_32x32x16_f16 v[80:95], a[248:251], v[180:183], v[80:95]
	ds_read_b128 v[180:183], v192 offset:5120
	v_mfma_f32_32x32x16_f16 v[64:79], a[252:255], v[184:187], v[64:79]
	ds_read_b128 v[184:187], v192 offset:6144
	v_mfma_f32_32x32x16_f16 v[80:95], a[252:255], v[188:191], v[80:95]
	ds_read_b128 v[188:191], v192 offset:7168
	s_add_u32 s44, s34, 0x10000
	s_addc_u32 s45, s35, 0
	s_mov_b32 m0, s56
	s_nop 0
	global_load_lds_dwordx4 v192, s[44:45] sc1
	s_and_b32 s64, s33, 1
	s_lshl_b32 s64, s64, 22
	s_add_u32 s64, s64, s50
	s_add_u32 s64, s64, 0x40000
	s_add_u32 s36, s6, s64
	s_addc_u32 s37, s7, 0
	s_lshl_b32 s64, s33, 3
	s_add_u32 s64, s64, s29
	s_lshl_b32 s64, s64, 5
	s_add_u32 s64, s64, s30
	s_lshl_b32 s64, s64, 2
	s_add_u32 s40, s8, s64
	s_addc_u32 s41, s9, 0
	s_lshl_b32 s64, s33, 19
	s_add_u32 s64, s64, 0x400
	s_add_u32 s72, s62, s64
	s_addc_u32 s73, s63, 0
	s_nop 3
	s_waitcnt lgkmcnt(4)
	v_mfma_f32_32x32x16_f16 v[96:111], a[0:3], v[160:163], v[96:111]
	ds_read_b128 v[160:163], v192 offset:8192
	v_exp_f32_e32 v200, v64
	v_mfma_f32_32x32x16_f16 v[112:127], a[0:3], v[164:167], v[112:127]
	ds_read_b128 v[164:167], v192 offset:9216
	v_exp_f32_e32 v201, v65
	v_add_f32_e32 v200, 1.0, v200
	v_mfma_f32_32x32x16_f16 v[96:111], a[4:7], v[168:171], v[96:111]
	ds_read_b128 v[168:171], v192 offset:10240
	v_exp_f32_e32 v202, v66
	v_add_f32_e32 v201, 1.0, v201
	v_mfma_f32_32x32x16_f16 v[112:127], a[4:7], v[172:175], v[112:127]
	ds_read_b128 v[172:175], v192 offset:11264
	global_load_lds_dwordx4 v192, s[44:45] offset:1024 sc1
	v_exp_f32_e32 v203, v67
	v_add_f32_e32 v202, 1.0, v202
	s_waitcnt lgkmcnt(4)
	v_mfma_f32_32x32x16_f16 v[96:111], a[8:11], v[176:179], v[96:111]
	ds_read_b128 v[176:179], v192 offset:12288
	v_exp_f32_e32 v204, v68
	v_add_f32_e32 v203, 1.0, v203
	v_mfma_f32_32x32x16_f16 v[112:127], a[8:11], v[180:183], v[112:127]
	ds_read_b128 v[180:183], v192 offset:13312
	v_exp_f32_e32 v205, v69
	v_add_f32_e32 v204, 1.0, v204
	v_mfma_f32_32x32x16_f16 v[96:111], a[12:15], v[184:187], v[96:111]
	ds_read_b128 v[184:187], v192 offset:14336
	v_exp_f32_e32 v206, v70
	v_add_f32_e32 v205, 1.0, v205
	v_mfma_f32_32x32x16_f16 v[112:127], a[12:15], v[188:191], v[112:127]
	ds_read_b128 v[188:191], v192 offset:15360
	global_load_lds_dwordx4 v192, s[44:45] offset:2048 sc1
	v_exp_f32_e32 v207, v71
	v_add_f32_e32 v206, 1.0, v206
	s_waitcnt lgkmcnt(4)
	v_mfma_f32_32x32x16_f16 v[96:111], a[16:19], v[160:163], v[96:111]
	ds_read_b128 v[160:163], v192 offset:16384
	v_exp_f32_e32 v208, v72
	v_add_f32_e32 v207, 1.0, v207
	v_mfma_f32_32x32x16_f16 v[112:127], a[16:19], v[164:167], v[112:127]
	ds_read_b128 v[164:167], v192 offset:17408
	v_exp_f32_e32 v209, v73
	v_add_f32_e32 v208, 1.0, v208
	v_mfma_f32_32x32x16_f16 v[96:111], a[20:23], v[168:171], v[96:111]
	ds_read_b128 v[168:171], v192 offset:18432
	v_exp_f32_e32 v210, v74
	v_add_f32_e32 v209, 1.0, v209
	v_mfma_f32_32x32x16_f16 v[112:127], a[20:23], v[172:175], v[112:127]
	ds_read_b128 v[172:175], v192 offset:19456
	global_load_lds_dwordx4 v192, s[44:45] offset:3072 sc1
	v_exp_f32_e32 v211, v75
	v_add_f32_e32 v210, 1.0, v210
	s_waitcnt lgkmcnt(4)
	v_mfma_f32_32x32x16_f16 v[96:111], a[24:27], v[176:179], v[96:111]
	ds_read_b128 v[176:179], v192 offset:20480
	v_exp_f32_e32 v212, v76
	v_add_f32_e32 v211, 1.0, v211
	v_mfma_f32_32x32x16_f16 v[112:127], a[24:27], v[180:183], v[112:127]
	ds_read_b128 v[180:183], v192 offset:21504
	v_exp_f32_e32 v213, v77
	v_add_f32_e32 v212, 1.0, v212
	v_mfma_f32_32x32x16_f16 v[96:111], a[28:31], v[184:187], v[96:111]
	ds_read_b128 v[184:187], v192 offset:22528
	v_exp_f32_e32 v214, v78
	v_add_f32_e32 v213, 1.0, v213
	v_mfma_f32_32x32x16_f16 v[112:127], a[28:31], v[188:191], v[112:127]
	ds_read_b128 v[188:191], v192 offset:23552
	s_add_u32 s44, s34, 0x11000
	s_addc_u32 s45, s35, 0
	s_mov_b32 m0, s57
	s_nop 0
	global_load_lds_dwordx4 v192, s[44:45] sc1
	v_exp_f32_e32 v215, v79
	v_add_f32_e32 v214, 1.0, v214
	s_waitcnt lgkmcnt(4)
	v_mfma_f32_32x32x16_f16 v[96:111], a[32:35], v[160:163], v[96:111]
	ds_read_b128 v[160:163], v192 offset:24576
	v_add_f32_e32 v215, 1.0, v215
	v_rcp_f32_e32 v200, v200
	v_mfma_f32_32x32x16_f16 v[112:127], a[32:35], v[164:167], v[112:127]
	ds_read_b128 v[164:167], v192 offset:25600
	v_rcp_f32_e32 v201, v201
	v_mfma_f32_32x32x16_f16 v[96:111], a[36:39], v[168:171], v[96:111]
	ds_read_b128 v[168:171], v192 offset:26624
	v_rcp_f32_e32 v202, v202
	v_mfma_f32_32x32x16_f16 v[112:127], a[36:39], v[172:175], v[112:127]
	ds_read_b128 v[172:175], v192 offset:27648
	global_load_lds_dwordx4 v192, s[44:45] offset:1024 sc1
	v_rcp_f32_e32 v203, v203
	s_waitcnt lgkmcnt(4)
	v_mfma_f32_32x32x16_f16 v[96:111], a[40:43], v[176:179], v[96:111]
	ds_read_b128 v[176:179], v192 offset:28672
	v_rcp_f32_e32 v204, v204
	v_mfma_f32_32x32x16_f16 v[112:127], a[40:43], v[180:183], v[112:127]
	ds_read_b128 v[180:183], v192 offset:29696
	v_rcp_f32_e32 v205, v205
	v_mul_f32_e32 v204, v204, v144
	v_mfma_f32_32x32x16_f16 v[96:111], a[44:47], v[184:187], v[96:111]
	ds_read_b128 v[184:187], v192 offset:30720
	v_rcp_f32_e32 v206, v206
	v_mul_f32_e32 v205, v205, v145
	v_mfma_f32_32x32x16_f16 v[112:127], a[44:47], v[188:191], v[112:127]
	ds_read_b128 v[188:191], v192 offset:31744
	global_load_lds_dwordx4 v192, s[44:45] offset:2048 sc1
	v_rcp_f32_e32 v207, v207
	v_mul_f32_e32 v206, v206, v146
	s_waitcnt vmcnt(7)
	s_barrier
	s_waitcnt lgkmcnt(4)
	v_mfma_f32_32x32x16_f16 v[96:111], a[48:51], v[160:163], v[96:111]
	ds_read_b128 v[160:163], v192 offset:32768
	v_rcp_f32_e32 v208, v208
	v_mul_f32_e32 v207, v207, v147
	v_mfma_f32_32x32x16_f16 v[112:127], a[48:51], v[164:167], v[112:127]
	ds_read_b128 v[164:167], v192 offset:33792
	v_rcp_f32_e32 v209, v209
	v_fmamk_f32 v208, v208, 0xc0b8aa3b, v198
	v_mfma_f32_32x32x16_f16 v[96:111], a[52:55], v[168:171], v[96:111]
	ds_read_b128 v[168:171], v192 offset:34816
	v_rcp_f32_e32 v210, v210
	v_fmamk_f32 v209, v209, 0xc0b8aa3b, v198
	v_fma_f32 v144, v200, v208, v204
	v_mfma_f32_32x32x16_f16 v[112:127], a[52:55], v[172:175], v[112:127]
	ds_read_b128 v[172:175], v192 offset:35840
	global_load_lds_dwordx4 v192, s[44:45] offset:3072 sc1
	v_rcp_f32_e32 v211, v211
	v_fmamk_f32 v210, v210, 0xc0b8aa3b, v198
	v_fma_f32 v145, v201, v209, v205
	s_waitcnt lgkmcnt(4)
	v_mfma_f32_32x32x16_f16 v[96:111], a[56:59], v[176:179], v[96:111]
	ds_read_b128 v[176:179], v192 offset:36864
	v_rcp_f32_e32 v212, v212
	v_fmamk_f32 v211, v211, 0xc0b8aa3b, v198
	v_fma_f32 v146, v202, v210, v206
	v_mfma_f32_32x32x16_f16 v[112:127], a[56:59], v[180:183], v[112:127]
	ds_read_b128 v[180:183], v192 offset:37888
	v_rcp_f32_e32 v213, v213
	v_fma_f32 v147, v203, v211, v207
	v_mfma_f32_32x32x16_f16 v[96:111], a[60:63], v[184:187], v[96:111]
	ds_read_b128 v[184:187], v192 offset:38912
	v_rcp_f32_e32 v214, v214
	v_mfma_f32_32x32x16_f16 v[112:127], a[60:63], v[188:191], v[112:127]
	ds_read_b128 v[188:191], v192 offset:39936
	s_add_u32 s44, s34, 0x18000
	s_addc_u32 s45, s35, 0
	s_mov_b32 m0, s58
	s_nop 0
	global_load_lds_dwordx4 v192, s[44:45] sc1
	v_rcp_f32_e32 v215, v215
	s_waitcnt lgkmcnt(4)
	v_mfma_f32_32x32x16_f16 v[96:111], a[64:67], v[160:163], v[96:111]
	ds_read_b128 v[160:163], v192 offset:40960
	v_exp_f32_e32 v200, v144
	v_mfma_f32_32x32x16_f16 v[112:127], a[64:67], v[164:167], v[112:127]
	ds_read_b128 v[164:167], v192 offset:41984
	v_exp_f32_e32 v201, v145
	v_add_f32_e32 v200, 1.0, v200
	v_mfma_f32_32x32x16_f16 v[96:111], a[68:71], v[168:171], v[96:111]
	ds_read_b128 v[168:171], v192 offset:43008
	v_exp_f32_e32 v202, v146
	v_add_f32_e32 v201, 1.0, v201
	v_mfma_f32_32x32x16_f16 v[112:127], a[68:71], v[172:175], v[112:127]
	ds_read_b128 v[172:175], v192 offset:44032
	global_load_lds_dwordx4 v192, s[44:45] offset:1024 sc1
	v_exp_f32_e32 v203, v147
	v_add_f32_e32 v202, 1.0, v202
	s_waitcnt lgkmcnt(4)
	v_mfma_f32_32x32x16_f16 v[96:111], a[72:75], v[176:179], v[96:111]
	ds_read_b128 v[176:179], v192 offset:45056
	v_add_f32_e32 v203, 1.0, v203
	v_rcp_f32_e32 v200, v200
	v_mfma_f32_32x32x16_f16 v[112:127], a[72:75], v[180:183], v[112:127]
	ds_read_b128 v[180:183], v192 offset:46080
	v_rcp_f32_e32 v201, v201
	v_fma_f32 v200, v200, 2.0, -1.0
	v_mfma_f32_32x32x16_f16 v[96:111], a[76:79], v[184:187], v[96:111]
	ds_read_b128 v[184:187], v192 offset:47104
	v_rcp_f32_e32 v202, v202
	v_fma_f32 v201, v201, 2.0, -1.0
	v_mul_f32_e32 v216, v212, v200
	v_mfma_f32_32x32x16_f16 v[112:127], a[76:79], v[188:191], v[112:127]
	ds_read_b128 v[188:191], v192 offset:48128
	global_load_lds_dwordx4 v192, s[44:45] offset:2048 sc1
	v_rcp_f32_e32 v203, v203
	v_fma_f32 v202, v202, 2.0, -1.0
	v_mul_f32_e32 v217, v213, v201
	s_waitcnt lgkmcnt(4)
	v_mfma_f32_32x32x16_f16 v[96:111], a[80:83], v[160:163], v[96:111]
	ds_read_b128 v[160:163], v192 offset:49152
	v_fma_f32 v203, v203, 2.0, -1.0
	v_mul_f32_e32 v218, v214, v202
	v_exp_f32_e32 v200, v80
	v_mfma_f32_32x32x16_f16 v[112:127], a[80:83], v[164:167], v[112:127]
	ds_read_b128 v[164:167], v192 offset:50176
	v_mul_f32_e32 v219, v215, v203
	v_mul_f32_e32 v236, v216, v228
	v_exp_f32_e32 v201, v81
	v_mfma_f32_32x32x16_f16 v[96:111], a[84:87], v[168:171], v[96:111]
	ds_read_b128 v[168:171], v192 offset:51200
	v_mul_f32_e32 v237, v216, v232
	v_fmac_f32_e32 v236, v217, v229
	v_exp_f32_e32 v202, v82
	v_mfma_f32_32x32x16_f16 v[112:127], a[84:87], v[172:175], v[112:127]
	ds_read_b128 v[172:175], v192 offset:52224
	global_load_lds_dwordx4 v192, s[44:45] offset:3072 sc1
	v_fmac_f32_e32 v237, v217, v233
	v_fmac_f32_e32 v236, v218, v230
	v_exp_f32_e32 v203, v83
	s_waitcnt lgkmcnt(4)
	v_mfma_f32_32x32x16_f16 v[96:111], a[88:91], v[176:179], v[96:111]
	ds_read_b128 v[176:179], v192 offset:53248
	v_fmac_f32_e32 v237, v218, v234
	v_fmac_f32_e32 v236, v219, v231
	v_exp_f32_e32 v204, v84
	v_mfma_f32_32x32x16_f16 v[112:127], a[88:91], v[180:183], v[112:127]
	ds_read_b128 v[180:183], v192 offset:54272
	v_fmac_f32_e32 v237, v219, v235
	v_mov_b32_e32 v238, v236
	v_exp_f32_e32 v205, v85
	v_mfma_f32_32x32x16_f16 v[96:111], a[92:95], v[184:187], v[96:111]
	ds_read_b128 v[184:187], v192 offset:55296
	v_mov_b32_e32 v239, v236
	v_mov_b32_e32 v240, v237
	v_exp_f32_e32 v206, v86
	v_mfma_f32_32x32x16_f16 v[112:127], a[92:95], v[188:191], v[112:127]
	ds_read_b128 v[188:191], v192 offset:56320
	s_add_u32 s44, s34, 0x19000
	s_addc_u32 s45, s35, 0
	s_mov_b32 m0, s59
	s_nop 0
	global_load_lds_dwordx4 v192, s[44:45] sc1
	s_lshl_b32 s64, s33, 3
	s_add_u32 s64, s64, s29
	s_lshl_b32 s64, s64, 7
	s_add_u32 s38, s8, s64
	s_addc_u32 s39, s9, 0
	global_load_dword v251, v196, s[38:39] sc1
	v_mov_b32_e32 v241, v237
	v_cvt_pk_f16_f32 v220, v216, v217
	v_exp_f32_e32 v207, v87
	s_waitcnt lgkmcnt(4)
	v_mfma_f32_32x32x16_f16 v[96:111], a[96:99], v[160:163], v[96:111]
	ds_read_b128 v[160:163], v192 offset:57344
	s_nop 1
	v_permlane32_swap_b32_e32 v238, v239
	v_permlane32_swap_b32_e32 v240, v241
	v_add_f32_e32 v238, v238, v239
	v_add_f32_e32 v239, v240, v241
	ds_write_b64 v248, v[238:239] offset:1024
	v_exp_f32_e32 v208, v88
	v_mfma_f32_32x32x16_f16 v[112:127], a[96:99], v[164:167], v[112:127]
	ds_read_b128 v[164:167], v192 offset:58368
	v_cvt_pk_f16_f32 v221, v218, v219
	v_exp_f32_e32 v209, v89
	v_add_f32_e32 v200, 1.0, v200
	v_mfma_f32_32x32x16_f16 v[96:111], a[100:103], v[168:171], v[96:111]
	ds_read_b128 v[168:171], v192 offset:59392
	v_exp_f32_e32 v210, v90
	v_add_f32_e32 v201, 1.0, v201
	v_add_f32_e32 v202, 1.0, v202
	v_mfma_f32_32x32x16_f16 v[112:127], a[100:103], v[172:175], v[112:127]
	ds_read_b128 v[172:175], v192 offset:60416
	global_load_lds_dwordx4 v192, s[44:45] offset:1024 sc1
	v_exp_f32_e32 v211, v91
	v_add_f32_e32 v203, 1.0, v203
	v_add_f32_e32 v204, 1.0, v204
	s_waitcnt lgkmcnt(5)
	v_mfma_f32_32x32x16_f16 v[96:111], a[104:107], v[176:179], v[96:111]
	ds_read_b128 v[176:179], v192 offset:61440
	v_exp_f32_e32 v212, v92
	v_add_f32_e32 v205, 1.0, v205
	v_add_f32_e32 v206, 1.0, v206
	v_mfma_f32_32x32x16_f16 v[112:127], a[104:107], v[180:183], v[112:127]
	ds_read_b128 v[180:183], v192 offset:62464
	v_exp_f32_e32 v213, v93
	v_add_f32_e32 v207, 1.0, v207
	v_add_f32_e32 v208, 1.0, v208
	v_mfma_f32_32x32x16_f16 v[96:111], a[108:111], v[184:187], v[96:111]
	ds_read_b128 v[184:187], v192 offset:63488
	v_exp_f32_e32 v214, v94
	v_add_f32_e32 v209, 1.0, v209
	v_add_f32_e32 v210, 1.0, v210
	v_mfma_f32_32x32x16_f16 v[112:127], a[108:111], v[188:191], v[112:127]
	ds_read_b128 v[188:191], v192 offset:64512
	global_load_lds_dwordx4 v192, s[44:45] offset:2048 sc1
	v_exp_f32_e32 v215, v95
	v_add_f32_e32 v211, 1.0, v211
	v_add_f32_e32 v212, 1.0, v212
	s_waitcnt vmcnt(8)
	s_barrier
	s_waitcnt lgkmcnt(4)
	v_mfma_f32_32x32x16_f16 v[96:111], a[112:115], v[160:163], v[96:111]
	ds_read_b128 v[160:163], v193 offset:0
	v_add_f32_e32 v213, 1.0, v213
	v_add_f32_e32 v214, 1.0, v214
	v_rcp_f32_e32 v200, v200
	v_mfma_f32_32x32x16_f16 v[112:127], a[112:115], v[164:167], v[112:127]
	ds_read_b128 v[164:167], v193 offset:1024
	v_add_f32_e32 v215, 1.0, v215
	v_rcp_f32_e32 v201, v201
	v_mfma_f32_32x32x16_f16 v[96:111], a[116:119], v[168:171], v[96:111]
	ds_read_b128 v[168:171], v193 offset:2048
	v_rcp_f32_e32 v202, v202
	v_mfma_f32_32x32x16_f16 v[112:127], a[116:119], v[172:175], v[112:127]
	ds_read_b128 v[172:175], v193 offset:3072
	global_load_lds_dwordx4 v192, s[44:45] offset:3072 sc1
	v_rcp_f32_e32 v203, v203
	s_waitcnt lgkmcnt(4)
	v_mfma_f32_32x32x16_f16 v[96:111], a[120:123], v[176:179], v[96:111]
	ds_read_b128 v[176:179], v193 offset:4096
	v_rcp_f32_e32 v204, v204
	s_add_u32 s46, s42, 0x2000
	s_addc_u32 s47, s43, 0
	global_load_dwordx4 v[32:35], v192, s[46:47] offset:0
	v_mfma_f32_32x32x16_f16 v[112:127], a[120:123], v[180:183], v[112:127]
	ds_read_b128 v[180:183], v193 offset:5120
	v_rcp_f32_e32 v205, v205
	v_mul_f32_e32 v204, v204, v148
	global_load_dwordx4 v[36:39], v192, s[46:47] offset:1024
	global_load_dwordx4 v[40:43], v192, s[46:47] offset:2048
	v_mfma_f32_32x32x16_f16 v[96:111], a[124:127], v[184:187], v[96:111]
	ds_read_b128 v[184:187], v193 offset:6144
	v_rcp_f32_e32 v206, v206
	v_mul_f32_e32 v205, v205, v149
	global_load_dwordx4 v[44:47], v192, s[46:47] offset:3072
	s_add_u32 s46, s42, 0x3000
	s_addc_u32 s47, s43, 0
	v_mfma_f32_32x32x16_f16 v[112:127], a[124:127], v[188:191], v[112:127]
	ds_read_b128 v[188:191], v193 offset:7168
	s_waitcnt vmcnt(7)
	v_cmp_gt_u32_e32 vcc, 1, v251
	s_cbranch_vccz .LD_tok38

.LD_tok38:
	s_and_b32 s64, s33, 1
	s_lshl_b32 s64, s64, 22
	s_add_u32 s64, s64, s49
	s_add_u32 s34, s6, s64
	s_addc_u32 s35, s7, 0
	s_add_u32 s44, s34, 0x0
	s_addc_u32 s45, s35, 0
	s_mov_b32 m0, s52
	s_nop 0
	global_load_lds_dwordx4 v192, s[44:45] sc1
	v_rcp_f32_e32 v207, v207
	v_mul_f32_e32 v206, v206, v150
	global_load_dwordx4 v[48:51], v192, s[46:47] offset:0
	global_load_dwordx4 v[52:55], v192, s[46:47] offset:1024
	s_waitcnt lgkmcnt(4)
	v_mfma_f32_32x32x16_f16 v[96:111], a[128:131], v[160:163], v[96:111]
	ds_read_b128 v[160:163], v193 offset:8192
	v_rcp_f32_e32 v208, v208
	v_mul_f32_e32 v207, v207, v151
	global_load_dwordx4 v[56:59], v192, s[46:47] offset:2048
	global_load_dwordx4 v[60:63], v192, s[46:47] offset:3072
	v_mfma_f32_32x32x16_f16 v[112:127], a[128:131], v[164:167], v[112:127]
	ds_read_b128 v[164:167], v193 offset:9216
	v_rcp_f32_e32 v209, v209
	v_fmamk_f32 v208, v208, 0xc0b8aa3b, v198
	v_mfma_f32_32x32x16_f16 v[96:111], a[132:135], v[168:171], v[96:111]
	ds_read_b128 v[168:171], v193 offset:10240
	v_rcp_f32_e32 v210, v210
	v_fmamk_f32 v209, v209, 0xc0b8aa3b, v198
	v_fma_f32 v148, v200, v208, v204
	v_mfma_f32_32x32x16_f16 v[112:127], a[132:135], v[172:175], v[112:127]
	ds_read_b128 v[172:175], v193 offset:11264
	global_load_lds_dwordx4 v192, s[44:45] offset:1024 sc1
	v_rcp_f32_e32 v211, v211
	v_fmamk_f32 v210, v210, 0xc0b8aa3b, v198
	v_fma_f32 v149, v201, v209, v205
	s_waitcnt lgkmcnt(4)
	v_mfma_f32_32x32x16_f16 v[96:111], a[136:139], v[176:179], v[96:111]
	ds_read_b128 v[176:179], v193 offset:12288
	v_rcp_f32_e32 v212, v212
	v_fmamk_f32 v211, v211, 0xc0b8aa3b, v198
	v_fma_f32 v150, v202, v210, v206
	v_mfma_f32_32x32x16_f16 v[112:127], a[136:139], v[180:183], v[112:127]
	ds_read_b128 v[180:183], v193 offset:13312
	v_rcp_f32_e32 v213, v213
	v_fma_f32 v151, v203, v211, v207
	v_mfma_f32_32x32x16_f16 v[96:111], a[140:143], v[184:187], v[96:111]
	ds_read_b128 v[184:187], v193 offset:14336
	v_rcp_f32_e32 v214, v214
	v_mfma_f32_32x32x16_f16 v[112:127], a[140:143], v[188:191], v[112:127]
	ds_read_b128 v[188:191], v193 offset:15360
	global_load_lds_dwordx4 v192, s[44:45] offset:2048 sc1
	v_rcp_f32_e32 v215, v215
	s_waitcnt lgkmcnt(4)
	v_mfma_f32_32x32x16_f16 v[96:111], a[144:147], v[160:163], v[96:111]
	ds_read_b128 v[160:163], v193 offset:16384
	v_exp_f32_e32 v200, v148
	v_mfma_f32_32x32x16_f16 v[112:127], a[144:147], v[164:167], v[112:127]
	ds_read_b128 v[164:167], v193 offset:17408
	v_exp_f32_e32 v201, v149
	v_add_f32_e32 v200, 1.0, v200
	v_mfma_f32_32x32x16_f16 v[96:111], a[148:151], v[168:171], v[96:111]
	ds_read_b128 v[168:171], v193 offset:18432
	v_exp_f32_e32 v202, v150
	v_add_f32_e32 v201, 1.0, v201
	v_mfma_f32_32x32x16_f16 v[112:127], a[148:151], v[172:175], v[112:127]
	ds_read_b128 v[172:175], v193 offset:19456
	global_load_lds_dwordx4 v192, s[44:45] offset:3072 sc1
	v_exp_f32_e32 v203, v151
	v_add_f32_e32 v202, 1.0, v202
	s_waitcnt lgkmcnt(4)
	v_mfma_f32_32x32x16_f16 v[96:111], a[152:155], v[176:179], v[96:111]
	ds_read_b128 v[176:179], v193 offset:20480
	v_add_f32_e32 v203, 1.0, v203
	v_rcp_f32_e32 v200, v200
	v_mfma_f32_32x32x16_f16 v[112:127], a[152:155], v[180:183], v[112:127]
	ds_read_b128 v[180:183], v193 offset:21504
	v_rcp_f32_e32 v201, v201
	v_fma_f32 v200, v200, 2.0, -1.0
	v_mfma_f32_32x32x16_f16 v[96:111], a[156:159], v[184:187], v[96:111]
	ds_read_b128 v[184:187], v193 offset:22528
	v_rcp_f32_e32 v202, v202
	v_fma_f32 v201, v201, 2.0, -1.0
	v_mul_f32_e32 v216, v212, v200
	v_mfma_f32_32x32x16_f16 v[112:127], a[156:159], v[188:191], v[112:127]
	ds_read_b128 v[188:191], v193 offset:23552
	s_add_u32 s44, s34, 0x1000
	s_addc_u32 s45, s35, 0
	s_mov_b32 m0, s53
	s_nop 0
	global_load_lds_dwordx4 v192, s[44:45] sc1
	v_rcp_f32_e32 v203, v203
	v_fma_f32 v202, v202, 2.0, -1.0
	v_mul_f32_e32 v217, v213, v201
	s_waitcnt lgkmcnt(4)
	v_mfma_f32_32x32x16_f16 v[96:111], a[160:163], v[160:163], v[96:111]
	ds_read_b128 v[160:163], v193 offset:24576
	v_fma_f32 v203, v203, 2.0, -1.0
	v_mul_f32_e32 v218, v214, v202
	v_mfma_f32_32x32x16_f16 v[112:127], a[160:163], v[164:167], v[112:127]
	ds_read_b128 v[164:167], v193 offset:25600
	v_mul_f32_e32 v219, v215, v203
	v_mul_f32_e32 v236, v216, v228
	v_mfma_f32_32x32x16_f16 v[96:111], a[164:167], v[168:171], v[96:111]
	ds_read_b128 v[168:171], v193 offset:26624
	v_mul_f32_e32 v237, v216, v232
	v_fmac_f32_e32 v236, v217, v229
	v_mfma_f32_32x32x16_f16 v[112:127], a[164:167], v[172:175], v[112:127]
	ds_read_b128 v[172:175], v193 offset:27648
	global_load_lds_dwordx4 v192, s[44:45] offset:1024 sc1
	v_fmac_f32_e32 v237, v217, v233
	v_fmac_f32_e32 v236, v218, v230
	s_waitcnt lgkmcnt(4)
	v_mfma_f32_32x32x16_f16 v[96:111], a[168:171], v[176:179], v[96:111]
	ds_read_b128 v[176:179], v193 offset:28672
	v_fmac_f32_e32 v237, v218, v234
	v_fmac_f32_e32 v236, v219, v231
	v_mfma_f32_32x32x16_f16 v[112:127], a[168:171], v[180:183], v[112:127]
	ds_read_b128 v[180:183], v193 offset:29696
	v_fmac_f32_e32 v237, v219, v235
	v_mov_b32_e32 v238, v236
	v_mfma_f32_32x32x16_f16 v[96:111], a[172:175], v[184:187], v[96:111]
	ds_read_b128 v[184:187], v193 offset:30720
	v_mov_b32_e32 v239, v236
	v_mov_b32_e32 v240, v237
	v_mfma_f32_32x32x16_f16 v[112:127], a[172:175], v[188:191], v[112:127]
	ds_read_b128 v[188:191], v193 offset:31744
	global_load_lds_dwordx4 v192, s[44:45] offset:2048 sc1
	v_mov_b32_e32 v241, v237
	v_cvt_pk_f16_f32 v222, v216, v217
	s_waitcnt vmcnt(15)
	s_barrier
	s_waitcnt lgkmcnt(4)
	v_mfma_f32_32x32x16_f16 v[96:111], a[176:179], v[160:163], v[96:111]
	ds_read_b128 v[160:163], v193 offset:32768
	s_nop 1
	v_permlane32_swap_b32_e32 v238, v239
	v_permlane32_swap_b32_e32 v240, v241
	v_add_f32_e32 v238, v238, v239
	v_add_f32_e32 v239, v240, v241
	ds_write_b64 v248, v[238:239] offset:1280
	v_mfma_f32_32x32x16_f16 v[112:127], a[176:179], v[164:167], v[112:127]
	ds_read_b128 v[164:167], v193 offset:33792
	v_cvt_pk_f16_f32 v223, v218, v219
	v_mfma_f32_32x32x16_f16 v[96:111], a[180:183], v[168:171], v[96:111]
	ds_read_b128 v[168:171], v193 offset:34816
	s_nop 1
	v_permlane32_swap_b32_e32 v220, v222
	v_permlane32_swap_b32_e32 v221, v223
	s_cmp_eq_u32 s31, 0
	s_cbranch_scc1 .LD_slow40
	global_store_dwordx4 v195, v[220:223], s[36:37] offset:0
	s_branch .LD_join41
